# static priority raise (7.4): trailing half (waves 4-7) set to priority 1 once per GEMM phase, all per-segment s_setprio flips deleted, reset to 0 at every seam; loops pinned at v43 offsets
# speedup vs baseline: 1.0326x; 1.0088x over previous
;     __device__ __forceinline__ void a_ready(const Unit&) const { if (++ncall == 3 && sig != nullptr && threadIdx.x == 0) __hip_atomic_fetch_add(sig, 1u, __ATOMIC_RELAXED, __HIP_MEMORY_SCOPE_AGENT); }
; __device__ __forceinline__ f32x4 load_row_partials(const float* rsp, int pm, int tid) { f32x4 p = {0.f, 0.f, 0.f, 0.f}; if (tid < BM) p = *(const f32x4*)(rsp + (size_t)(pm * BM + tid) * 4); return p; }
; #define PG8_BAR __builtin_amdgcn_s_barrier()
; template <class Epi, class Sched, bool ALIGN_EPI = false, bool SP2 = false>
; __device__ __forceinline__ void gemm_phase(PG8_LAS unsigned char* lds, const Gemm g, const Sched& S, const Epi& E) {
;     ...
;     for (int i = 0; i < 2; ++i) { int R, C; stage_rc(tid * 16 + i * 8192, R, C); const int Rb = Epi::PERM ? ((R & ~31) + perm32(R & 31)) : R;
;         voffA[i] = (unsigned)(R * K + C) * 2u; voffB[i] = (unsigned)(Rb * K + C) * 2u; }
;     const size_t kstep = (size_t)(BK * 2);
;     const size_t hstep = (size_t)HALF * K * 2;
;     const size_t tstep = 2 * hstep;
;     const unsigned ldsw = (unsigned)wid * 1024u;
;     const int aoff = lds_byte(wr * 64 + fr, fq * 8), boff = lds_byte(wc * 32 + fr, fq * 8);
;     ...
;     Unit cur, nxt; int ui = 0;
;     ...
;     unsigned pg8_probe_acc = 0u;
;     ...
;     if (!S.next(0, cur)) return;
;     ...
;     const unsigned long long tramp_ = __builtin_amdgcn_s_memrealtime();
;     ...
;     static_assert(!Epi::ROWSCALE || SP2, "row factors are staged in the SP2 prologue");
;     f32x4 rowp_ = {0.f, 0.f, 0.f, 0.f}; if constexpr (Epi::ROWSCALE) rowp_ = load_row_partials(E.rsp, cur.pm, tid);
;     f32x4 acc[2][2][4][2];
; #pragma unroll
;     for (int a = 0; a < 2; ++a)
; #pragma unroll
;         for (int b = 0; b < 2; ++b)
; #pragma unroll
;             for (int m = 0; m < 4; ++m)
; #pragma unroll
;                 for (int n = 0; n < 2; ++n) acc[a][b][m][n] = (f32x4){0.f, 0.f, 0.f, 0.f};
;     bf16x8 At[4][2], B0[2][2], B1[2][2];
;     const char* cA = (const char*)g.A + (size_t)cur.pm * tstep + (cur.half == 2 ? hstep : (size_t)0); const char* cB = (const char*)g.Bt + (size_t)cur.pn * tstep;
;     S.a_ready(cur);
;     if constexpr (SP2) {
;         PG8_STAGE(PG8_SB(0, 0), cB, voffB); PG8_STAGE(PG8_SB(0, 1), cB + hstep, voffB); PG8_STAGE(PG8_SA(0, 0), cA, voffA); PG8_STAGE(PG8_SA(0, 1), cA + hstep, voffA);
;         if (wr == 1) PG8_BAR;
.LBB0_385:
	s_or_b64 exec, exec, s[0:1]
	v_ashrrev_i32_e32 v9, 31, v2
	v_lshrrev_b32_e32 v9, 26, v9
	v_add_u32_e32 v9, v2, v9
	v_ashrrev_i32_e32 v16, 6, v9
	v_bfe_i32 v9, v2, 27, 1
	v_lshlrev_b32_e32 v8, 4, v2
	v_lshrrev_b32_e32 v9, 22, v9
	v_add_u32_e32 v9, v8, v9
	v_and_b32_e32 v9, 0xfffffc00, v9
	v_sub_u32_e32 v9, v8, v9
	v_lshrrev_b32_e32 v10, 4, v9
	v_bitop3_b32 v9, v10, v9, 32 bitop3:0x6c
	v_ashrrev_i32_e32 v11, 31, v9
	v_lshrrev_b32_e32 v11, 26, v11
	v_add_u32_e32 v11, v9, v11
	v_lshlrev_b32_e32 v10, 3, v16
	v_ashrrev_i32_e32 v17, 6, v11
	v_and_b32_e32 v11, 0xc0, v11
	v_and_b32_e32 v10, -16, v10
	v_sub_u32_e32 v9, v9, v11
	v_add_u32_e32 v10, v17, v10
	v_ashrrev_i16_sdwa v9, v224, sext(v9) dst_sel:DWORD dst_unused:UNUSED_PAD src0_sel:DWORD src1_sel:BYTE_0
	v_lshlrev_b32_e32 v12, 5, v16
	v_bfe_i32 v18, v9, 0, 16
	v_lshlrev_b32_e32 v9, 1, v10
	v_lshrrev_b32_e32 v11, 2, v10
	v_and_b32_e32 v13, 3, v17
	s_mov_b32 s0, 0x1fffe0
	v_and_b32_e32 v12, 32, v12
	v_and_b32_e32 v9, 24, v9
	v_and_b32_e32 v11, 4, v11
	v_and_or_b32 v13, v10, s0, v13
	v_or3_b32 v9, v13, v11, v9
	v_add_lshl_u32 v11, v12, v18, 1
	v_add_u32_e32 v8, 0x2000, v8
	v_lshl_add_u32 v166, v9, 11, v11
	v_ashrrev_i32_e32 v9, 31, v8
	v_lshrrev_b32_e32 v9, 22, v9
	v_add_u32_e32 v9, v8, v9
	v_ashrrev_i32_e32 v19, 10, v9
	v_mul_i32_i24_e32 v9, 0x400, v19
	v_sub_u32_e32 v8, v8, v9
	v_lshrrev_b32_e32 v9, 4, v8
	v_bitop3_b32 v8, v9, v8, 32 bitop3:0x6c
	v_lshl_add_u32 v164, v10, 11, v11
	v_ashrrev_i32_e32 v10, 31, v8
	v_lshrrev_b32_e32 v10, 26, v10
	v_lshlrev_b32_e32 v9, 3, v19
	v_add_u32_e32 v10, v8, v10
	s_add_u32 s24, s16, 0x14000000
	v_and_b32_e32 v9, -16, v9
	v_ashrrev_i32_e32 v20, 6, v10
	s_addc_u32 s25, s17, 0
	s_ashr_i32 s11, s10, 6
	v_add_u32_e32 v9, v20, v9
	v_and_b32_e32 v12, 3, v20
	s_mul_i32 s36, s77, 0xee0000
	v_and_or_b32 v12, v9, s0, v12
	s_ashr_i32 s26, s10, 8
	s_lshl_b32 s27, s11, 10
	s_lshl_b64 s[0:1], s[36:37], 1
	s_add_u32 s28, s22, s0
	v_and_b32_e32 v10, 0xc0, v10
	s_addc_u32 s29, s23, s1
	s_ashr_i32 s19, s18, 31
	s_ashr_i32 s71, s70, 31
	v_sub_u32_e32 v8, v8, v10
	s_lshl_b64 s[6:7], s[18:19], 19
	s_lshl_b64 s[0:1], s[70:71], 19
	v_ashrrev_i16_sdwa v8, v224, sext(v8) dst_sel:DWORD dst_unused:UNUSED_PAD src0_sel:DWORD src1_sel:BYTE_0
	s_add_u32 s0, s28, s0
	v_lshlrev_b32_e32 v11, 5, v19
	v_bfe_i32 v21, v8, 0, 16
	v_lshlrev_b32_e32 v8, 1, v9
	v_lshrrev_b32_e32 v10, 2, v9
	s_addc_u32 s1, s29, s1
	s_add_i32 s19, s27, 0
	v_and_b32_e32 v11, 32, v11
	v_and_b32_e32 v8, 24, v8
	v_and_b32_e32 v10, 4, v10
	s_add_i32 m0, s19, 0x10000
	v_or3_b32 v8, v12, v10, v8
	v_add_lshl_u32 v10, v11, v21, 1
	global_load_lds_dwordx4 v166, s[0:1]
	s_add_i32 m0, s19, 0x12000
	v_lshl_add_u32 v170, v8, 11, v10
	s_add_u32 s8, s0, 0x40000
	global_load_lds_dwordx4 v170, s[0:1]
	s_addc_u32 s9, s1, 0
	s_add_i32 m0, s19, 0x14000
	v_lshl_add_u32 v168, v9, 11, v10
	global_load_lds_dwordx4 v166, s[8:9]
	s_add_i32 m0, s19, 0x16000
	s_nop 0
	global_load_lds_dwordx4 v170, s[8:9]
	s_add_u32 s8, s24, s6
	s_addc_u32 s9, s25, s7
	s_add_i32 s30, s19, 0x2000
	s_mov_b32 m0, s19
	s_add_u32 s6, s8, 0x40000
	global_load_lds_dwordx4 v164, s[8:9]
	s_mov_b32 m0, s30
	s_addc_u32 s7, s9, 0
	s_add_i32 s31, s19, 0x4000
	global_load_lds_dwordx4 v168, s[8:9]
	s_mov_b32 m0, s31
	s_add_i32 s34, s19, 0x6000
	global_load_lds_dwordx4 v164, s[6:7]
	s_mov_b32 m0, s34
	s_cmp_eq_u32 s26, 1
	global_load_lds_dwordx4 v168, s[6:7]
	s_cselect_b64 s[56:57], -1, 0
	s_cmp_lg_u32 s26, 1
	s_cbranch_scc1 .LBB0_387
	s_setprio 1
	s_barrier

; #define PG8_STAGE(bufoff, gbase, voff) do { _Pragma("unroll") for (int _i = 0; _i < 2; ++_i) \
;         __builtin_amdgcn_global_load_lds((const unsigned*)((const char*)(gbase) + (voff)[_i]), (PG8_LAS unsigned*)(lds + (bufoff) + ldsw + _i * 8192), 16, 0, 0); } while (0)
; #define PG8_LDA(dst, b, h) do { _Pragma("unroll") for (int m = 0; m < 4; ++m) _Pragma("unroll") for (int k = 0; k < 2; ++k) dst[m][k] = *(const PG8_LAS bf16x8*)(lds + PG8_SA(b, h) + aoff + m * 2048 + k * 1024); } while (0)
; #define PG8_LDB(dst, b, h) do { _Pragma("unroll") for (int n = 0; n < 2; ++n) _Pragma("unroll") for (int k = 0; k < 2; ++k) dst[n][k] = *(const PG8_LAS bf16x8*)(lds + PG8_SB(b, h) + boff + n * 2048 + k * 1024); } while (0)
; #define PG8_MMA(ai, bj, At, Bt) do { __builtin_amdgcn_s_setprio(1); _Pragma("unroll") for (int m = 0; m < 4; ++m) _Pragma("unroll") for (int n = 0; n < 2; ++n) _Pragma("unroll") for (int k = 0; k < 2; ++k) \
;         acc[ai][bj][m][n] = __builtin_amdgcn_mfma_f32_16x16x32_bf16(Bt[n][k], At[m][k], acc[ai][bj][m][n], 0, 0, 0); __builtin_amdgcn_s_setprio(0); } while (0)
; #define PG8_WAIT_V(n) asm volatile("s_waitcnt vmcnt(" #n ")" ::: "memory")
; #define PG8_WAIT_L(n) asm volatile("s_waitcnt lgkmcnt(" #n ")" ::: "memory")
; #define PG8_BAR __builtin_amdgcn_s_barrier()
; #define PG8_SCHED __builtin_amdgcn_sched_barrier(0)
; template <class Epi, class Sched, bool ALIGN_EPI = false, bool SP2 = false>
; __device__ __forceinline__ void gemm_phase(PG8_LAS unsigned char* lds, const Gemm g, const Sched& S, const Epi& E) {
;     ...
;             PG8_LDB(B0, 0, 0); PG8_LDB(B1, 0, 1); PG8_SCHED; PG8_LDA(At, 0, 0); PG8_STAGE(PG8_SA(1, 1), a1 + hstep, voffA);
;     ...
;             if (PROBE_KIND == 18 && t == 0 && ui > 0 && g.probe) { const unsigned long long tq_ = __builtin_amdgcn_s_memrealtime(); PG8_WAIT_V(8); pg8_probe_acc += (unsigned)(__builtin_amdgcn_s_memrealtime() - tq_); }
;     ...
;             PG8_WAIT_V(8); PG8_WAIT_L(0); PG8_BAR; PG8_MMA(0, 0, At, B0); PG8_MMA(0, 1, At, B1); PG8_BAR; PG8_SCHED;
;             PG8_LDA(At, 0, 1); PG8_STAGE(PG8_SB(0, 0), b2, voffB); PG8_STAGE(PG8_SB(0, 1), b2 + hstep, voffB); PG8_STAGE(PG8_SA(0, 0), a2, voffA);
;             PG8_WAIT_V(8); PG8_WAIT_L(0); PG8_BAR; if (cur.half == 0) { PG8_MMA(1, 0, At, B0); PG8_MMA(1, 1, At, B1); } PG8_BAR; PG8_SCHED;
.Lpj_ip_1:
	s_waitcnt lgkmcnt(0)
	s_barrier
	s_waitcnt lgkmcnt(0)
	v_mfma_f32_16x16x32_bf16 v[128:131], v[132:135], v[182:185], 0
	v_mfma_f32_16x16x32_bf16 v[124:127], v[140:143], v[182:185], 0
	v_mfma_f32_16x16x32_bf16 v[112:115], v[132:135], v[190:193], 0
	v_mfma_f32_16x16x32_bf16 v[108:111], v[140:143], v[190:193], 0
	v_mfma_f32_16x16x32_bf16 v[96:99], v[132:135], v[198:201], 0
	v_mfma_f32_16x16x32_bf16 v[92:95], v[140:143], v[198:201], 0
	v_mfma_f32_16x16x32_bf16 v[80:83], v[132:135], v[212:215], 0
	v_mfma_f32_16x16x32_bf16 v[76:79], v[140:143], v[212:215], 0
	v_mfma_f32_16x16x32_bf16 v[128:131], v[136:139], v[186:189], v[128:131]
	v_mfma_f32_16x16x32_bf16 v[124:127], v[144:147], v[186:189], v[124:127]
	v_mfma_f32_16x16x32_bf16 v[112:115], v[136:139], v[194:197], v[112:115]
	v_mfma_f32_16x16x32_bf16 v[108:111], v[144:147], v[194:197], v[108:111]
	v_mfma_f32_16x16x32_bf16 v[96:99], v[136:139], v[208:211], v[96:99]
	v_mfma_f32_16x16x32_bf16 v[92:95], v[144:147], v[208:211], v[92:95]
	v_mfma_f32_16x16x32_bf16 v[80:83], v[136:139], v[216:219], v[80:83]
	v_mfma_f32_16x16x32_bf16 v[76:79], v[144:147], v[216:219], v[76:79]
	v_mfma_f32_16x16x32_bf16 v[120:123], v[148:151], v[182:185], 0
	v_mfma_f32_16x16x32_bf16 v[116:119], v[156:159], v[182:185], 0
	v_mfma_f32_16x16x32_bf16 v[104:107], v[148:151], v[190:193], 0
	v_mfma_f32_16x16x32_bf16 v[100:103], v[156:159], v[190:193], 0
	v_mfma_f32_16x16x32_bf16 v[88:91], v[148:151], v[198:201], 0
	v_mfma_f32_16x16x32_bf16 v[84:87], v[156:159], v[198:201], 0
	v_mfma_f32_16x16x32_bf16 v[72:75], v[148:151], v[212:215], 0
	v_mfma_f32_16x16x32_bf16 v[68:71], v[156:159], v[212:215], 0
	v_mfma_f32_16x16x32_bf16 v[120:123], v[152:155], v[186:189], v[120:123]
	v_mfma_f32_16x16x32_bf16 v[116:119], v[160:163], v[186:189], v[116:119]
	v_mfma_f32_16x16x32_bf16 v[104:107], v[152:155], v[194:197], v[104:107]
	v_mfma_f32_16x16x32_bf16 v[100:103], v[160:163], v[194:197], v[100:103]
	v_mfma_f32_16x16x32_bf16 v[88:91], v[152:155], v[208:211], v[88:91]
	v_mfma_f32_16x16x32_bf16 v[84:87], v[160:163], v[208:211], v[84:87]
	v_mfma_f32_16x16x32_bf16 v[72:75], v[152:155], v[216:219], v[72:75]
	v_mfma_f32_16x16x32_bf16 v[68:71], v[160:163], v[216:219], v[68:71]
	s_barrier
	s_add_i32 s61, s61, s27
	v_lshl_add_u64 v[228:229], s[0:1], 0, v[166:167]
	s_mov_b32 m0, s61
	ds_read_b128 v[182:185], v206 offset:16384
	ds_read_b128 v[186:189], v206 offset:17408
	ds_read_b128 v[190:193], v206 offset:18432
	ds_read_b128 v[194:197], v206 offset:19456
	ds_read_b128 v[198:201], v206 offset:20480
	ds_read_b128 v[208:211], v206 offset:21504
	ds_read_b128 v[212:215], v206 offset:22528
	ds_read_b128 v[216:219], v206 offset:23552
	global_load_lds_dwordx4 v[228:229], off
	s_add_i32 m0, s61, 0x2000
	s_add_u32 s78, s0, 0x40000
	v_lshl_add_u64 v[230:231], s[0:1], 0, v[170:171]
	s_addc_u32 s79, s1, 0
	s_add_i32 s61, s63, s27
	global_load_lds_dwordx4 v[230:231], off
	v_lshl_add_u64 v[232:233], s[78:79], 0, v[166:167]
	s_mov_b32 m0, s61
	v_lshl_add_u64 v[234:235], s[10:11], 0, v[168:169]
	global_load_lds_dwordx4 v[232:233], off
	v_lshl_add_u64 v[232:233], s[78:79], 0, v[170:171]
	s_add_i32 m0, s61, 0x2000
	s_nop 0
	global_load_lds_dwordx4 v[232:233], off
	v_lshl_add_u64 v[232:233], s[10:11], 0, v[164:165]
	s_mov_b32 m0, s19
	s_nop 0
	global_load_lds_dwordx4 v[232:233], off
	s_mov_b32 m0, s30
	s_nop 0
	global_load_lds_dwordx4 v[234:235], off
	s_cmp_eq_u32 s32, 0
	s_cbranch_scc1 .Lpw_ip_2
	s_waitcnt vmcnt(24)
	s_branch .Lpj_ip_2
	.p2align 6
	s_nop 0
	s_nop 0
	s_nop 0
	s_nop 0
	s_nop 0
	s_nop 0
	s_nop 0
	s_nop 0
	s_nop 0
	s_nop 0
	s_nop 0
	s_nop 0
	s_nop 0

; #define PG8_STAGE(bufoff, gbase, voff) do { _Pragma("unroll") for (int _i = 0; _i < 2; ++_i) \
;         __builtin_amdgcn_global_load_lds((const unsigned*)((const char*)(gbase) + (voff)[_i]), (PG8_LAS unsigned*)(lds + (bufoff) + ldsw + _i * 8192), 16, 0, 0); } while (0)
; #define PG8_LDA(dst, b, h) do { _Pragma("unroll") for (int m = 0; m < 4; ++m) _Pragma("unroll") for (int k = 0; k < 2; ++k) dst[m][k] = *(const PG8_LAS bf16x8*)(lds + PG8_SA(b, h) + aoff + m * 2048 + k * 1024); } while (0)
; #define PG8_LDB(dst, b, h) do { _Pragma("unroll") for (int n = 0; n < 2; ++n) _Pragma("unroll") for (int k = 0; k < 2; ++k) dst[n][k] = *(const PG8_LAS bf16x8*)(lds + PG8_SB(b, h) + boff + n * 2048 + k * 1024); } while (0)
; #define PG8_MMA(ai, bj, At, Bt) do { __builtin_amdgcn_s_setprio(1); _Pragma("unroll") for (int m = 0; m < 4; ++m) _Pragma("unroll") for (int n = 0; n < 2; ++n) _Pragma("unroll") for (int k = 0; k < 2; ++k) \
;         acc[ai][bj][m][n] = __builtin_amdgcn_mfma_f32_16x16x32_bf16(Bt[n][k], At[m][k], acc[ai][bj][m][n], 0, 0, 0); __builtin_amdgcn_s_setprio(0); } while (0)
; #define PG8_WAIT_V(n) asm volatile("s_waitcnt vmcnt(" #n ")" ::: "memory")
; #define PG8_WAIT_L(n) asm volatile("s_waitcnt lgkmcnt(" #n ")" ::: "memory")
; #define PG8_BAR __builtin_amdgcn_s_barrier()
; #define PG8_SCHED __builtin_amdgcn_sched_barrier(0)
; template <class Epi, class Sched, bool ALIGN_EPI = false, bool SP2 = false>
; __device__ __forceinline__ void gemm_phase(PG8_LAS unsigned char* lds, const Gemm g, const Sched& S, const Epi& E) {
;     ...
;             PG8_WAIT_V(8); PG8_WAIT_L(0); PG8_BAR; if (cur.half == 0) { PG8_MMA(1, 0, At, B0); PG8_MMA(1, 1, At, B1); } PG8_BAR; PG8_SCHED;
;             PG8_LDB(B0, 1, 0); PG8_LDB(B1, 1, 1); PG8_SCHED; PG8_LDA(At, 1, 0); PG8_STAGE(PG8_SA(0, 1), a2 + hstep, voffA);
;             PG8_WAIT_V(8); PG8_WAIT_L(0); PG8_BAR; PG8_MMA(0, 0, At, B0); PG8_MMA(0, 1, At, B1); PG8_BAR; PG8_SCHED;
.Lpj_ip_2:
	s_waitcnt lgkmcnt(0)
	s_barrier
	s_waitcnt lgkmcnt(0)
	v_mfma_f32_16x16x32_bf16 v[64:67], v[132:135], v[182:185], 0
	v_mfma_f32_16x16x32_bf16 v[60:63], v[140:143], v[182:185], 0
	v_mfma_f32_16x16x32_bf16 v[48:51], v[132:135], v[190:193], 0
	v_mfma_f32_16x16x32_bf16 v[44:47], v[140:143], v[190:193], 0
	v_mfma_f32_16x16x32_bf16 v[32:35], v[132:135], v[198:201], 0
	v_mfma_f32_16x16x32_bf16 v[28:31], v[140:143], v[198:201], 0
	v_mfma_f32_16x16x32_bf16 v[16:19], v[132:135], v[212:215], 0
	v_mfma_f32_16x16x32_bf16 v[12:15], v[140:143], v[212:215], 0
	v_mfma_f32_16x16x32_bf16 v[64:67], v[136:139], v[186:189], v[64:67]
	v_mfma_f32_16x16x32_bf16 v[60:63], v[144:147], v[186:189], v[60:63]
	v_mfma_f32_16x16x32_bf16 v[48:51], v[136:139], v[194:197], v[48:51]
	v_mfma_f32_16x16x32_bf16 v[44:47], v[144:147], v[194:197], v[44:47]
	v_mfma_f32_16x16x32_bf16 v[32:35], v[136:139], v[208:211], v[32:35]
	v_mfma_f32_16x16x32_bf16 v[28:31], v[144:147], v[208:211], v[28:31]
	v_mfma_f32_16x16x32_bf16 v[16:19], v[136:139], v[216:219], v[16:19]
	v_mfma_f32_16x16x32_bf16 v[12:15], v[144:147], v[216:219], v[12:15]
	v_mfma_f32_16x16x32_bf16 v[56:59], v[148:151], v[182:185], 0
	v_mfma_f32_16x16x32_bf16 v[52:55], v[156:159], v[182:185], 0
	v_mfma_f32_16x16x32_bf16 v[40:43], v[148:151], v[190:193], 0
	v_mfma_f32_16x16x32_bf16 v[36:39], v[156:159], v[190:193], 0
	v_mfma_f32_16x16x32_bf16 v[24:27], v[148:151], v[198:201], 0
	v_mfma_f32_16x16x32_bf16 v[20:23], v[156:159], v[198:201], 0
	v_mfma_f32_16x16x32_bf16 v[8:11], v[148:151], v[212:215], 0
	v_mfma_f32_16x16x32_bf16 v[4:7], v[156:159], v[212:215], 0
	v_mfma_f32_16x16x32_bf16 v[56:59], v[152:155], v[186:189], v[56:59]
	v_mfma_f32_16x16x32_bf16 v[52:55], v[160:163], v[186:189], v[52:55]
	v_mfma_f32_16x16x32_bf16 v[40:43], v[152:155], v[194:197], v[40:43]
	v_mfma_f32_16x16x32_bf16 v[36:39], v[160:163], v[194:197], v[36:39]
	v_mfma_f32_16x16x32_bf16 v[24:27], v[152:155], v[208:211], v[24:27]
	v_mfma_f32_16x16x32_bf16 v[20:23], v[160:163], v[208:211], v[20:23]
	v_mfma_f32_16x16x32_bf16 v[8:11], v[152:155], v[216:219], v[8:11]
	v_mfma_f32_16x16x32_bf16 v[4:7], v[160:163], v[216:219], v[4:7]
	s_barrier
	s_add_i32 s61, 0, 0x18000
	v_add_u32_e32 v2, s61, v203
	s_add_i32 s63, 0, 0x1c000
	ds_read_b128 v[132:135], v2
	ds_read_b128 v[136:139], v2 offset:1024
	ds_read_b128 v[140:143], v2 offset:2048
	ds_read_b128 v[144:147], v2 offset:3072
	v_add_u32_e32 v2, s63, v203
	ds_read_b128 v[148:151], v2
	ds_read_b128 v[152:155], v2 offset:1024
	ds_read_b128 v[156:159], v2 offset:2048
	ds_read_b128 v[160:163], v2 offset:3072
	s_add_u32 s10, s10, 0x40000
	s_addc_u32 s11, s11, 0
	s_mov_b32 m0, s31
	v_lshl_add_u64 v[236:237], s[10:11], 0, v[164:165]
	ds_read_b128 v[182:185], v206 offset:32768
	ds_read_b128 v[186:189], v206 offset:33792
	ds_read_b128 v[190:193], v206 offset:34816
	ds_read_b128 v[194:197], v206 offset:35840
	ds_read_b128 v[198:201], v206 offset:36864
	ds_read_b128 v[208:211], v206 offset:37888
	ds_read_b128 v[212:215], v206 offset:38912
	ds_read_b128 v[216:219], v206 offset:39936
	global_load_lds_dwordx4 v[236:237], off
	v_lshl_add_u64 v[236:237], s[10:11], 0, v[168:169]
	s_mov_b32 m0, s34
	s_nop 0
	global_load_lds_dwordx4 v[236:237], off
	s_waitcnt vmcnt(8)
	s_waitcnt lgkmcnt(0)
	s_barrier
	s_waitcnt lgkmcnt(0)
	v_mfma_f32_16x16x32_bf16 v[128:131], v[132:135], v[182:185], v[128:131]
	v_mfma_f32_16x16x32_bf16 v[124:127], v[140:143], v[182:185], v[124:127]
	v_mfma_f32_16x16x32_bf16 v[112:115], v[132:135], v[190:193], v[112:115]
	v_mfma_f32_16x16x32_bf16 v[108:111], v[140:143], v[190:193], v[108:111]
	v_mfma_f32_16x16x32_bf16 v[96:99], v[132:135], v[198:201], v[96:99]
	v_mfma_f32_16x16x32_bf16 v[92:95], v[140:143], v[198:201], v[92:95]
	v_mfma_f32_16x16x32_bf16 v[80:83], v[132:135], v[212:215], v[80:83]
	v_mfma_f32_16x16x32_bf16 v[76:79], v[140:143], v[212:215], v[76:79]
	v_mfma_f32_16x16x32_bf16 v[128:131], v[136:139], v[186:189], v[128:131]
	v_mfma_f32_16x16x32_bf16 v[124:127], v[144:147], v[186:189], v[124:127]
	v_mfma_f32_16x16x32_bf16 v[112:115], v[136:139], v[194:197], v[112:115]
	v_mfma_f32_16x16x32_bf16 v[108:111], v[144:147], v[194:197], v[108:111]
	v_mfma_f32_16x16x32_bf16 v[96:99], v[136:139], v[208:211], v[96:99]
	v_mfma_f32_16x16x32_bf16 v[92:95], v[144:147], v[208:211], v[92:95]
	v_mfma_f32_16x16x32_bf16 v[80:83], v[136:139], v[216:219], v[80:83]
	v_mfma_f32_16x16x32_bf16 v[76:79], v[144:147], v[216:219], v[76:79]
	v_mfma_f32_16x16x32_bf16 v[120:123], v[148:151], v[182:185], v[120:123]
	v_mfma_f32_16x16x32_bf16 v[116:119], v[156:159], v[182:185], v[116:119]
	v_mfma_f32_16x16x32_bf16 v[104:107], v[148:151], v[190:193], v[104:107]
	v_mfma_f32_16x16x32_bf16 v[100:103], v[156:159], v[190:193], v[100:103]
	v_mfma_f32_16x16x32_bf16 v[88:91], v[148:151], v[198:201], v[88:91]
	v_mfma_f32_16x16x32_bf16 v[84:87], v[156:159], v[198:201], v[84:87]
	v_mfma_f32_16x16x32_bf16 v[72:75], v[148:151], v[212:215], v[72:75]
	v_mfma_f32_16x16x32_bf16 v[68:71], v[156:159], v[212:215], v[68:71]
	v_mfma_f32_16x16x32_bf16 v[120:123], v[152:155], v[186:189], v[120:123]
	v_mfma_f32_16x16x32_bf16 v[116:119], v[160:163], v[186:189], v[116:119]
	v_mfma_f32_16x16x32_bf16 v[104:107], v[152:155], v[194:197], v[104:107]
	v_mfma_f32_16x16x32_bf16 v[100:103], v[160:163], v[194:197], v[100:103]
	v_mfma_f32_16x16x32_bf16 v[88:91], v[152:155], v[208:211], v[88:91]
	v_mfma_f32_16x16x32_bf16 v[84:87], v[160:163], v[208:211], v[84:87]
	v_mfma_f32_16x16x32_bf16 v[72:75], v[152:155], v[216:219], v[72:75]
	v_mfma_f32_16x16x32_bf16 v[68:71], v[160:163], v[216:219], v[68:71]
	s_barrier
; #define PG8_STAGE(bufoff, gbase, voff) do { _Pragma("unroll") for (int _i = 0; _i < 2; ++_i) \
;         __builtin_amdgcn_global_load_lds((const unsigned*)((const char*)(gbase) + (voff)[_i]), (PG8_LAS unsigned*)(lds + (bufoff) + ldsw + _i * 8192), 16, 0, 0); } while (0)
; #define PG8_LDA(dst, b, h) do { _Pragma("unroll") for (int m = 0; m < 4; ++m) _Pragma("unroll") for (int k = 0; k < 2; ++k) dst[m][k] = *(const PG8_LAS bf16x8*)(lds + PG8_SA(b, h) + aoff + m * 2048 + k * 1024); } while (0)
; #define PG8_LDB(dst, b, h) do { _Pragma("unroll") for (int n = 0; n < 2; ++n) _Pragma("unroll") for (int k = 0; k < 2; ++k) dst[n][k] = *(const PG8_LAS bf16x8*)(lds + PG8_SB(b, h) + boff + n * 2048 + k * 1024); } while (0)
; #define PG8_WAIT_V(n) asm volatile("s_waitcnt vmcnt(" #n ")" ::: "memory")
; #define PG8_WAIT_L(n) asm volatile("s_waitcnt lgkmcnt(" #n ")" ::: "memory")
; template <class Epi, class Sched, bool ALIGN_EPI = false, bool SP2 = false>
; __device__ __forceinline__ void gemm_phase(PG8_LAS unsigned char* lds, const Gemm g, const Sched& S, const Epi& E) {
;     ...
;             PG8_LDB(B0, 0, 0); PG8_LDB(B1, 0, 1); PG8_SCHED; PG8_LDA(At, 0, 0); PG8_STAGE(PG8_SA(1, 1), a1 + hstep, voffA);
;     ...
;             if (PROBE_KIND == 18 && t == 0 && ui > 0 && g.probe) { const unsigned long long tq_ = __builtin_amdgcn_s_memrealtime(); PG8_WAIT_V(8); pg8_probe_acc += (unsigned)(__builtin_amdgcn_s_memrealtime() - tq_); }
;     ...
;             PG8_WAIT_V(8); PG8_WAIT_L(0); PG8_BAR; PG8_MMA(0, 0, At, B0); PG8_MMA(0, 1, At, B1); PG8_BAR; PG8_SCHED;
;             PG8_LDA(At, 0, 1); PG8_STAGE(PG8_SB(0, 0), b2, voffB); PG8_STAGE(PG8_SB(0, 1), b2 + hstep, voffB); PG8_STAGE(PG8_SA(0, 0), a2, voffA);
;             PG8_WAIT_V(8); PG8_WAIT_L(0); PG8_BAR; if (cur.half == 0) { PG8_MMA(1, 0, At, B0); PG8_MMA(1, 1, At, B1); } PG8_BAR; PG8_SCHED;
;             PG8_LDB(B0, 1, 0); PG8_LDB(B1, 1, 1); PG8_SCHED; PG8_LDA(At, 1, 0); PG8_STAGE(PG8_SA(0, 1), a2 + hstep, voffA);
;             PG8_WAIT_V(8); PG8_WAIT_L(0); PG8_BAR; PG8_MMA(0, 0, At, B0); PG8_MMA(0, 1, At, B1); PG8_BAR; PG8_SCHED;
;             PG8_LDA(At, 1, 1); PG8_STAGE(PG8_SB(1, 0), b3, voffB); PG8_STAGE(PG8_SB(1, 1), b3 + hstep, voffB); PG8_STAGE(PG8_SA(1, 0), a3, voffA);
;             PG8_WAIT_V(8); PG8_WAIT_L(0); PG8_BAR; if (cur.half == 0) { PG8_MMA(1, 0, At, B0); PG8_MMA(1, 1, At, B1); } PG8_BAR; PG8_SCHED;
	s_add_i32 s10, s61, s27
	v_lshl_add_u64 v[228:229], v[228:229], 0, s[42:43]
	s_mov_b32 m0, s10
	ds_read_b128 v[182:185], v206 offset:49152
	ds_read_b128 v[186:189], v206 offset:50176
	ds_read_b128 v[190:193], v206 offset:51200
	ds_read_b128 v[194:197], v206 offset:52224
	ds_read_b128 v[198:201], v206 offset:53248
	ds_read_b128 v[208:211], v206 offset:54272
	ds_read_b128 v[212:215], v206 offset:55296
	ds_read_b128 v[216:219], v206 offset:56320
	global_load_lds_dwordx4 v[228:229], off
	s_add_i32 m0, s10, 0x2000
	s_add_u32 s0, s0, 0x40080
	v_lshl_add_u64 v[228:229], v[230:231], 0, s[42:43]
	s_addc_u32 s1, s1, 0
	s_add_i32 s10, s63, s27
	global_load_lds_dwordx4 v[228:229], off
	v_lshl_add_u64 v[228:229], s[0:1], 0, v[166:167]
	s_mov_b32 m0, s10
	s_nop 0
	global_load_lds_dwordx4 v[228:229], off
	v_lshl_add_u64 v[228:229], s[0:1], 0, v[170:171]
	s_add_i32 m0, s10, 0x2000
	s_nop 0
	global_load_lds_dwordx4 v[228:229], off
	v_lshl_add_u64 v[228:229], v[232:233], 0, s[42:43]
	s_mov_b32 m0, s41
	s_nop 0
	global_load_lds_dwordx4 v[228:229], off
	v_lshl_add_u64 v[228:229], v[234:235], 0, s[42:43]
	s_mov_b32 m0, s71
	s_nop 0
	global_load_lds_dwordx4 v[228:229], off
	s_waitcnt vmcnt(8)
	s_waitcnt lgkmcnt(0)
	s_barrier
	s_waitcnt lgkmcnt(0)
	v_mfma_f32_16x16x32_bf16 v[64:67], v[132:135], v[182:185], v[64:67]
	v_mfma_f32_16x16x32_bf16 v[60:63], v[140:143], v[182:185], v[60:63]
	v_mfma_f32_16x16x32_bf16 v[48:51], v[132:135], v[190:193], v[48:51]
	v_mfma_f32_16x16x32_bf16 v[44:47], v[140:143], v[190:193], v[44:47]
	v_mfma_f32_16x16x32_bf16 v[32:35], v[132:135], v[198:201], v[32:35]
	v_mfma_f32_16x16x32_bf16 v[28:31], v[140:143], v[198:201], v[28:31]
	v_mfma_f32_16x16x32_bf16 v[16:19], v[132:135], v[212:215], v[16:19]
	v_mfma_f32_16x16x32_bf16 v[12:15], v[140:143], v[212:215], v[12:15]
	v_mfma_f32_16x16x32_bf16 v[64:67], v[136:139], v[186:189], v[64:67]
	v_mfma_f32_16x16x32_bf16 v[60:63], v[144:147], v[186:189], v[60:63]
	v_mfma_f32_16x16x32_bf16 v[48:51], v[136:139], v[194:197], v[48:51]
	v_mfma_f32_16x16x32_bf16 v[44:47], v[144:147], v[194:197], v[44:47]
	v_mfma_f32_16x16x32_bf16 v[32:35], v[136:139], v[208:211], v[32:35]
	v_mfma_f32_16x16x32_bf16 v[28:31], v[144:147], v[208:211], v[28:31]
	v_mfma_f32_16x16x32_bf16 v[16:19], v[136:139], v[216:219], v[16:19]
	v_mfma_f32_16x16x32_bf16 v[12:15], v[144:147], v[216:219], v[12:15]
	v_mfma_f32_16x16x32_bf16 v[56:59], v[148:151], v[182:185], v[56:59]
	v_mfma_f32_16x16x32_bf16 v[52:55], v[156:159], v[182:185], v[52:55]
	v_mfma_f32_16x16x32_bf16 v[40:43], v[148:151], v[190:193], v[40:43]
	v_mfma_f32_16x16x32_bf16 v[36:39], v[156:159], v[190:193], v[36:39]
	v_mfma_f32_16x16x32_bf16 v[24:27], v[148:151], v[198:201], v[24:27]
	v_mfma_f32_16x16x32_bf16 v[20:23], v[156:159], v[198:201], v[20:23]
	v_mfma_f32_16x16x32_bf16 v[8:11], v[148:151], v[212:215], v[8:11]
	v_mfma_f32_16x16x32_bf16 v[4:7], v[156:159], v[212:215], v[4:7]
	v_mfma_f32_16x16x32_bf16 v[56:59], v[152:155], v[186:189], v[56:59]
	v_mfma_f32_16x16x32_bf16 v[52:55], v[160:163], v[186:189], v[52:55]
	v_mfma_f32_16x16x32_bf16 v[40:43], v[152:155], v[194:197], v[40:43]
	v_mfma_f32_16x16x32_bf16 v[36:39], v[160:163], v[194:197], v[36:39]
	v_mfma_f32_16x16x32_bf16 v[24:27], v[152:155], v[208:211], v[24:27]
	v_mfma_f32_16x16x32_bf16 v[20:23], v[160:163], v[208:211], v[20:23]
	v_mfma_f32_16x16x32_bf16 v[8:11], v[152:155], v[216:219], v[8:11]
	v_mfma_f32_16x16x32_bf16 v[4:7], v[160:163], v[216:219], v[4:7]
	s_barrier
	s_add_i32 s39, s39, 2
	s_add_u32 s8, s8, 0x100
	s_addc_u32 s9, s9, 0
	s_add_u32 s36, s36, 0x100
	s_addc_u32 s38, s38, 0
	s_mov_b32 s32, 1
.LBB0_395:
	s_add_u32 s0, s8, 0xfffc0080
	s_addc_u32 s1, s9, -1
	s_add_i32 s61, 0, 0x10000
	s_cmp_eq_u32 s39, 12
	s_cselect_b32 s11, s12, s1
	s_cselect_b32 s10, s13, s0
	v_add_u32_e32 v2, s61, v203
	s_cselect_b32 s1, s14, s38
	s_cselect_b32 s0, s15, s36
	s_add_i32 s63, 0, 0x14000
	ds_read_b128 v[132:135], v2
	ds_read_b128 v[136:139], v2 offset:1024
	ds_read_b128 v[140:143], v2 offset:2048
	ds_read_b128 v[144:147], v2 offset:3072
	v_add_u32_e32 v2, s63, v203
	ds_read_b128 v[148:151], v2
	ds_read_b128 v[152:155], v2 offset:1024
	ds_read_b128 v[156:159], v2 offset:2048
	ds_read_b128 v[160:163], v2 offset:3072
	v_lshl_add_u64 v[228:229], s[8:9], 0, v[178:179]
	s_add_i32 m0, s19, 0xc000
	ds_read_b128 v[182:185], v206
	ds_read_b128 v[186:189], v206 offset:1024
	ds_read_b128 v[190:193], v206 offset:2048
	ds_read_b128 v[194:197], v206 offset:3072
	ds_read_b128 v[198:201], v206 offset:4096
	ds_read_b128 v[208:211], v206 offset:5120
	ds_read_b128 v[212:215], v206 offset:6144
	ds_read_b128 v[216:219], v206 offset:7168
	global_load_lds_dwordx4 v[228:229], off
	v_lshl_add_u64 v[228:229], s[8:9], 0, v[180:181]
	s_add_i32 m0, s19, 0xe000
	s_nop 0
	global_load_lds_dwordx4 v[228:229], off
	s_waitcnt vmcnt(8)
	s_waitcnt lgkmcnt(0)
	s_barrier
; #define PG8_STAGE(bufoff, gbase, voff) do { _Pragma("unroll") for (int _i = 0; _i < 2; ++_i) \
;         __builtin_amdgcn_global_load_lds((const unsigned*)((const char*)(gbase) + (voff)[_i]), (PG8_LAS unsigned*)(lds + (bufoff) + ldsw + _i * 8192), 16, 0, 0); } while (0)
; #define PG8_LDA(dst, b, h) do { _Pragma("unroll") for (int m = 0; m < 4; ++m) _Pragma("unroll") for (int k = 0; k < 2; ++k) dst[m][k] = *(const PG8_LAS bf16x8*)(lds + PG8_SA(b, h) + aoff + m * 2048 + k * 1024); } while (0)
; #define PG8_MMA(ai, bj, At, Bt) do { __builtin_amdgcn_s_setprio(1); _Pragma("unroll") for (int m = 0; m < 4; ++m) _Pragma("unroll") for (int n = 0; n < 2; ++n) _Pragma("unroll") for (int k = 0; k < 2; ++k) \
;         acc[ai][bj][m][n] = __builtin_amdgcn_mfma_f32_16x16x32_bf16(Bt[n][k], At[m][k], acc[ai][bj][m][n], 0, 0, 0); __builtin_amdgcn_s_setprio(0); } while (0)
; #define PG8_WAIT_V(n) asm volatile("s_waitcnt vmcnt(" #n ")" ::: "memory")
; #define PG8_WAIT_L(n) asm volatile("s_waitcnt lgkmcnt(" #n ")" ::: "memory")
; #define PG8_BAR __builtin_amdgcn_s_barrier()
; #define PG8_SCHED __builtin_amdgcn_sched_barrier(0)
; template <class Epi, class Sched, bool ALIGN_EPI = false, bool SP2 = false>
; __device__ __forceinline__ void gemm_phase(PG8_LAS unsigned char* lds, const Gemm g, const Sched& S, const Epi& E) {
;     ...
;             PG8_WAIT_V(8); PG8_WAIT_L(0); PG8_BAR; PG8_MMA(0, 0, At, B0); PG8_MMA(0, 1, At, B1); PG8_BAR; PG8_SCHED;
;             PG8_LDA(At, 0, 1); PG8_STAGE(PG8_SB(0, 0), b2, voffB); PG8_STAGE(PG8_SB(0, 1), b2 + hstep, voffB); PG8_STAGE(PG8_SA(0, 0), a2, voffA);
;             PG8_WAIT_V(8); PG8_WAIT_L(0); PG8_BAR; if (cur.half == 0) { PG8_MMA(1, 0, At, B0); PG8_MMA(1, 1, At, B1); } PG8_BAR; PG8_SCHED;
	s_waitcnt lgkmcnt(0)
	v_mfma_f32_16x16x32_bf16 v[128:131], v[132:135], v[182:185], v[128:131]
	v_mfma_f32_16x16x32_bf16 v[124:127], v[140:143], v[182:185], v[124:127]
	v_mfma_f32_16x16x32_bf16 v[112:115], v[132:135], v[190:193], v[112:115]
	v_mfma_f32_16x16x32_bf16 v[108:111], v[140:143], v[190:193], v[108:111]
	v_mfma_f32_16x16x32_bf16 v[96:99], v[132:135], v[198:201], v[96:99]
	v_mfma_f32_16x16x32_bf16 v[92:95], v[140:143], v[198:201], v[92:95]
	v_mfma_f32_16x16x32_bf16 v[80:83], v[132:135], v[212:215], v[80:83]
	v_mfma_f32_16x16x32_bf16 v[76:79], v[140:143], v[212:215], v[76:79]
	v_mfma_f32_16x16x32_bf16 v[128:131], v[136:139], v[186:189], v[128:131]
	v_mfma_f32_16x16x32_bf16 v[124:127], v[144:147], v[186:189], v[124:127]
	v_mfma_f32_16x16x32_bf16 v[112:115], v[136:139], v[194:197], v[112:115]
	v_mfma_f32_16x16x32_bf16 v[108:111], v[144:147], v[194:197], v[108:111]
	v_mfma_f32_16x16x32_bf16 v[96:99], v[136:139], v[208:211], v[96:99]
	v_mfma_f32_16x16x32_bf16 v[92:95], v[144:147], v[208:211], v[92:95]
	v_mfma_f32_16x16x32_bf16 v[80:83], v[136:139], v[216:219], v[80:83]
	v_mfma_f32_16x16x32_bf16 v[76:79], v[144:147], v[216:219], v[76:79]
	v_mfma_f32_16x16x32_bf16 v[120:123], v[148:151], v[182:185], v[120:123]
	v_mfma_f32_16x16x32_bf16 v[116:119], v[156:159], v[182:185], v[116:119]
	v_mfma_f32_16x16x32_bf16 v[104:107], v[148:151], v[190:193], v[104:107]
	v_mfma_f32_16x16x32_bf16 v[100:103], v[156:159], v[190:193], v[100:103]
	v_mfma_f32_16x16x32_bf16 v[88:91], v[148:151], v[198:201], v[88:91]
	v_mfma_f32_16x16x32_bf16 v[84:87], v[156:159], v[198:201], v[84:87]
	v_mfma_f32_16x16x32_bf16 v[72:75], v[148:151], v[212:215], v[72:75]
	v_mfma_f32_16x16x32_bf16 v[68:71], v[156:159], v[212:215], v[68:71]
	v_mfma_f32_16x16x32_bf16 v[120:123], v[152:155], v[186:189], v[120:123]
	v_mfma_f32_16x16x32_bf16 v[116:119], v[160:163], v[186:189], v[116:119]
	v_mfma_f32_16x16x32_bf16 v[104:107], v[152:155], v[194:197], v[104:107]
	v_mfma_f32_16x16x32_bf16 v[100:103], v[160:163], v[194:197], v[100:103]
	v_mfma_f32_16x16x32_bf16 v[88:91], v[152:155], v[208:211], v[88:91]
	v_mfma_f32_16x16x32_bf16 v[84:87], v[160:163], v[208:211], v[84:87]
	v_mfma_f32_16x16x32_bf16 v[72:75], v[152:155], v[216:219], v[72:75]
	v_mfma_f32_16x16x32_bf16 v[68:71], v[160:163], v[216:219], v[68:71]
	s_barrier
	s_add_i32 s61, s61, s27
	v_lshl_add_u64 v[228:229], s[0:1], 0, v[166:167]
	s_mov_b32 m0, s61
	ds_read_b128 v[182:185], v206 offset:16384
	ds_read_b128 v[186:189], v206 offset:17408
	ds_read_b128 v[190:193], v206 offset:18432
	ds_read_b128 v[194:197], v206 offset:19456
	ds_read_b128 v[198:201], v206 offset:20480
	ds_read_b128 v[208:211], v206 offset:21504
	ds_read_b128 v[212:215], v206 offset:22528
	ds_read_b128 v[216:219], v206 offset:23552
	global_load_lds_dwordx4 v[228:229], off
	s_add_i32 m0, s61, 0x2000
	s_add_u32 s78, s0, 0x40000
	v_lshl_add_u64 v[230:231], s[0:1], 0, v[170:171]
	s_addc_u32 s79, s1, 0
	s_add_i32 s61, s63, s27
	global_load_lds_dwordx4 v[230:231], off
	v_lshl_add_u64 v[232:233], s[78:79], 0, v[166:167]
	s_mov_b32 m0, s61
	v_lshl_add_u64 v[234:235], s[10:11], 0, v[168:169]
	global_load_lds_dwordx4 v[232:233], off
	v_lshl_add_u64 v[232:233], s[78:79], 0, v[170:171]
	s_add_i32 m0, s61, 0x2000
	s_nop 0
	global_load_lds_dwordx4 v[232:233], off
	v_lshl_add_u64 v[232:233], s[10:11], 0, v[164:165]
	s_mov_b32 m0, s19
	s_nop 0
	global_load_lds_dwordx4 v[232:233], off
	s_mov_b32 m0, s30
	s_nop 0
	global_load_lds_dwordx4 v[234:235], off
	s_waitcnt vmcnt(8)
	s_waitcnt lgkmcnt(0)
	s_barrier
	s_waitcnt lgkmcnt(0)
	v_mfma_f32_16x16x32_bf16 v[64:67], v[132:135], v[182:185], v[64:67]
	v_mfma_f32_16x16x32_bf16 v[60:63], v[140:143], v[182:185], v[60:63]
	v_mfma_f32_16x16x32_bf16 v[48:51], v[132:135], v[190:193], v[48:51]
	v_mfma_f32_16x16x32_bf16 v[44:47], v[140:143], v[190:193], v[44:47]
	v_mfma_f32_16x16x32_bf16 v[32:35], v[132:135], v[198:201], v[32:35]
	v_mfma_f32_16x16x32_bf16 v[28:31], v[140:143], v[198:201], v[28:31]
	v_mfma_f32_16x16x32_bf16 v[16:19], v[132:135], v[212:215], v[16:19]
	v_mfma_f32_16x16x32_bf16 v[12:15], v[140:143], v[212:215], v[12:15]
	v_mfma_f32_16x16x32_bf16 v[64:67], v[136:139], v[186:189], v[64:67]
	v_mfma_f32_16x16x32_bf16 v[60:63], v[144:147], v[186:189], v[60:63]
	v_mfma_f32_16x16x32_bf16 v[48:51], v[136:139], v[194:197], v[48:51]
	v_mfma_f32_16x16x32_bf16 v[44:47], v[144:147], v[194:197], v[44:47]
	v_mfma_f32_16x16x32_bf16 v[32:35], v[136:139], v[208:211], v[32:35]
	v_mfma_f32_16x16x32_bf16 v[28:31], v[144:147], v[208:211], v[28:31]
	v_mfma_f32_16x16x32_bf16 v[16:19], v[136:139], v[216:219], v[16:19]
	v_mfma_f32_16x16x32_bf16 v[12:15], v[144:147], v[216:219], v[12:15]
	v_mfma_f32_16x16x32_bf16 v[56:59], v[148:151], v[182:185], v[56:59]
	v_mfma_f32_16x16x32_bf16 v[52:55], v[156:159], v[182:185], v[52:55]
	v_mfma_f32_16x16x32_bf16 v[40:43], v[148:151], v[190:193], v[40:43]
	v_mfma_f32_16x16x32_bf16 v[36:39], v[156:159], v[190:193], v[36:39]
	v_mfma_f32_16x16x32_bf16 v[24:27], v[148:151], v[198:201], v[24:27]
	v_mfma_f32_16x16x32_bf16 v[20:23], v[156:159], v[198:201], v[20:23]
	v_mfma_f32_16x16x32_bf16 v[8:11], v[148:151], v[212:215], v[8:11]
	v_mfma_f32_16x16x32_bf16 v[4:7], v[156:159], v[212:215], v[4:7]
	v_mfma_f32_16x16x32_bf16 v[56:59], v[152:155], v[186:189], v[56:59]
	v_mfma_f32_16x16x32_bf16 v[52:55], v[160:163], v[186:189], v[52:55]
	v_mfma_f32_16x16x32_bf16 v[40:43], v[152:155], v[194:197], v[40:43]
	v_mfma_f32_16x16x32_bf16 v[36:39], v[160:163], v[194:197], v[36:39]
	v_mfma_f32_16x16x32_bf16 v[24:27], v[152:155], v[208:211], v[24:27]
	v_mfma_f32_16x16x32_bf16 v[20:23], v[160:163], v[208:211], v[20:23]
	v_mfma_f32_16x16x32_bf16 v[8:11], v[152:155], v[216:219], v[8:11]
	v_mfma_f32_16x16x32_bf16 v[4:7], v[160:163], v[216:219], v[4:7]
	s_barrier
; #define PG8_STAGE(bufoff, gbase, voff) do { _Pragma("unroll") for (int _i = 0; _i < 2; ++_i) \
;         __builtin_amdgcn_global_load_lds((const unsigned*)((const char*)(gbase) + (voff)[_i]), (PG8_LAS unsigned*)(lds + (bufoff) + ldsw + _i * 8192), 16, 0, 0); } while (0)
; #define PG8_LDA(dst, b, h) do { _Pragma("unroll") for (int m = 0; m < 4; ++m) _Pragma("unroll") for (int k = 0; k < 2; ++k) dst[m][k] = *(const PG8_LAS bf16x8*)(lds + PG8_SA(b, h) + aoff + m * 2048 + k * 1024); } while (0)
; #define PG8_LDB(dst, b, h) do { _Pragma("unroll") for (int n = 0; n < 2; ++n) _Pragma("unroll") for (int k = 0; k < 2; ++k) dst[n][k] = *(const PG8_LAS bf16x8*)(lds + PG8_SB(b, h) + boff + n * 2048 + k * 1024); } while (0)
; #define PG8_MMA(ai, bj, At, Bt) do { __builtin_amdgcn_s_setprio(1); _Pragma("unroll") for (int m = 0; m < 4; ++m) _Pragma("unroll") for (int n = 0; n < 2; ++n) _Pragma("unroll") for (int k = 0; k < 2; ++k) \
;         acc[ai][bj][m][n] = __builtin_amdgcn_mfma_f32_16x16x32_bf16(Bt[n][k], At[m][k], acc[ai][bj][m][n], 0, 0, 0); __builtin_amdgcn_s_setprio(0); } while (0)
; #define PG8_WAIT_V(n) asm volatile("s_waitcnt vmcnt(" #n ")" ::: "memory")
; #define PG8_WAIT_L(n) asm volatile("s_waitcnt lgkmcnt(" #n ")" ::: "memory")
; #define PG8_BAR __builtin_amdgcn_s_barrier()
; #define PG8_SCHED __builtin_amdgcn_sched_barrier(0)
; template <class Epi, class Sched, bool ALIGN_EPI = false, bool SP2 = false>
; __device__ __forceinline__ void gemm_phase(PG8_LAS unsigned char* lds, const Gemm g, const Sched& S, const Epi& E) {
;     ...
;             PG8_LDB(B0, 1, 0); PG8_LDB(B1, 1, 1); PG8_SCHED; PG8_LDA(At, 1, 0); PG8_STAGE(PG8_SA(0, 1), a2 + hstep, voffA);
;             PG8_WAIT_V(8); PG8_WAIT_L(0); PG8_BAR; PG8_MMA(0, 0, At, B0); PG8_MMA(0, 1, At, B1); PG8_BAR; PG8_SCHED;
	s_add_i32 s61, 0, 0x18000
	v_add_u32_e32 v2, s61, v203
	s_add_i32 s63, 0, 0x1c000
	ds_read_b128 v[132:135], v2
	ds_read_b128 v[136:139], v2 offset:1024
	ds_read_b128 v[140:143], v2 offset:2048
	ds_read_b128 v[144:147], v2 offset:3072
	v_add_u32_e32 v2, s63, v203
	ds_read_b128 v[148:151], v2
	ds_read_b128 v[152:155], v2 offset:1024
	ds_read_b128 v[156:159], v2 offset:2048
	ds_read_b128 v[160:163], v2 offset:3072
	s_add_u32 s10, s10, 0x40000
	s_addc_u32 s11, s11, 0
	s_mov_b32 m0, s31
	v_lshl_add_u64 v[236:237], s[10:11], 0, v[164:165]
	ds_read_b128 v[182:185], v206 offset:32768
	ds_read_b128 v[186:189], v206 offset:33792
	ds_read_b128 v[190:193], v206 offset:34816
	ds_read_b128 v[194:197], v206 offset:35840
	ds_read_b128 v[198:201], v206 offset:36864
	ds_read_b128 v[208:211], v206 offset:37888
	ds_read_b128 v[212:215], v206 offset:38912
	ds_read_b128 v[216:219], v206 offset:39936
	global_load_lds_dwordx4 v[236:237], off
	v_lshl_add_u64 v[236:237], s[10:11], 0, v[168:169]
	s_mov_b32 m0, s34
	s_nop 0
	global_load_lds_dwordx4 v[236:237], off
	s_waitcnt vmcnt(8)
	s_waitcnt lgkmcnt(0)
	s_barrier
	s_waitcnt lgkmcnt(0)
	v_mfma_f32_16x16x32_bf16 v[128:131], v[132:135], v[182:185], v[128:131]
	v_mfma_f32_16x16x32_bf16 v[124:127], v[140:143], v[182:185], v[124:127]
	v_mfma_f32_16x16x32_bf16 v[112:115], v[132:135], v[190:193], v[112:115]
	v_mfma_f32_16x16x32_bf16 v[108:111], v[140:143], v[190:193], v[108:111]
	v_mfma_f32_16x16x32_bf16 v[96:99], v[132:135], v[198:201], v[96:99]
	v_mfma_f32_16x16x32_bf16 v[92:95], v[140:143], v[198:201], v[92:95]
	v_mfma_f32_16x16x32_bf16 v[80:83], v[132:135], v[212:215], v[80:83]
	v_mfma_f32_16x16x32_bf16 v[76:79], v[140:143], v[212:215], v[76:79]
	v_mfma_f32_16x16x32_bf16 v[128:131], v[136:139], v[186:189], v[128:131]
	v_mfma_f32_16x16x32_bf16 v[124:127], v[144:147], v[186:189], v[124:127]
	v_mfma_f32_16x16x32_bf16 v[112:115], v[136:139], v[194:197], v[112:115]
	v_mfma_f32_16x16x32_bf16 v[108:111], v[144:147], v[194:197], v[108:111]
	v_mfma_f32_16x16x32_bf16 v[96:99], v[136:139], v[208:211], v[96:99]
	v_mfma_f32_16x16x32_bf16 v[92:95], v[144:147], v[208:211], v[92:95]
	v_mfma_f32_16x16x32_bf16 v[80:83], v[136:139], v[216:219], v[80:83]
	v_mfma_f32_16x16x32_bf16 v[76:79], v[144:147], v[216:219], v[76:79]
	v_mfma_f32_16x16x32_bf16 v[120:123], v[148:151], v[182:185], v[120:123]
	v_mfma_f32_16x16x32_bf16 v[116:119], v[156:159], v[182:185], v[116:119]
	v_mfma_f32_16x16x32_bf16 v[104:107], v[148:151], v[190:193], v[104:107]
	v_mfma_f32_16x16x32_bf16 v[100:103], v[156:159], v[190:193], v[100:103]
	v_mfma_f32_16x16x32_bf16 v[88:91], v[148:151], v[198:201], v[88:91]
	v_mfma_f32_16x16x32_bf16 v[84:87], v[156:159], v[198:201], v[84:87]
	v_mfma_f32_16x16x32_bf16 v[72:75], v[148:151], v[212:215], v[72:75]
	v_mfma_f32_16x16x32_bf16 v[68:71], v[156:159], v[212:215], v[68:71]
	v_mfma_f32_16x16x32_bf16 v[120:123], v[152:155], v[186:189], v[120:123]
	v_mfma_f32_16x16x32_bf16 v[116:119], v[160:163], v[186:189], v[116:119]
	v_mfma_f32_16x16x32_bf16 v[104:107], v[152:155], v[194:197], v[104:107]
	v_mfma_f32_16x16x32_bf16 v[100:103], v[160:163], v[194:197], v[100:103]
	v_mfma_f32_16x16x32_bf16 v[88:91], v[152:155], v[208:211], v[88:91]
	v_mfma_f32_16x16x32_bf16 v[84:87], v[160:163], v[208:211], v[84:87]
	v_mfma_f32_16x16x32_bf16 v[72:75], v[152:155], v[216:219], v[72:75]
	v_mfma_f32_16x16x32_bf16 v[68:71], v[160:163], v[216:219], v[68:71]
	s_barrier
; #define PG8_STAGE(bufoff, gbase, voff) do { _Pragma("unroll") for (int _i = 0; _i < 2; ++_i) \
;         __builtin_amdgcn_global_load_lds((const unsigned*)((const char*)(gbase) + (voff)[_i]), (PG8_LAS unsigned*)(lds + (bufoff) + ldsw + _i * 8192), 16, 0, 0); } while (0)
; #define PG8_LDA(dst, b, h) do { _Pragma("unroll") for (int m = 0; m < 4; ++m) _Pragma("unroll") for (int k = 0; k < 2; ++k) dst[m][k] = *(const PG8_LAS bf16x8*)(lds + PG8_SA(b, h) + aoff + m * 2048 + k * 1024); } while (0)
; #define PG8_BAR __builtin_amdgcn_s_barrier()
; template <class Epi, class Sched, bool ALIGN_EPI = false, bool SP2 = false>
; __device__ __forceinline__ void gemm_phase(PG8_LAS unsigned char* lds, const Gemm g, const Sched& S, const Epi& E) {
;     ...
;             PG8_LDA(At, 1, 1); PG8_STAGE(PG8_SB(1, 0), b3, voffB); PG8_STAGE(PG8_SB(1, 1), b3 + hstep, voffB); PG8_STAGE(PG8_SA(1, 0), a3, voffA);
;             PG8_WAIT_V(8); PG8_WAIT_L(0); PG8_BAR; if (cur.half == 0) { PG8_MMA(1, 0, At, B0); PG8_MMA(1, 1, At, B1); } PG8_BAR; PG8_SCHED;
;             } else {
;             PG8_LDB(B0, 0, 0); PG8_SCHED; PG8_LDA(At, 0, 0); PG8_STAGE(PG8_SA(1, 1), a1 + hstep, voffA);
;             PG8_WAIT_L(8); PG8_BAR; PG8_WAIT_L(0); PG8_MMA(0, 0, At, B0); PG8_BAR; PG8_SCHED;
;             PG8_LDB(B1, 0, 1); PG8_STAGE(PG8_SB(0, 0), b2, voffB);
;             PG8_BAR; PG8_WAIT_L(0); PG8_MMA(0, 1, At, B1); PG8_BAR;
;             PG8_LDA(At, 0, 1); PG8_STAGE(PG8_SA(0, 0), a2, voffA);
;             PG8_BAR; PG8_WAIT_L(0); PG8_MMA(1, 0, At, B0); PG8_BAR; PG8_SCHED;
;             PG8_STAGE(PG8_SB(0, 1), b2 + hstep, voffB);
;             PG8_WAIT_V(6); PG8_BAR; PG8_MMA(1, 1, At, B1); PG8_BAR;
;             PG8_LDB(B0, 1, 0); PG8_SCHED; PG8_LDA(At, 1, 0); PG8_STAGE(PG8_SA(0, 1), a2 + hstep, voffA);
;             PG8_WAIT_L(8); PG8_BAR; PG8_WAIT_L(0); PG8_MMA(0, 0, At, B0); PG8_BAR; PG8_SCHED;
;             PG8_LDB(B1, 1, 1); PG8_STAGE(PG8_SB(1, 0), b3, voffB);
;             PG8_BAR; PG8_WAIT_L(0); PG8_MMA(0, 1, At, B1); PG8_BAR;
;             PG8_LDA(At, 1, 1); PG8_STAGE(PG8_SA(1, 0), a3, voffA);
;             PG8_BAR; PG8_WAIT_L(0); PG8_MMA(1, 0, At, B0); PG8_BAR; PG8_SCHED;
;             PG8_STAGE(PG8_SB(1, 1), b3 + hstep, voffB);
;             PG8_WAIT_V(6); PG8_BAR; PG8_MMA(1, 1, At, B1); PG8_BAR;
;             }
;         }
;         if constexpr (ALIGN_EPI) { if (wr == 0) PG8_BAR; }
	s_add_i32 s10, s61, s27
	v_lshl_add_u64 v[228:229], v[228:229], 0, s[42:43]
	s_mov_b32 m0, s10
	ds_read_b128 v[182:185], v206 offset:49152
	ds_read_b128 v[186:189], v206 offset:50176
	ds_read_b128 v[190:193], v206 offset:51200
	ds_read_b128 v[194:197], v206 offset:52224
	ds_read_b128 v[198:201], v206 offset:53248
	ds_read_b128 v[208:211], v206 offset:54272
	ds_read_b128 v[212:215], v206 offset:55296
	ds_read_b128 v[216:219], v206 offset:56320
	global_load_lds_dwordx4 v[228:229], off
	s_add_i32 m0, s10, 0x2000
	s_add_u32 s0, s0, 0x40080
	v_lshl_add_u64 v[228:229], v[230:231], 0, s[42:43]
	s_addc_u32 s1, s1, 0
	s_add_i32 s10, s63, s27
	global_load_lds_dwordx4 v[228:229], off
	v_lshl_add_u64 v[228:229], s[0:1], 0, v[166:167]
	s_mov_b32 m0, s10
	s_nop 0
	global_load_lds_dwordx4 v[228:229], off
	v_lshl_add_u64 v[228:229], s[0:1], 0, v[170:171]
	s_add_i32 m0, s10, 0x2000
	s_nop 0
	global_load_lds_dwordx4 v[228:229], off
	v_lshl_add_u64 v[228:229], v[232:233], 0, s[42:43]
	s_mov_b32 m0, s41
	s_nop 0
	global_load_lds_dwordx4 v[228:229], off
	v_lshl_add_u64 v[228:229], v[234:235], 0, s[42:43]
	s_mov_b32 m0, s71
	s_nop 0
	global_load_lds_dwordx4 v[228:229], off
	s_waitcnt vmcnt(8)
	s_waitcnt lgkmcnt(0)
	s_barrier
	s_waitcnt lgkmcnt(0)
	v_mfma_f32_16x16x32_bf16 v[64:67], v[132:135], v[182:185], v[64:67]
	v_mfma_f32_16x16x32_bf16 v[60:63], v[140:143], v[182:185], v[60:63]
	v_mfma_f32_16x16x32_bf16 v[48:51], v[132:135], v[190:193], v[48:51]
	v_mfma_f32_16x16x32_bf16 v[44:47], v[140:143], v[190:193], v[44:47]
	v_mfma_f32_16x16x32_bf16 v[32:35], v[132:135], v[198:201], v[32:35]
	v_mfma_f32_16x16x32_bf16 v[28:31], v[140:143], v[198:201], v[28:31]
	v_mfma_f32_16x16x32_bf16 v[16:19], v[132:135], v[212:215], v[16:19]
	v_mfma_f32_16x16x32_bf16 v[12:15], v[140:143], v[212:215], v[12:15]
	v_mfma_f32_16x16x32_bf16 v[64:67], v[136:139], v[186:189], v[64:67]
	v_mfma_f32_16x16x32_bf16 v[60:63], v[144:147], v[186:189], v[60:63]
	v_mfma_f32_16x16x32_bf16 v[48:51], v[136:139], v[194:197], v[48:51]
	v_mfma_f32_16x16x32_bf16 v[44:47], v[144:147], v[194:197], v[44:47]
	v_mfma_f32_16x16x32_bf16 v[32:35], v[136:139], v[208:211], v[32:35]
	v_mfma_f32_16x16x32_bf16 v[28:31], v[144:147], v[208:211], v[28:31]
	v_mfma_f32_16x16x32_bf16 v[16:19], v[136:139], v[216:219], v[16:19]
	v_mfma_f32_16x16x32_bf16 v[12:15], v[144:147], v[216:219], v[12:15]
	v_mfma_f32_16x16x32_bf16 v[56:59], v[148:151], v[182:185], v[56:59]
	v_mfma_f32_16x16x32_bf16 v[52:55], v[156:159], v[182:185], v[52:55]
	v_mfma_f32_16x16x32_bf16 v[40:43], v[148:151], v[190:193], v[40:43]
	v_mfma_f32_16x16x32_bf16 v[36:39], v[156:159], v[190:193], v[36:39]
	v_mfma_f32_16x16x32_bf16 v[24:27], v[148:151], v[198:201], v[24:27]
	v_mfma_f32_16x16x32_bf16 v[20:23], v[156:159], v[198:201], v[20:23]
	v_mfma_f32_16x16x32_bf16 v[8:11], v[148:151], v[212:215], v[8:11]
	v_mfma_f32_16x16x32_bf16 v[4:7], v[156:159], v[212:215], v[4:7]
	v_mfma_f32_16x16x32_bf16 v[56:59], v[152:155], v[186:189], v[56:59]
	v_mfma_f32_16x16x32_bf16 v[52:55], v[160:163], v[186:189], v[52:55]
	v_mfma_f32_16x16x32_bf16 v[40:43], v[152:155], v[194:197], v[40:43]
	v_mfma_f32_16x16x32_bf16 v[36:39], v[160:163], v[194:197], v[36:39]
	v_mfma_f32_16x16x32_bf16 v[24:27], v[152:155], v[208:211], v[24:27]
	v_mfma_f32_16x16x32_bf16 v[20:23], v[160:163], v[208:211], v[20:23]
	v_mfma_f32_16x16x32_bf16 v[8:11], v[152:155], v[216:219], v[8:11]
	v_mfma_f32_16x16x32_bf16 v[4:7], v[160:163], v[216:219], v[4:7]
	s_barrier
	s_add_i32 s39, s39, 2
	s_add_u32 s8, s8, 0x100
	s_addc_u32 s9, s9, 0
	s_add_u32 s36, s36, 0x100
	s_addc_u32 s38, s38, 0
	s_cmp_gt_u32 s39, 13
	s_cbranch_scc0 .LBB0_395
	s_and_b64 vcc, exec, s[58:59]
	s_cbranch_vccz .LBB0_398
	s_barrier

; #define GAS __attribute__((address_space(1)))
; __device__ __forceinline__ unsigned xb_add(unsigned* p, unsigned v) { return __hip_atomic_fetch_add(p, v, __ATOMIC_RELAXED, __HIP_MEMORY_SCOPE_AGENT); }
; #define SEAM_LOCAL(k) do { if (IN(k) && IN((k) + 1)) { TBAR0(); xcd_barrier(bar, true, true); TBAR1(); } } while (0)
; __device__ __forceinline__ void xcd_barrier(const XcdBarrier& b, const bool group_local = false, const bool xcc_only = false) {
;     asm volatile("s_waitcnt vmcnt(0)" ::: "memory");
;     __syncthreads();
;     if (threadIdx.x == 0) {
;         GAS unsigned* barg = (GAS unsigned*)b.bar; asm volatile("" : "+s"(barg)); unsigned* bar = (unsigned*)barg;
;         __builtin_amdgcn_s_waitcnt(0);
;         unsigned nloc = b.st[0], nx = b.st[1];
;         if (nloc == 0u) { xcd_barrier_complete(bar, b.x, nloc, nx); b.st[0] = nloc; b.st[1] = nx; }
;         const unsigned old = xb_add(&bar[XB_XSUB(b.x)], 1u);
; __global__ void __launch_bounds__(NWAVES * 64, 2) mk_fwd(Args args) {
;     ...
;             SEAM_LOCAL(pb);
.LBB0_740:
	v_readlane_b32 s0, v255, 23
	s_add_i32 s22, s0, 2
	v_readlane_b32 s4, v255, 6
	v_readlane_b32 s5, v255, 7
	s_cmp_gt_i32 s4, s22
	s_cselect_b64 s[0:1], -1, 0
	s_cmp_ge_i32 s22, s5
	s_cselect_b64 s[4:5], -1, 0
	s_or_b64 s[0:1], s[0:1], s[4:5]
	s_and_b64 vcc, exec, s[0:1]
	s_cbranch_vccnz .LBB0_804
	s_waitcnt vmcnt(0)
	s_waitcnt vmcnt(0) lgkmcnt(0)
	s_barrier
	s_setprio 0
	s_mov_b64 s[14:15], exec
	v_readlane_b32 s0, v255, 43
	v_readlane_b32 s1, v255, 44
	s_and_b64 s[0:1], s[14:15], s[0:1]
	s_mov_b64 exec, s[0:1]
	s_cbranch_execz .LBB0_803
	v_readlane_b32 s0, v255, 10
	v_readlane_b32 s4, v255, 12
	v_readlane_b32 s1, v255, 11
	s_waitcnt vmcnt(0) expcnt(0) lgkmcnt(0)
	v_mov_b32_e32 v4, s4
	ds_read_b32 v2, v4
	ds_read_b32 v6, v4 offset:4
	s_waitcnt lgkmcnt(1)
	v_cmp_ne_u32_e32 vcc, 0, v2
	s_cbranch_vccnz .LBB0_757
	v_readlane_b32 s4, v255, 0
	v_readlane_b32 s5, v255, 1
	s_load_dwordx2 s[8:9], s[4:5], 0x4
	v_readlane_b32 s4, v255, 47
	s_lshl_b32 s4, s4, 2
	s_add_u32 s4, s0, s4
	s_addc_u32 s5, s1, 0
	s_add_u32 s6, s0, 0x1000
	s_addc_u32 s7, s1, 0
	s_waitcnt lgkmcnt(0)
	s_mul_i32 s23, s8, s33
	s_add_u32 s8, s0, 0x1100
	s_mul_i32 s23, s23, s9
	s_addc_u32 s9, s1, 0
	s_add_u32 s10, s0, 0x1200
	s_addc_u32 s11, s1, 0
	s_add_u32 s12, s0, 0x1300
	s_addc_u32 s13, s1, 0
	s_mov_b32 s24, 1
	s_branch .LBB0_745

; #define GAS __attribute__((address_space(1)))
; __device__ __forceinline__ unsigned xb_add(unsigned* p, unsigned v) { return __hip_atomic_fetch_add(p, v, __ATOMIC_RELAXED, __HIP_MEMORY_SCOPE_AGENT); }
; #define SEAM_LOCAL(k) do { if (IN(k) && IN((k) + 1)) { TBAR0(); xcd_barrier(bar, true, true); TBAR1(); } } while (0)
; __device__ __forceinline__ void xcd_barrier(const XcdBarrier& b, const bool group_local = false, const bool xcc_only = false) {
;     asm volatile("s_waitcnt vmcnt(0)" ::: "memory");
;     __syncthreads();
;     if (threadIdx.x == 0) {
;         GAS unsigned* barg = (GAS unsigned*)b.bar; asm volatile("" : "+s"(barg)); unsigned* bar = (unsigned*)barg;
;         __builtin_amdgcn_s_waitcnt(0);
;         unsigned nloc = b.st[0], nx = b.st[1];
;         if (nloc == 0u) { xcd_barrier_complete(bar, b.x, nloc, nx); b.st[0] = nloc; b.st[1] = nx; }
;         const unsigned old = xb_add(&bar[XB_XSUB(b.x)], 1u);
; __global__ void __launch_bounds__(NWAVES * 64, 2) mk_fwd(Args args) {
;     ...
;             SEAM_LOCAL(pb + 1);
.LBB0_1036:
	v_readlane_b32 s0, v255, 23
	s_add_i32 s22, s0, 3
	v_readlane_b32 s0, v255, 6
	v_readlane_b32 s1, v255, 7
	s_cmp_ge_i32 s22, s1
	s_cbranch_scc1 .LBB0_1048
	s_waitcnt vmcnt(0)
	s_waitcnt vmcnt(0)
	s_barrier
	s_setprio 0
	s_mov_b64 s[14:15], exec
	v_readlane_b32 s0, v255, 43
	v_readlane_b32 s1, v255, 44
	s_and_b64 s[0:1], s[14:15], s[0:1]
	v_readlane_b32 s77, v255, 52
	s_mov_b64 exec, s[0:1]
	s_cbranch_execz .LBB0_1112
	v_readlane_b32 s0, v255, 10
	v_readlane_b32 s4, v255, 12
	v_readlane_b32 s1, v255, 11
	s_waitcnt vmcnt(0) expcnt(0) lgkmcnt(0)
	v_mov_b32_e32 v4, s4
	ds_read_b32 v2, v4
	ds_read_b32 v6, v4 offset:4
	s_waitcnt lgkmcnt(1)
	v_cmp_ne_u32_e32 vcc, 0, v2
	s_cbranch_vccnz .LBB0_1054
	v_readlane_b32 s4, v255, 0
	v_readlane_b32 s5, v255, 1
	s_load_dwordx2 s[8:9], s[4:5], 0x4
	v_readlane_b32 s4, v255, 47
	s_lshl_b32 s4, s4, 2
	s_add_u32 s4, s0, s4
	s_addc_u32 s5, s1, 0
	s_add_u32 s6, s0, 0x1000
	s_addc_u32 s7, s1, 0
	s_waitcnt lgkmcnt(0)
	s_mul_i32 s23, s8, s33
	s_add_u32 s8, s0, 0x1100
	s_mul_i32 s23, s23, s9
	s_addc_u32 s9, s1, 0
	s_add_u32 s10, s0, 0x1200
	s_addc_u32 s11, s1, 0
	s_add_u32 s12, s0, 0x1300
	s_addc_u32 s13, s1, 0
	s_mov_b32 s24, 1
	s_branch .LBB0_1041

;     __device__ __forceinline__ void a_ready(const Unit&) const { if (++ncall == 3 && sig != nullptr && threadIdx.x == 0) __hip_atomic_fetch_add(sig, 1u, __ATOMIC_RELAXED, __HIP_MEMORY_SCOPE_AGENT); }
; __device__ __forceinline__ f32x4 load_row_partials(const float* rsp, int pm, int tid) { f32x4 p = {0.f, 0.f, 0.f, 0.f}; if (tid < BM) p = *(const f32x4*)(rsp + (size_t)(pm * BM + tid) * 4); return p; }
; #define PG8_BAR __builtin_amdgcn_s_barrier()
; template <class Epi, class Sched, bool ALIGN_EPI = false, bool SP2 = false>
; __device__ __forceinline__ void gemm_phase(PG8_LAS unsigned char* lds, const Gemm g, const Sched& S, const Epi& E) {
;     ...
;     for (int i = 0; i < 2; ++i) { int R, C; stage_rc(tid * 16 + i * 8192, R, C); const int Rb = Epi::PERM ? ((R & ~31) + perm32(R & 31)) : R;
;         voffA[i] = (unsigned)(R * K + C) * 2u; voffB[i] = (unsigned)(Rb * K + C) * 2u; }
;     const size_t kstep = (size_t)(BK * 2);
;     const size_t hstep = (size_t)HALF * K * 2;
;     const size_t tstep = 2 * hstep;
;     const unsigned ldsw = (unsigned)wid * 1024u;
;     const int aoff = lds_byte(wr * 64 + fr, fq * 8), boff = lds_byte(wc * 32 + fr, fq * 8);
;     ...
;     Unit cur, nxt; int ui = 0;
;     ...
;     unsigned pg8_probe_acc = 0u;
;     ...
;     if (!S.next(0, cur)) return;
;     ...
;     const unsigned long long tramp_ = __builtin_amdgcn_s_memrealtime();
;     ...
;     static_assert(!Epi::ROWSCALE || SP2, "row factors are staged in the SP2 prologue");
;     f32x4 rowp_ = {0.f, 0.f, 0.f, 0.f}; if constexpr (Epi::ROWSCALE) rowp_ = load_row_partials(E.rsp, cur.pm, tid);
;     f32x4 acc[2][2][4][2];
; #pragma unroll
;     for (int a = 0; a < 2; ++a)
; #pragma unroll
;         for (int b = 0; b < 2; ++b)
; #pragma unroll
;             for (int m = 0; m < 4; ++m)
; #pragma unroll
;                 for (int n = 0; n < 2; ++n) acc[a][b][m][n] = (f32x4){0.f, 0.f, 0.f, 0.f};
;     bf16x8 At[4][2], B0[2][2], B1[2][2];
;     const char* cA = (const char*)g.A + (size_t)cur.pm * tstep + (cur.half == 2 ? hstep : (size_t)0); const char* cB = (const char*)g.Bt + (size_t)cur.pn * tstep;
;     S.a_ready(cur);
;     if constexpr (SP2) {
;         PG8_STAGE(PG8_SB(0, 0), cB, voffB); PG8_STAGE(PG8_SB(0, 1), cB + hstep, voffB); PG8_STAGE(PG8_SA(0, 0), cA, voffA); PG8_STAGE(PG8_SA(0, 1), cA + hstep, voffA);
;         if (wr == 1) PG8_BAR;
.LBB0_1122:
	s_andn2_b64 vcc, exec, s[6:7]
	s_cbranch_vccnz .LBB0_1206
	v_ashrrev_i32_e32 v2, 31, v12
	v_lshrrev_b32_e32 v2, 26, v2
	v_add_u32_e32 v2, v12, v2
	v_ashrrev_i32_e32 v13, 6, v2
	v_bfe_i32 v2, v12, 27, 1
	v_lshlrev_b32_e32 v4, 4, v12
	v_lshrrev_b32_e32 v2, 22, v2
	v_add_u32_e32 v2, v4, v2
	v_and_b32_e32 v2, 0xfffffc00, v2
	v_sub_u32_e32 v2, v4, v2
	v_lshrrev_b32_e32 v5, 4, v2
	v_bitop3_b32 v2, v5, v2, 32 bitop3:0x6c
	s_mul_i32 s36, s77, 0xee0000
	v_ashrrev_i32_e32 v6, 31, v2
	s_lshl_b64 s[6:7], s[36:37], 1
	v_lshrrev_b32_e32 v6, 26, v6
	s_add_u32 s1, s12, s6
	v_add_u32_e32 v6, v2, v6
	s_addc_u32 s5, s13, s7
	v_lshlrev_b32_e32 v5, 3, v13
	v_ashrrev_i32_e32 v14, 6, v6
	v_and_b32_e32 v6, 0xc0, v6
	s_add_u32 s23, s12, 0xa000000
	v_and_b32_e32 v5, -16, v5
	v_sub_u32_e32 v2, v2, v6
	s_addc_u32 s24, s13, 0
	v_add_u32_e32 v5, v14, v5
	v_ashrrev_i16_sdwa v2, v224, sext(v2) dst_sel:DWORD dst_unused:UNUSED_PAD src0_sel:DWORD src1_sel:BYTE_0
	s_add_u32 s25, s1, 0x1100000
	v_lshlrev_b32_e32 v7, 5, v13
	v_bfe_i32 v15, v2, 0, 16
	v_lshlrev_b32_e32 v2, 1, v5
	v_lshrrev_b32_e32 v6, 2, v5
	v_and_b32_e32 v8, 3, v14
	s_mov_b32 s1, 0x3fffe0
	v_and_b32_e32 v7, 32, v7
	v_and_b32_e32 v2, 24, v2
	v_and_b32_e32 v6, 4, v6
	v_and_or_b32 v8, v5, s1, v8
	v_or3_b32 v2, v8, v6, v2
	v_add_lshl_u32 v6, v7, v15, 1
	v_add_u32_e32 v4, 0x2000, v4
	v_lshl_add_u32 v164, v5, 10, v6
	v_ashrrev_i32_e32 v5, 31, v4
	v_lshrrev_b32_e32 v5, 22, v5
	v_add_u32_e32 v5, v4, v5
	v_ashrrev_i32_e32 v16, 10, v5
	v_mul_i32_i24_e32 v5, 0x400, v16
	v_sub_u32_e32 v4, v4, v5
	v_lshrrev_b32_e32 v5, 4, v4
	v_bitop3_b32 v4, v5, v4, 32 bitop3:0x6c
	v_lshl_add_u32 v2, v2, 10, v6
	v_ashrrev_i32_e32 v6, 31, v4
	v_lshrrev_b32_e32 v6, 26, v6
	v_lshlrev_b32_e32 v5, 3, v16
	v_add_u32_e32 v6, v4, v6
	v_and_b32_e32 v5, -16, v5
	v_ashrrev_i32_e32 v17, 6, v6
	v_add_u32_e32 v5, v17, v5
	v_and_b32_e32 v8, 3, v17
	s_addc_u32 s26, s5, 0
	v_and_b32_e32 v6, 0xc0, v6
	v_and_or_b32 v8, v5, s1, v8
	s_ashr_i32 s18, s16, 6
	s_ashr_i32 s5, s4, 31
	s_ashr_i32 s1, s0, 31
	s_ashr_i32 s17, s16, 8
	v_sub_u32_e32 v4, v4, v6
	s_lshl_b32 s27, s18, 10
	s_lshl_b64 s[6:7], s[4:5], 18
	s_lshl_b64 s[8:9], s[0:1], 18
	v_ashrrev_i16_sdwa v4, v224, sext(v4) dst_sel:DWORD dst_unused:UNUSED_PAD src0_sel:DWORD src1_sel:BYTE_0
	s_add_u32 s14, s25, s8
	v_lshlrev_b32_e32 v7, 5, v16
	v_bfe_i32 v18, v4, 0, 16
	v_lshlrev_b32_e32 v4, 1, v5
	v_lshrrev_b32_e32 v6, 2, v5
	s_addc_u32 s15, s26, s9
	s_add_i32 s28, s27, 0
	v_and_b32_e32 v7, 32, v7
	v_and_b32_e32 v4, 24, v4
	v_and_b32_e32 v6, 4, v6
	s_add_i32 m0, s28, 0x10000
	v_or3_b32 v4, v8, v6, v4
	v_add_lshl_u32 v6, v7, v18, 1
	global_load_lds_dwordx4 v2, s[14:15]
	s_add_i32 m0, s28, 0x12000
	v_lshl_add_u32 v168, v4, 10, v6
	s_add_u32 s8, s14, 0x20000
	global_load_lds_dwordx4 v168, s[14:15]
	s_addc_u32 s9, s15, 0
	s_add_i32 m0, s28, 0x14000
	v_lshl_add_u32 v166, v5, 10, v6
	global_load_lds_dwordx4 v2, s[8:9]
	s_add_i32 m0, s28, 0x16000
	s_add_u32 s6, s23, s6
	s_addc_u32 s7, s24, s7
	s_add_i32 s29, s28, 0x2000
	global_load_lds_dwordx4 v168, s[8:9]
	s_mov_b32 m0, s28
	s_add_u32 s8, s6, 0x20000
	global_load_lds_dwordx4 v164, s[6:7]
	s_mov_b32 m0, s29
	s_addc_u32 s9, s7, 0
	s_add_i32 s30, s28, 0x4000
	global_load_lds_dwordx4 v166, s[6:7]
	s_mov_b32 m0, s30
	s_add_i32 s31, s28, 0x6000
	global_load_lds_dwordx4 v164, s[8:9]
	s_mov_b32 m0, s31
	v_mov_b32_e32 v169, v3
	global_load_lds_dwordx4 v166, s[8:9]
	v_mov_b32_e32 v165, v3
	v_mov_b32_e32 v167, v3
	s_cmp_eq_u32 s17, 1
	v_lshl_add_u64 v[10:11], s[14:15], 0, v[2:3]
	v_lshl_add_u64 v[8:9], s[14:15], 0, v[168:169]
	v_lshl_add_u64 v[4:5], s[6:7], 0, v[164:165]
	s_cselect_b64 s[8:9], -1, 0
	s_cmp_lg_u32 s17, 1
	v_lshl_add_u64 v[6:7], s[6:7], 0, v[166:167]
	s_cbranch_scc1 .LBB0_1125
	s_setprio 1
	s_barrier

; #define PG8_STAGE(bufoff, gbase, voff) do { _Pragma("unroll") for (int _i = 0; _i < 2; ++_i) \
;         __builtin_amdgcn_global_load_lds((const unsigned*)((const char*)(gbase) + (voff)[_i]), (PG8_LAS unsigned*)(lds + (bufoff) + ldsw + _i * 8192), 16, 0, 0); } while (0)
; #define PG8_LDA(dst, b, h) do { _Pragma("unroll") for (int m = 0; m < 4; ++m) _Pragma("unroll") for (int k = 0; k < 2; ++k) dst[m][k] = *(const PG8_LAS bf16x8*)(lds + PG8_SA(b, h) + aoff + m * 2048 + k * 1024); } while (0)
; #define PG8_LDB(dst, b, h) do { _Pragma("unroll") for (int n = 0; n < 2; ++n) _Pragma("unroll") for (int k = 0; k < 2; ++k) dst[n][k] = *(const PG8_LAS bf16x8*)(lds + PG8_SB(b, h) + boff + n * 2048 + k * 1024); } while (0)
; #define PG8_MMA(ai, bj, At, Bt) do { __builtin_amdgcn_s_setprio(1); _Pragma("unroll") for (int m = 0; m < 4; ++m) _Pragma("unroll") for (int n = 0; n < 2; ++n) _Pragma("unroll") for (int k = 0; k < 2; ++k) \
;         acc[ai][bj][m][n] = __builtin_amdgcn_mfma_f32_16x16x32_bf16(Bt[n][k], At[m][k], acc[ai][bj][m][n], 0, 0, 0); __builtin_amdgcn_s_setprio(0); } while (0)
; #define PG8_WAIT_V(n) asm volatile("s_waitcnt vmcnt(" #n ")" ::: "memory")
; #define PG8_WAIT_L(n) asm volatile("s_waitcnt lgkmcnt(" #n ")" ::: "memory")
; #define PG8_BAR __builtin_amdgcn_s_barrier()
; #define PG8_SCHED __builtin_amdgcn_sched_barrier(0)
; template <class Epi, class Sched, bool ALIGN_EPI = false, bool SP2 = false>
; __device__ __forceinline__ void gemm_phase(PG8_LAS unsigned char* lds, const Gemm g, const Sched& S, const Epi& E) {
;     ...
;             PG8_LDB(B0, 0, 0); PG8_LDB(B1, 0, 1); PG8_SCHED; PG8_LDA(At, 0, 0); PG8_STAGE(PG8_SA(1, 1), a1 + hstep, voffA);
;     ...
;             if (PROBE_KIND == 18 && t == 0 && ui > 0 && g.probe) { const unsigned long long tq_ = __builtin_amdgcn_s_memrealtime(); PG8_WAIT_V(8); pg8_probe_acc += (unsigned)(__builtin_amdgcn_s_memrealtime() - tq_); }
;     ...
;             PG8_WAIT_V(8); PG8_WAIT_L(0); PG8_BAR; PG8_MMA(0, 0, At, B0); PG8_MMA(0, 1, At, B1); PG8_BAR; PG8_SCHED;
;             PG8_LDA(At, 0, 1); PG8_STAGE(PG8_SB(0, 0), b2, voffB); PG8_STAGE(PG8_SB(0, 1), b2 + hstep, voffB); PG8_STAGE(PG8_SA(0, 0), a2, voffA);
;             PG8_WAIT_V(8); PG8_WAIT_L(0); PG8_BAR; if (cur.half == 0) { PG8_MMA(1, 0, At, B0); PG8_MMA(1, 1, At, B1); } PG8_BAR; PG8_SCHED;
.LBB0_1135:
	s_add_u32 s14, s6, 0xfffe0080
	s_addc_u32 s15, s7, -1
	s_add_i32 s65, 0, 0x10000
	s_cmp_eq_u32 s64, 4
	s_cselect_b32 s21, s1, s15
	s_cselect_b32 s20, s5, s14
	s_cselect_b32 s15, s19, s63
	s_cselect_b32 s14, s39, s62
	s_add_i32 s68, 0, 0x14000
	v_add_u32_e32 v72, s65, v201
	v_add_u32_e32 v136, s68, v201
	ds_read_b128 v[36:39], v72
	ds_read_b128 v[40:43], v72 offset:1024
	ds_read_b128 v[68:71], v72 offset:2048
	ds_read_b128 v[72:75], v72 offset:3072
	ds_read_b128 v[100:103], v136
	ds_read_b128 v[104:107], v136 offset:1024
	ds_read_b128 v[132:135], v136 offset:2048
	ds_read_b128 v[136:139], v136 offset:3072
	v_lshl_add_u64 v[198:199], s[6:7], 0, v[170:171]
	s_add_i32 m0, s28, 0xc000
	ds_read_b128 v[174:177], v203
	ds_read_b128 v[178:181], v203 offset:1024
	ds_read_b128 v[182:185], v203 offset:2048
	ds_read_b128 v[186:189], v203 offset:3072
	ds_read_b128 v[190:193], v203 offset:4096
	ds_read_b128 v[194:197], v203 offset:5120
	ds_read_b128 v[204:207], v203 offset:6144
	ds_read_b128 v[208:211], v203 offset:7168
	global_load_lds_dwordx4 v[198:199], off
	v_lshl_add_u64 v[198:199], s[6:7], 0, v[172:173]
	s_add_i32 m0, s28, 0xe000
	s_nop 0
	global_load_lds_dwordx4 v[198:199], off
	s_waitcnt vmcnt(8)
	s_waitcnt lgkmcnt(0)
	s_barrier
	s_waitcnt lgkmcnt(0)
	v_mfma_f32_16x16x32_bf16 v[56:59], v[36:39], v[174:177], v[56:59]
	v_mfma_f32_16x16x32_bf16 v[52:55], v[68:71], v[174:177], v[52:55]
	v_mfma_f32_16x16x32_bf16 v[88:91], v[36:39], v[182:185], v[88:91]
	v_mfma_f32_16x16x32_bf16 v[84:87], v[68:71], v[182:185], v[84:87]
	v_mfma_f32_16x16x32_bf16 v[120:123], v[36:39], v[190:193], v[120:123]
	v_mfma_f32_16x16x32_bf16 v[116:119], v[68:71], v[190:193], v[116:119]
	v_mfma_f32_16x16x32_bf16 v[128:131], v[36:39], v[204:207], v[128:131]
	v_mfma_f32_16x16x32_bf16 v[124:127], v[68:71], v[204:207], v[124:127]
	v_mfma_f32_16x16x32_bf16 v[56:59], v[40:43], v[178:181], v[56:59]
	v_mfma_f32_16x16x32_bf16 v[52:55], v[72:75], v[178:181], v[52:55]
	v_mfma_f32_16x16x32_bf16 v[88:91], v[40:43], v[186:189], v[88:91]
	v_mfma_f32_16x16x32_bf16 v[84:87], v[72:75], v[186:189], v[84:87]
	v_mfma_f32_16x16x32_bf16 v[120:123], v[40:43], v[194:197], v[120:123]
	v_mfma_f32_16x16x32_bf16 v[116:119], v[72:75], v[194:197], v[116:119]
	v_mfma_f32_16x16x32_bf16 v[128:131], v[40:43], v[208:211], v[128:131]
	v_mfma_f32_16x16x32_bf16 v[124:127], v[72:75], v[208:211], v[124:127]
	v_mfma_f32_16x16x32_bf16 v[160:163], v[100:103], v[174:177], v[160:163]
	v_mfma_f32_16x16x32_bf16 v[156:159], v[132:135], v[174:177], v[156:159]
	v_mfma_f32_16x16x32_bf16 v[152:155], v[100:103], v[182:185], v[152:155]
	v_mfma_f32_16x16x32_bf16 v[148:151], v[132:135], v[182:185], v[148:151]
	v_mfma_f32_16x16x32_bf16 v[144:147], v[100:103], v[190:193], v[144:147]
	v_mfma_f32_16x16x32_bf16 v[140:143], v[132:135], v[190:193], v[140:143]
	v_mfma_f32_16x16x32_bf16 v[112:115], v[100:103], v[204:207], v[112:115]
	v_mfma_f32_16x16x32_bf16 v[108:111], v[132:135], v[204:207], v[108:111]
	v_mfma_f32_16x16x32_bf16 v[160:163], v[104:107], v[178:181], v[160:163]
	v_mfma_f32_16x16x32_bf16 v[156:159], v[136:139], v[178:181], v[156:159]
	v_mfma_f32_16x16x32_bf16 v[152:155], v[104:107], v[186:189], v[152:155]
	v_mfma_f32_16x16x32_bf16 v[148:151], v[136:139], v[186:189], v[148:151]
	v_mfma_f32_16x16x32_bf16 v[144:147], v[104:107], v[194:197], v[144:147]
	v_mfma_f32_16x16x32_bf16 v[140:143], v[136:139], v[194:197], v[140:143]
	v_mfma_f32_16x16x32_bf16 v[112:115], v[104:107], v[208:211], v[112:115]
	v_mfma_f32_16x16x32_bf16 v[108:111], v[136:139], v[208:211], v[108:111]
	s_barrier
	s_add_i32 s65, s65, s27
	v_lshl_add_u64 v[198:199], s[14:15], 0, v[2:3]
	s_mov_b32 m0, s65
	ds_read_b128 v[174:177], v203 offset:16384
	ds_read_b128 v[178:181], v203 offset:17408
	ds_read_b128 v[182:185], v203 offset:18432
	ds_read_b128 v[186:189], v203 offset:19456
	ds_read_b128 v[190:193], v203 offset:20480
	ds_read_b128 v[194:197], v203 offset:21504
	ds_read_b128 v[204:207], v203 offset:22528
	ds_read_b128 v[208:211], v203 offset:23552
	global_load_lds_dwordx4 v[198:199], off
	s_add_i32 m0, s65, 0x2000
	s_add_u32 s66, s14, 0x20000
	v_lshl_add_u64 v[212:213], s[14:15], 0, v[168:169]
	s_addc_u32 s67, s15, 0
	s_add_i32 s65, s68, s27
	global_load_lds_dwordx4 v[212:213], off
	v_lshl_add_u64 v[214:215], s[66:67], 0, v[2:3]
	s_mov_b32 m0, s65
	v_lshl_add_u64 v[216:217], s[20:21], 0, v[166:167]
	global_load_lds_dwordx4 v[214:215], off
	v_lshl_add_u64 v[214:215], s[66:67], 0, v[168:169]
	s_add_i32 m0, s65, 0x2000
	s_nop 0
	global_load_lds_dwordx4 v[214:215], off
	v_lshl_add_u64 v[214:215], s[20:21], 0, v[164:165]
	s_mov_b32 m0, s28
	s_nop 0
	global_load_lds_dwordx4 v[214:215], off
	s_mov_b32 m0, s29
	s_nop 0
	global_load_lds_dwordx4 v[216:217], off
	s_waitcnt vmcnt(8)
	s_waitcnt lgkmcnt(0)
	s_barrier
; #define PG8_STAGE(bufoff, gbase, voff) do { _Pragma("unroll") for (int _i = 0; _i < 2; ++_i) \
;         __builtin_amdgcn_global_load_lds((const unsigned*)((const char*)(gbase) + (voff)[_i]), (PG8_LAS unsigned*)(lds + (bufoff) + ldsw + _i * 8192), 16, 0, 0); } while (0)
; #define PG8_LDA(dst, b, h) do { _Pragma("unroll") for (int m = 0; m < 4; ++m) _Pragma("unroll") for (int k = 0; k < 2; ++k) dst[m][k] = *(const PG8_LAS bf16x8*)(lds + PG8_SA(b, h) + aoff + m * 2048 + k * 1024); } while (0)
; #define PG8_LDB(dst, b, h) do { _Pragma("unroll") for (int n = 0; n < 2; ++n) _Pragma("unroll") for (int k = 0; k < 2; ++k) dst[n][k] = *(const PG8_LAS bf16x8*)(lds + PG8_SB(b, h) + boff + n * 2048 + k * 1024); } while (0)
; #define PG8_MMA(ai, bj, At, Bt) do { __builtin_amdgcn_s_setprio(1); _Pragma("unroll") for (int m = 0; m < 4; ++m) _Pragma("unroll") for (int n = 0; n < 2; ++n) _Pragma("unroll") for (int k = 0; k < 2; ++k) \
;         acc[ai][bj][m][n] = __builtin_amdgcn_mfma_f32_16x16x32_bf16(Bt[n][k], At[m][k], acc[ai][bj][m][n], 0, 0, 0); __builtin_amdgcn_s_setprio(0); } while (0)
; #define PG8_WAIT_V(n) asm volatile("s_waitcnt vmcnt(" #n ")" ::: "memory")
; #define PG8_WAIT_L(n) asm volatile("s_waitcnt lgkmcnt(" #n ")" ::: "memory")
; #define PG8_BAR __builtin_amdgcn_s_barrier()
; #define PG8_SCHED __builtin_amdgcn_sched_barrier(0)
; template <class Epi, class Sched, bool ALIGN_EPI = false, bool SP2 = false>
; __device__ __forceinline__ void gemm_phase(PG8_LAS unsigned char* lds, const Gemm g, const Sched& S, const Epi& E) {
;     ...
;             PG8_WAIT_V(8); PG8_WAIT_L(0); PG8_BAR; if (cur.half == 0) { PG8_MMA(1, 0, At, B0); PG8_MMA(1, 1, At, B1); } PG8_BAR; PG8_SCHED;
;             PG8_LDB(B0, 1, 0); PG8_LDB(B1, 1, 1); PG8_SCHED; PG8_LDA(At, 1, 0); PG8_STAGE(PG8_SA(0, 1), a2 + hstep, voffA);
;             PG8_WAIT_V(8); PG8_WAIT_L(0); PG8_BAR; PG8_MMA(0, 0, At, B0); PG8_MMA(0, 1, At, B1); PG8_BAR; PG8_SCHED;
	s_waitcnt lgkmcnt(0)
	v_mfma_f32_16x16x32_bf16 v[96:99], v[36:39], v[174:177], v[96:99]
	v_mfma_f32_16x16x32_bf16 v[92:95], v[68:71], v[174:177], v[92:95]
	v_mfma_f32_16x16x32_bf16 v[64:67], v[36:39], v[182:185], v[64:67]
	v_mfma_f32_16x16x32_bf16 v[60:63], v[68:71], v[182:185], v[60:63]
	v_mfma_f32_16x16x32_bf16 v[32:35], v[36:39], v[190:193], v[32:35]
	v_mfma_f32_16x16x32_bf16 v[28:31], v[68:71], v[190:193], v[28:31]
	v_mfma_f32_16x16x32_bf16 v[16:19], v[36:39], v[204:207], v[16:19]
	v_mfma_f32_16x16x32_bf16 v[12:15], v[68:71], v[204:207], v[12:15]
	v_mfma_f32_16x16x32_bf16 v[96:99], v[40:43], v[178:181], v[96:99]
	v_mfma_f32_16x16x32_bf16 v[92:95], v[72:75], v[178:181], v[92:95]
	v_mfma_f32_16x16x32_bf16 v[64:67], v[40:43], v[186:189], v[64:67]
	v_mfma_f32_16x16x32_bf16 v[60:63], v[72:75], v[186:189], v[60:63]
	v_mfma_f32_16x16x32_bf16 v[32:35], v[40:43], v[194:197], v[32:35]
	v_mfma_f32_16x16x32_bf16 v[28:31], v[72:75], v[194:197], v[28:31]
	v_mfma_f32_16x16x32_bf16 v[16:19], v[40:43], v[208:211], v[16:19]
	v_mfma_f32_16x16x32_bf16 v[12:15], v[72:75], v[208:211], v[12:15]
	v_mfma_f32_16x16x32_bf16 v[48:51], v[100:103], v[182:185], v[48:51]
	v_mfma_f32_16x16x32_bf16 v[44:47], v[132:135], v[182:185], v[44:47]
	v_mfma_f32_16x16x32_bf16 v[24:27], v[100:103], v[190:193], v[24:27]
	v_mfma_f32_16x16x32_bf16 v[20:23], v[132:135], v[190:193], v[20:23]
	v_mfma_f32_16x16x32_bf16 v[8:11], v[100:103], v[204:207], v[8:11]
	v_mfma_f32_16x16x32_bf16 v[4:7], v[132:135], v[204:207], v[4:7]
	v_mfma_f32_16x16x32_bf16 v[36:39], v[100:103], v[174:177], v[80:83]
	v_mfma_f32_16x16x32_bf16 v[40:43], v[132:135], v[174:177], v[76:79]
	v_mfma_f32_16x16x32_bf16 v[48:51], v[104:107], v[186:189], v[48:51]
	v_mfma_f32_16x16x32_bf16 v[44:47], v[136:139], v[186:189], v[44:47]
	v_mfma_f32_16x16x32_bf16 v[24:27], v[104:107], v[194:197], v[24:27]
	v_mfma_f32_16x16x32_bf16 v[20:23], v[136:139], v[194:197], v[20:23]
	v_mfma_f32_16x16x32_bf16 v[8:11], v[104:107], v[208:211], v[8:11]
	v_mfma_f32_16x16x32_bf16 v[4:7], v[136:139], v[208:211], v[4:7]
	v_mfma_f32_16x16x32_bf16 v[36:39], v[104:107], v[178:181], v[36:39]
	v_mfma_f32_16x16x32_bf16 v[40:43], v[136:139], v[178:181], v[40:43]
	s_barrier
	s_add_i32 s65, 0, 0x18000
	s_add_i32 s66, 0, 0x1c000
	v_add_u32_e32 v80, s65, v201
	v_add_u32_e32 v136, s66, v201
	ds_read_b128 v[68:71], v80
	ds_read_b128 v[72:75], v80 offset:1024
	ds_read_b128 v[76:79], v80 offset:2048
	ds_read_b128 v[80:83], v80 offset:3072
	ds_read_b128 v[100:103], v136
	ds_read_b128 v[104:107], v136 offset:1024
	ds_read_b128 v[132:135], v136 offset:2048
	ds_read_b128 v[136:139], v136 offset:3072
	s_add_u32 s20, s20, 0x20000
	s_addc_u32 s21, s21, 0
	s_mov_b32 m0, s30
	v_lshl_add_u64 v[218:219], s[20:21], 0, v[164:165]
	ds_read_b128 v[174:177], v203 offset:32768
	ds_read_b128 v[178:181], v203 offset:33792
	ds_read_b128 v[182:185], v203 offset:34816
	ds_read_b128 v[186:189], v203 offset:35840
	ds_read_b128 v[190:193], v203 offset:36864
	ds_read_b128 v[194:197], v203 offset:37888
	ds_read_b128 v[204:207], v203 offset:38912
	ds_read_b128 v[208:211], v203 offset:39936
	global_load_lds_dwordx4 v[218:219], off
	v_lshl_add_u64 v[218:219], s[20:21], 0, v[166:167]
	s_mov_b32 m0, s31
	s_nop 0
	global_load_lds_dwordx4 v[218:219], off
	s_waitcnt vmcnt(8)
	s_waitcnt lgkmcnt(0)
	s_barrier
; #define MG_LOAD(c, buf) do { _Pragma("unroll") for (int m2 = 0; m2 < 2; ++m2) _Pragma("unroll") for (int bj = 0; bj < 2; ++bj) { \
;             const size_t ro = (size_t)(row0 + ((c) >> 1) * HALF + (2 * ((c) & 1) + m2) * 16) * DM + col0 + bj * HALF; ga[buf][m2][bj] = *(const u32x2*)(GAx + (ro & amask)); gb[buf][m2][bj] = *(const u32x2*)(GB + ro); } } while (0)
; #define PG8_STAGE(bufoff, gbase, voff) do { _Pragma("unroll") for (int _i = 0; _i < 2; ++_i) \
;         __builtin_amdgcn_global_load_lds((const unsigned*)((const char*)(gbase) + (voff)[_i]), (PG8_LAS unsigned*)(lds + (bufoff) + ldsw + _i * 8192), 16, 0, 0); } while (0)
; #define PG8_LDA(dst, b, h) do { _Pragma("unroll") for (int m = 0; m < 4; ++m) _Pragma("unroll") for (int k = 0; k < 2; ++k) dst[m][k] = *(const PG8_LAS bf16x8*)(lds + PG8_SA(b, h) + aoff + m * 2048 + k * 1024); } while (0)
; #define PG8_MMA(ai, bj, At, Bt) do { __builtin_amdgcn_s_setprio(1); _Pragma("unroll") for (int m = 0; m < 4; ++m) _Pragma("unroll") for (int n = 0; n < 2; ++n) _Pragma("unroll") for (int k = 0; k < 2; ++k) \
;         acc[ai][bj][m][n] = __builtin_amdgcn_mfma_f32_16x16x32_bf16(Bt[n][k], At[m][k], acc[ai][bj][m][n], 0, 0, 0); __builtin_amdgcn_s_setprio(0); } while (0)
; #define PG8_WAIT_V(n) asm volatile("s_waitcnt vmcnt(" #n ")" ::: "memory")
; #define PG8_WAIT_L(n) asm volatile("s_waitcnt lgkmcnt(" #n ")" ::: "memory")
; #define PG8_BAR __builtin_amdgcn_s_barrier()
; #define PG8_SCHED __builtin_amdgcn_sched_barrier(0)
;     __device__ __forceinline__ void operator()(f32x4 (&acc)[2][2][4][2], const Unit& u, int wr, int wc, int fr, int fq) const {
;     ...
;         MG_LOAD(0, 0); MG_LOAD(1, 1);
; template <class Epi, class Sched, bool ALIGN_EPI = false, bool SP2 = false>
; __device__ __forceinline__ void gemm_phase(PG8_LAS unsigned char* lds, const Gemm g, const Sched& S, const Epi& E) {
;     ...
;             PG8_WAIT_V(8); PG8_WAIT_L(0); PG8_BAR; PG8_MMA(0, 0, At, B0); PG8_MMA(0, 1, At, B1); PG8_BAR; PG8_SCHED;
;             PG8_LDA(At, 1, 1); PG8_STAGE(PG8_SB(1, 0), b3, voffB); PG8_STAGE(PG8_SB(1, 1), b3 + hstep, voffB); PG8_STAGE(PG8_SA(1, 0), a3, voffA);
;             PG8_WAIT_V(8); PG8_WAIT_L(0); PG8_BAR; if (cur.half == 0) { PG8_MMA(1, 0, At, B0); PG8_MMA(1, 1, At, B1); } PG8_BAR; PG8_SCHED;
	s_waitcnt lgkmcnt(0)
	v_mfma_f32_16x16x32_bf16 v[56:59], v[68:71], v[174:177], v[56:59]
	v_mfma_f32_16x16x32_bf16 v[52:55], v[76:79], v[174:177], v[52:55]
	v_mfma_f32_16x16x32_bf16 v[88:91], v[68:71], v[182:185], v[88:91]
	v_mfma_f32_16x16x32_bf16 v[84:87], v[76:79], v[182:185], v[84:87]
	v_mfma_f32_16x16x32_bf16 v[120:123], v[68:71], v[190:193], v[120:123]
	v_mfma_f32_16x16x32_bf16 v[116:119], v[76:79], v[190:193], v[116:119]
	v_mfma_f32_16x16x32_bf16 v[128:131], v[68:71], v[204:207], v[128:131]
	v_mfma_f32_16x16x32_bf16 v[124:127], v[76:79], v[204:207], v[124:127]
	v_mfma_f32_16x16x32_bf16 v[56:59], v[72:75], v[178:181], v[56:59]
	v_mfma_f32_16x16x32_bf16 v[52:55], v[80:83], v[178:181], v[52:55]
	v_mfma_f32_16x16x32_bf16 v[88:91], v[72:75], v[186:189], v[88:91]
	v_mfma_f32_16x16x32_bf16 v[84:87], v[80:83], v[186:189], v[84:87]
	v_mfma_f32_16x16x32_bf16 v[120:123], v[72:75], v[194:197], v[120:123]
	v_mfma_f32_16x16x32_bf16 v[116:119], v[80:83], v[194:197], v[116:119]
	v_mfma_f32_16x16x32_bf16 v[128:131], v[72:75], v[208:211], v[128:131]
	v_mfma_f32_16x16x32_bf16 v[124:127], v[80:83], v[208:211], v[124:127]
	v_mfma_f32_16x16x32_bf16 v[160:163], v[100:103], v[174:177], v[160:163]
	v_mfma_f32_16x16x32_bf16 v[156:159], v[132:135], v[174:177], v[156:159]
	v_mfma_f32_16x16x32_bf16 v[152:155], v[100:103], v[182:185], v[152:155]
	v_mfma_f32_16x16x32_bf16 v[148:151], v[132:135], v[182:185], v[148:151]
	v_mfma_f32_16x16x32_bf16 v[144:147], v[100:103], v[190:193], v[144:147]
	v_mfma_f32_16x16x32_bf16 v[140:143], v[132:135], v[190:193], v[140:143]
	v_mfma_f32_16x16x32_bf16 v[112:115], v[100:103], v[204:207], v[112:115]
	v_mfma_f32_16x16x32_bf16 v[108:111], v[132:135], v[204:207], v[108:111]
	v_mfma_f32_16x16x32_bf16 v[160:163], v[104:107], v[178:181], v[160:163]
	v_mfma_f32_16x16x32_bf16 v[156:159], v[136:139], v[178:181], v[156:159]
	v_mfma_f32_16x16x32_bf16 v[152:155], v[104:107], v[186:189], v[152:155]
	v_mfma_f32_16x16x32_bf16 v[148:151], v[136:139], v[186:189], v[148:151]
	v_mfma_f32_16x16x32_bf16 v[144:147], v[104:107], v[194:197], v[144:147]
	v_mfma_f32_16x16x32_bf16 v[140:143], v[136:139], v[194:197], v[140:143]
	v_mfma_f32_16x16x32_bf16 v[112:115], v[104:107], v[208:211], v[112:115]
	v_mfma_f32_16x16x32_bf16 v[108:111], v[136:139], v[208:211], v[108:111]
	s_barrier
	s_add_i32 s20, s65, s27
	v_lshl_add_u64 v[198:199], v[198:199], 0, s[42:43]
	s_mov_b32 m0, s20
	ds_read_b128 v[174:177], v203 offset:49152
	ds_read_b128 v[178:181], v203 offset:50176
	ds_read_b128 v[182:185], v203 offset:51200
	ds_read_b128 v[186:189], v203 offset:52224
	ds_read_b128 v[190:193], v203 offset:53248
	ds_read_b128 v[194:197], v203 offset:54272
	ds_read_b128 v[204:207], v203 offset:55296
	ds_read_b128 v[208:211], v203 offset:56320
	global_load_lds_dwordx4 v[198:199], off
	s_add_i32 m0, s20, 0x2000
	s_add_u32 s14, s14, 0x20080
	v_lshl_add_u64 v[198:199], v[212:213], 0, s[42:43]
	s_addc_u32 s15, s15, 0
	s_add_i32 s20, s66, s27
	global_load_lds_dwordx4 v[198:199], off
	v_lshl_add_u64 v[198:199], s[14:15], 0, v[2:3]
	s_mov_b32 m0, s20
	s_nop 0
	global_load_lds_dwordx4 v[198:199], off
	v_lshl_add_u64 v[198:199], s[14:15], 0, v[168:169]
	s_add_i32 m0, s20, 0x2000
	s_nop 0
	global_load_lds_dwordx4 v[198:199], off
	v_lshl_add_u64 v[198:199], v[214:215], 0, s[42:43]
	s_mov_b32 m0, s36
	s_nop 0
	global_load_lds_dwordx4 v[198:199], off
	v_lshl_add_u64 v[198:199], v[216:217], 0, s[42:43]
	s_mov_b32 m0, s40
	s_nop 0
	global_load_lds_dwordx4 v[198:199], off
	s_waitcnt vmcnt(8)
	s_cmp_lg_u32 s64, 4
	s_cbranch_scc1 .Lmg_nopf
	s_lshl_b32 s20, s4, 8
	s_lshl_b32 s21, s0, 8
	s_cmp_gt_i32 s0, 3
	s_cbranch_scc1 .Lmg_pf2
	v_add_u32_e32 v253, s20, v200
	v_or_b32_e32 v252, s21, v202
	v_lshl_add_u32 v252, v253, 10, v252
	global_load_dwordx2 v[228:229], v252, s[10:11]
	global_load_dwordx2 v[232:233], v252, s[34:35]
	global_load_dwordx2 v[230:231], v252, s[10:11] offset:128
	global_load_dwordx2 v[234:235], v252, s[34:35] offset:128
	v_add_u32_e32 v252, 0x4000, v252
	global_load_dwordx2 v[236:237], v252, s[10:11]
	global_load_dwordx2 v[240:241], v252, s[34:35]
	global_load_dwordx2 v[238:239], v252, s[10:11] offset:128
	global_load_dwordx2 v[242:243], v252, s[34:35] offset:128
	v_add_u32_e32 v252, 0x4000, v252
	global_load_dwordx2 v[244:245], v252, s[10:11]
	global_load_dwordx2 v[248:249], v252, s[34:35]
	global_load_dwordx2 v[246:247], v252, s[10:11] offset:128
	global_load_dwordx2 v[250:251], v252, s[34:35] offset:128
	s_branch .Lmg_nopf

; #define PG8_STAGE(bufoff, gbase, voff) do { _Pragma("unroll") for (int _i = 0; _i < 2; ++_i) \
;         __builtin_amdgcn_global_load_lds((const unsigned*)((const char*)(gbase) + (voff)[_i]), (PG8_LAS unsigned*)(lds + (bufoff) + ldsw + _i * 8192), 16, 0, 0); } while (0)
; #define PG8_LDA(dst, b, h) do { _Pragma("unroll") for (int m = 0; m < 4; ++m) _Pragma("unroll") for (int k = 0; k < 2; ++k) dst[m][k] = *(const PG8_LAS bf16x8*)(lds + PG8_SA(b, h) + aoff + m * 2048 + k * 1024); } while (0)
; #define PG8_MMA(ai, bj, At, Bt) do { __builtin_amdgcn_s_setprio(1); _Pragma("unroll") for (int m = 0; m < 4; ++m) _Pragma("unroll") for (int n = 0; n < 2; ++n) _Pragma("unroll") for (int k = 0; k < 2; ++k) \
;         acc[ai][bj][m][n] = __builtin_amdgcn_mfma_f32_16x16x32_bf16(Bt[n][k], At[m][k], acc[ai][bj][m][n], 0, 0, 0); __builtin_amdgcn_s_setprio(0); } while (0)
; #define PG8_WAIT_V(n) asm volatile("s_waitcnt vmcnt(" #n ")" ::: "memory")
; #define PG8_WAIT_L(n) asm volatile("s_waitcnt lgkmcnt(" #n ")" ::: "memory")
; #define PG8_BAR __builtin_amdgcn_s_barrier()
; #define PG8_SCHED __builtin_amdgcn_sched_barrier(0)
; template <class Epi, class Sched, bool ALIGN_EPI = false, bool SP2 = false>
; __device__ __forceinline__ void gemm_phase(PG8_LAS unsigned char* lds, const Gemm g, const Sched& S, const Epi& E) {
;     ...
;             PG8_LDA(At, 1, 1); PG8_STAGE(PG8_SB(1, 0), b3, voffB); PG8_STAGE(PG8_SB(1, 1), b3 + hstep, voffB); PG8_STAGE(PG8_SA(1, 0), a3, voffA);
;             PG8_WAIT_V(8); PG8_WAIT_L(0); PG8_BAR; if (cur.half == 0) { PG8_MMA(1, 0, At, B0); PG8_MMA(1, 1, At, B1); } PG8_BAR; PG8_SCHED;
.Lmg_nopf:
	s_waitcnt lgkmcnt(0)
	s_barrier
	s_waitcnt lgkmcnt(0)
	v_mfma_f32_16x16x32_bf16 v[96:99], v[68:71], v[174:177], v[96:99]
	v_mfma_f32_16x16x32_bf16 v[92:95], v[76:79], v[174:177], v[92:95]
	v_mfma_f32_16x16x32_bf16 v[64:67], v[68:71], v[182:185], v[64:67]
	v_mfma_f32_16x16x32_bf16 v[60:63], v[76:79], v[182:185], v[60:63]
	v_mfma_f32_16x16x32_bf16 v[32:35], v[68:71], v[190:193], v[32:35]
	v_mfma_f32_16x16x32_bf16 v[28:31], v[76:79], v[190:193], v[28:31]
	v_mfma_f32_16x16x32_bf16 v[16:19], v[68:71], v[204:207], v[16:19]
	v_mfma_f32_16x16x32_bf16 v[12:15], v[76:79], v[204:207], v[12:15]
	v_mfma_f32_16x16x32_bf16 v[96:99], v[72:75], v[178:181], v[96:99]
	v_mfma_f32_16x16x32_bf16 v[92:95], v[80:83], v[178:181], v[92:95]
	v_mfma_f32_16x16x32_bf16 v[64:67], v[72:75], v[186:189], v[64:67]
	v_mfma_f32_16x16x32_bf16 v[60:63], v[80:83], v[186:189], v[60:63]
	v_mfma_f32_16x16x32_bf16 v[32:35], v[72:75], v[194:197], v[32:35]
	v_mfma_f32_16x16x32_bf16 v[28:31], v[80:83], v[194:197], v[28:31]
	v_mfma_f32_16x16x32_bf16 v[16:19], v[72:75], v[208:211], v[16:19]
	v_mfma_f32_16x16x32_bf16 v[12:15], v[80:83], v[208:211], v[12:15]
	v_mfma_f32_16x16x32_bf16 v[36:39], v[100:103], v[174:177], v[36:39]
	v_mfma_f32_16x16x32_bf16 v[80:83], v[104:107], v[178:181], v[36:39]
	v_mfma_f32_16x16x32_bf16 v[36:39], v[132:135], v[174:177], v[40:43]
	v_mfma_f32_16x16x32_bf16 v[76:79], v[136:139], v[178:181], v[36:39]
	v_mfma_f32_16x16x32_bf16 v[36:39], v[100:103], v[182:185], v[48:51]
	v_mfma_f32_16x16x32_bf16 v[48:51], v[104:107], v[186:189], v[36:39]
	v_mfma_f32_16x16x32_bf16 v[36:39], v[132:135], v[182:185], v[44:47]
	v_mfma_f32_16x16x32_bf16 v[24:27], v[100:103], v[190:193], v[24:27]
	v_mfma_f32_16x16x32_bf16 v[20:23], v[132:135], v[190:193], v[20:23]
	v_mfma_f32_16x16x32_bf16 v[8:11], v[100:103], v[204:207], v[8:11]
	v_mfma_f32_16x16x32_bf16 v[4:7], v[132:135], v[204:207], v[4:7]
	v_mfma_f32_16x16x32_bf16 v[44:47], v[136:139], v[186:189], v[36:39]
	v_mfma_f32_16x16x32_bf16 v[24:27], v[104:107], v[194:197], v[24:27]
	v_mfma_f32_16x16x32_bf16 v[20:23], v[136:139], v[194:197], v[20:23]
	v_mfma_f32_16x16x32_bf16 v[8:11], v[104:107], v[208:211], v[8:11]
	v_mfma_f32_16x16x32_bf16 v[4:7], v[136:139], v[208:211], v[4:7]
	s_barrier
	s_add_i32 s64, s64, 2
	s_add_u32 s6, s6, 0x100
	s_addc_u32 s7, s7, 0
	s_add_u32 s62, s62, 0x100
	s_addc_u32 s63, s63, 0
	s_cmp_gt_u32 s64, 5
	s_cbranch_scc0 .LBB0_1135
	s_and_b64 vcc, exec, s[16:17]
	s_cbranch_vccz .LBB0_1138
	s_barrier

; #define GAS __attribute__((address_space(1)))
; __device__ __forceinline__ unsigned xb_add(unsigned* p, unsigned v) { return __hip_atomic_fetch_add(p, v, __ATOMIC_RELAXED, __HIP_MEMORY_SCOPE_AGENT); }
; #define SEAM_LOCAL(k) do { if (IN(k) && IN((k) + 1)) { TBAR0(); xcd_barrier(bar, true, true); TBAR1(); } } while (0)
; __device__ __forceinline__ void xcd_barrier(const XcdBarrier& b, const bool group_local = false, const bool xcc_only = false) {
;     asm volatile("s_waitcnt vmcnt(0)" ::: "memory");
;     __syncthreads();
;     if (threadIdx.x == 0) {
;         GAS unsigned* barg = (GAS unsigned*)b.bar; asm volatile("" : "+s"(barg)); unsigned* bar = (unsigned*)barg;
;         __builtin_amdgcn_s_waitcnt(0);
;         unsigned nloc = b.st[0], nx = b.st[1];
;         if (nloc == 0u) { xcd_barrier_complete(bar, b.x, nloc, nx); b.st[0] = nloc; b.st[1] = nx; }
;         const unsigned old = xb_add(&bar[XB_XSUB(b.x)], 1u);
; __global__ void __launch_bounds__(NWAVES * 64, 2) mk_fwd(Args args) {
;     ...
;             SEAM_LOCAL(pb + 2);
.LBB0_1206:
	v_readlane_b32 s0, v255, 23
	s_add_i32 s22, s0, 4
	v_readlane_b32 s0, v255, 6
	v_readlane_b32 s1, v255, 7
	s_cmp_ge_i32 s22, s1
	s_cbranch_scc1 .LBB0_1282
	s_waitcnt vmcnt(0)
	s_waitcnt vmcnt(0) lgkmcnt(0)
	s_barrier
	s_setprio 0
	s_mov_b64 s[14:15], exec
	v_readlane_b32 s0, v255, 43
	v_readlane_b32 s1, v255, 44
	s_and_b64 s[0:1], s[14:15], s[0:1]
	s_mov_b64 exec, s[0:1]
	s_cbranch_execz .LBB0_1281
	v_readlane_b32 s0, v255, 10
	v_readlane_b32 s4, v255, 12
	v_readlane_b32 s1, v255, 11
	s_waitcnt vmcnt(0) expcnt(0) lgkmcnt(0)
	v_mov_b32_e32 v4, s4
	ds_read_b32 v2, v4
	ds_read_b32 v6, v4 offset:4
	s_waitcnt lgkmcnt(1)
	v_cmp_ne_u32_e32 vcc, 0, v2
	s_cbranch_vccnz .LBB0_1223
	v_readlane_b32 s4, v255, 0
	v_readlane_b32 s5, v255, 1
	s_load_dwordx2 s[8:9], s[4:5], 0x4
	v_readlane_b32 s4, v255, 47
	s_lshl_b32 s4, s4, 2
	s_add_u32 s4, s0, s4
	s_addc_u32 s5, s1, 0
	s_add_u32 s6, s0, 0x1000
	s_addc_u32 s7, s1, 0
	s_waitcnt lgkmcnt(0)
	s_mul_i32 s23, s8, s33
	s_add_u32 s8, s0, 0x1100
	s_mul_i32 s23, s23, s9
	s_addc_u32 s9, s1, 0
	s_add_u32 s10, s0, 0x1200
	s_addc_u32 s11, s1, 0
	s_add_u32 s12, s0, 0x1300
	s_addc_u32 s13, s1, 0
	s_mov_b32 s24, 1
	s_branch .LBB0_1211

;     __device__ __forceinline__ void a_ready(const Unit&) const { if (++ncall == 3 && sig != nullptr && threadIdx.x == 0) __hip_atomic_fetch_add(sig, 1u, __ATOMIC_RELAXED, __HIP_MEMORY_SCOPE_AGENT); }
; __device__ __forceinline__ f32x4 load_row_partials(const float* rsp, int pm, int tid) { f32x4 p = {0.f, 0.f, 0.f, 0.f}; if (tid < BM) p = *(const f32x4*)(rsp + (size_t)(pm * BM + tid) * 4); return p; }
; #define PG8_BAR __builtin_amdgcn_s_barrier()
; template <class Epi, class Sched, bool ALIGN_EPI = false, bool SP2 = false>
; __device__ __forceinline__ void gemm_phase(PG8_LAS unsigned char* lds, const Gemm g, const Sched& S, const Epi& E) {
;     ...
;     for (int i = 0; i < 2; ++i) { int R, C; stage_rc(tid * 16 + i * 8192, R, C); const int Rb = Epi::PERM ? ((R & ~31) + perm32(R & 31)) : R;
;         voffA[i] = (unsigned)(R * K + C) * 2u; voffB[i] = (unsigned)(Rb * K + C) * 2u; }
;     const size_t kstep = (size_t)(BK * 2);
;     const size_t hstep = (size_t)HALF * K * 2;
;     const size_t tstep = 2 * hstep;
;     const unsigned ldsw = (unsigned)wid * 1024u;
;     const int aoff = lds_byte(wr * 64 + fr, fq * 8), boff = lds_byte(wc * 32 + fr, fq * 8);
;     ...
;     Unit cur, nxt; int ui = 0;
;     ...
;     unsigned pg8_probe_acc = 0u;
;     ...
;     if (!S.next(0, cur)) return;
;     ...
;     const unsigned long long tramp_ = __builtin_amdgcn_s_memrealtime();
;     ...
;     static_assert(!Epi::ROWSCALE || SP2, "row factors are staged in the SP2 prologue");
;     f32x4 rowp_ = {0.f, 0.f, 0.f, 0.f}; if constexpr (Epi::ROWSCALE) rowp_ = load_row_partials(E.rsp, cur.pm, tid);
;     f32x4 acc[2][2][4][2];
; #pragma unroll
;     for (int a = 0; a < 2; ++a)
; #pragma unroll
;         for (int b = 0; b < 2; ++b)
; #pragma unroll
;             for (int m = 0; m < 4; ++m)
; #pragma unroll
;                 for (int n = 0; n < 2; ++n) acc[a][b][m][n] = (f32x4){0.f, 0.f, 0.f, 0.f};
;     bf16x8 At[4][2], B0[2][2], B1[2][2];
;     const char* cA = (const char*)g.A + (size_t)cur.pm * tstep + (cur.half == 2 ? hstep : (size_t)0); const char* cB = (const char*)g.Bt + (size_t)cur.pn * tstep;
;     S.a_ready(cur);
;     if constexpr (SP2) {
;         PG8_STAGE(PG8_SB(0, 0), cB, voffB); PG8_STAGE(PG8_SB(0, 1), cB + hstep, voffB); PG8_STAGE(PG8_SA(0, 0), cA, voffA); PG8_STAGE(PG8_SA(0, 1), cA + hstep, voffA);
;         if (wr == 1) PG8_BAR;
.LBB0_1290:
	v_ashrrev_i32_e32 v2, 31, v146
	v_lshrrev_b32_e32 v2, 26, v2
	v_add_u32_e32 v2, v146, v2
	v_ashrrev_i32_e32 v4, 6, v2
	v_bfe_i32 v2, v146, 27, 1
	v_lshlrev_b32_e32 v7, 4, v146
	v_lshrrev_b32_e32 v2, 22, v2
	v_add_u32_e32 v2, v7, v2
	v_and_b32_e32 v2, 0xfffffc00, v2
	v_sub_u32_e32 v2, v7, v2
	v_lshrrev_b32_e32 v5, 4, v2
	v_bitop3_b32 v2, v5, v2, 32 bitop3:0x6c
	v_lshlrev_b32_e32 v5, 3, v4
	v_and_b32_e32 v6, -16, v5
	v_ashrrev_i32_e32 v5, 31, v2
	v_lshrrev_b32_e32 v5, 26, v5
	s_mul_i32 s36, s77, 0xee0000
	v_add_u32_e32 v8, v2, v5
	s_lshl_b64 s[6:7], s[36:37], 1
	v_ashrrev_i32_e32 v5, 6, v8
	s_add_u32 s1, s12, s6
	v_add_u32_e32 v9, v5, v6
	v_lshlrev_b32_e32 v6, 5, v4
	s_addc_u32 s5, s13, s7
	v_and_b32_e32 v10, 32, v6
	v_and_b32_e32 v6, 0xc0, v8
	s_add_u32 s34, s12, 0x12000000
	v_sub_u32_e32 v2, v2, v6
	s_addc_u32 s35, s13, 0
	v_ashrrev_i16_sdwa v2, v224, sext(v2) dst_sel:DWORD dst_unused:UNUSED_PAD src0_sel:DWORD src1_sel:BYTE_0
	s_add_u32 s36, s1, 0x1300000
	v_bfe_i32 v6, v2, 0, 16
	v_lshlrev_b32_e32 v2, 1, v9
	v_lshrrev_b32_e32 v8, 2, v9
	v_and_b32_e32 v11, 3, v5
	s_mov_b32 s1, 0x1fffe0
	v_and_b32_e32 v2, 24, v2
	v_and_b32_e32 v8, 4, v8
	v_and_or_b32 v11, v9, s1, v11
	v_or3_b32 v2, v11, v8, v2
	v_add_lshl_u32 v8, v10, v6, 1
	v_lshl_add_u32 v132, v9, 11, v8
	v_lshl_add_u32 v2, v2, 11, v8
	v_add_u32_e32 v8, 0x2000, v7
	v_ashrrev_i32_e32 v7, 31, v8
	v_lshrrev_b32_e32 v7, 22, v7
	v_add_u32_e32 v7, v8, v7
	v_ashrrev_i32_e32 v7, 10, v7
	v_mul_i32_i24_e32 v9, 0x400, v7
	v_sub_u32_e32 v8, v8, v9
	v_lshrrev_b32_e32 v9, 4, v8
	v_bitop3_b32 v9, v9, v8, 32 bitop3:0x6c
	v_lshlrev_b32_e32 v8, 3, v7
	v_and_b32_e32 v10, -16, v8
	v_ashrrev_i32_e32 v8, 31, v9
	v_lshrrev_b32_e32 v8, 26, v8
	v_add_u32_e32 v11, v9, v8
	v_ashrrev_i32_e32 v8, 6, v11
	s_addc_u32 s38, s5, 0
	v_add_u32_e32 v10, v8, v10
	v_and_b32_e32 v14, 3, v8
	s_add_i32 s0, s4, s0
	v_and_or_b32 v14, v10, s1, v14
	s_ashr_i32 s1, s0, 31
	s_lshr_b32 s1, s1, 27
	s_add_i32 s1, s0, s1
	s_ashr_i32 s4, s1, 5
	s_and_b32 s1, s1, 0xffe0
	s_sub_i32 s0, s0, s1
	s_bfe_i32 s1, s0, 0x80000
	s_bfe_u32 s1, s1, 0x3000c
	s_add_i32 s1, s0, s1
	s_bfe_i32 s5, s1, 0x80000
	s_and_b32 s1, s1, 0xf8
	s_sub_i32 s0, s0, s1
	s_lshl_b32 s4, s4, 3
	s_sext_i32_i16 s5, s5
	s_sext_i32_i8 s0, s0
	s_lshr_b32 s6, s5, 3
	s_add_i32 s8, s4, s0
	s_ashr_i32 s17, s25, 6
	s_ashr_i32 s9, s8, 31
	s_bfe_i64 s[0:1], s[6:7], 0x100000
	s_ashr_i32 s22, s25, 8
	v_and_b32_e32 v11, 0xc0, v11
	s_lshl_b32 s39, s17, 10
	s_lshl_b64 s[4:5], s[8:9], 19
	s_lshl_b64 s[0:1], s[0:1], 19
	v_sub_u32_e32 v9, v9, v11
	s_add_u32 s0, s36, s0
	v_lshlrev_b32_e32 v12, 5, v7
	v_ashrrev_i16_sdwa v9, v224, sext(v9) dst_sel:DWORD dst_unused:UNUSED_PAD src0_sel:DWORD src1_sel:BYTE_0
	v_lshlrev_b32_e32 v11, 1, v10
	v_lshrrev_b32_e32 v13, 2, v10
	s_addc_u32 s1, s38, s1
	s_add_i32 s40, s39, 0
	v_and_b32_e32 v12, 32, v12
	v_bfe_i32 v9, v9, 0, 16
	v_and_b32_e32 v11, 24, v11
	v_and_b32_e32 v13, 4, v13
	s_add_i32 m0, s40, 0x10000
	v_or3_b32 v11, v14, v13, v11
	v_add_lshl_u32 v12, v12, v9, 1
	global_load_lds_dwordx4 v2, s[0:1]
	s_add_i32 m0, s40, 0x12000
	v_lshl_add_u32 v136, v11, 11, v12
	s_add_u32 s10, s0, 0x40000
	global_load_lds_dwordx4 v136, s[0:1]
	s_addc_u32 s11, s1, 0
	s_add_i32 m0, s40, 0x14000
	v_lshl_add_u32 v134, v10, 11, v12
	global_load_lds_dwordx4 v2, s[10:11]
	s_add_i32 m0, s40, 0x16000
	s_add_u32 s4, s34, s4
	s_addc_u32 s5, s35, s5
	s_add_i32 s41, s40, 0x2000
	global_load_lds_dwordx4 v136, s[10:11]
	s_mov_b32 m0, s40
	s_add_u32 s10, s4, 0x40000
	global_load_lds_dwordx4 v132, s[4:5]
	s_mov_b32 m0, s41
	s_addc_u32 s11, s5, 0
	s_add_i32 s56, s40, 0x4000
	global_load_lds_dwordx4 v134, s[4:5]
	s_mov_b32 m0, s56
	s_add_i32 s57, s40, 0x6000
	global_load_lds_dwordx4 v132, s[10:11]
	s_mov_b32 m0, s57
	s_cmp_lg_u32 s22, 1
	global_load_lds_dwordx4 v134, s[10:11]
	s_cbranch_scc1 .LBB0_1292
	s_setprio 1
	s_barrier

; #define PG8_STAGE(bufoff, gbase, voff) do { _Pragma("unroll") for (int _i = 0; _i < 2; ++_i) \
;         __builtin_amdgcn_global_load_lds((const unsigned*)((const char*)(gbase) + (voff)[_i]), (PG8_LAS unsigned*)(lds + (bufoff) + ldsw + _i * 8192), 16, 0, 0); } while (0)
; #define PG8_LDA(dst, b, h) do { _Pragma("unroll") for (int m = 0; m < 4; ++m) _Pragma("unroll") for (int k = 0; k < 2; ++k) dst[m][k] = *(const PG8_LAS bf16x8*)(lds + PG8_SA(b, h) + aoff + m * 2048 + k * 1024); } while (0)
; #define PG8_LDB(dst, b, h) do { _Pragma("unroll") for (int n = 0; n < 2; ++n) _Pragma("unroll") for (int k = 0; k < 2; ++k) dst[n][k] = *(const PG8_LAS bf16x8*)(lds + PG8_SB(b, h) + boff + n * 2048 + k * 1024); } while (0)
; #define PG8_MMA(ai, bj, At, Bt) do { __builtin_amdgcn_s_setprio(1); _Pragma("unroll") for (int m = 0; m < 4; ++m) _Pragma("unroll") for (int n = 0; n < 2; ++n) _Pragma("unroll") for (int k = 0; k < 2; ++k) \
;         acc[ai][bj][m][n] = __builtin_amdgcn_mfma_f32_16x16x32_bf16(Bt[n][k], At[m][k], acc[ai][bj][m][n], 0, 0, 0); __builtin_amdgcn_s_setprio(0); } while (0)
; #define PG8_WAIT_V(n) asm volatile("s_waitcnt vmcnt(" #n ")" ::: "memory")
; #define PG8_WAIT_L(n) asm volatile("s_waitcnt lgkmcnt(" #n ")" ::: "memory")
; #define PG8_BAR __builtin_amdgcn_s_barrier()
; #define PG8_SCHED __builtin_amdgcn_sched_barrier(0)
; template <class Epi, class Sched, bool ALIGN_EPI = false, bool SP2 = false>
; __device__ __forceinline__ void gemm_phase(PG8_LAS unsigned char* lds, const Gemm g, const Sched& S, const Epi& E) {
;     ...
;             PG8_LDB(B0, 0, 0); PG8_LDB(B1, 0, 1); PG8_SCHED; PG8_LDA(At, 0, 0); PG8_STAGE(PG8_SA(1, 1), a1 + hstep, voffA);
;     ...
;             if (PROBE_KIND == 18 && t == 0 && ui > 0 && g.probe) { const unsigned long long tq_ = __builtin_amdgcn_s_memrealtime(); PG8_WAIT_V(8); pg8_probe_acc += (unsigned)(__builtin_amdgcn_s_memrealtime() - tq_); }
;     ...
;             PG8_WAIT_V(8); PG8_WAIT_L(0); PG8_BAR; PG8_MMA(0, 0, At, B0); PG8_MMA(0, 1, At, B1); PG8_BAR; PG8_SCHED;
;             PG8_LDA(At, 0, 1); PG8_STAGE(PG8_SB(0, 0), b2, voffB); PG8_STAGE(PG8_SB(0, 1), b2 + hstep, voffB); PG8_STAGE(PG8_SA(0, 0), a2, voffA);
;             PG8_WAIT_V(8); PG8_WAIT_L(0); PG8_BAR; if (cur.half == 0) { PG8_MMA(1, 0, At, B0); PG8_MMA(1, 1, At, B1); } PG8_BAR; PG8_SCHED;
.LBB0_1300:
	s_add_u32 s28, s4, s0
	s_addc_u32 s29, s5, s1
	s_add_u32 s28, s28, 0x100
	s_addc_u32 s29, s29, 0
	s_add_u32 s67, s62, s0
	s_addc_u32 s68, s63, s1
	s_add_i32 s69, 0, 0x10000
	s_cmpk_eq_i32 s0, 0x700
	s_cselect_b32 s31, s7, s29
	s_cselect_b32 s30, s64, s28
	s_cselect_b32 s29, s11, s68
	s_cselect_b32 s28, s65, s67
	s_add_i32 s67, 0, 0x14000
	v_add_u32_e32 v162, s69, v148
	v_add_u32_e32 v178, s67, v148
	ds_read_b128 v[150:153], v162
	ds_read_b128 v[154:157], v162 offset:1024
	ds_read_b128 v[158:161], v162 offset:2048
	ds_read_b128 v[162:165], v162 offset:3072
	ds_read_b128 v[166:169], v178
	ds_read_b128 v[170:173], v178 offset:1024
	ds_read_b128 v[174:177], v178 offset:2048
	ds_read_b128 v[178:181], v178 offset:3072
	v_lshl_add_u64 v[216:217], v[142:143], 0, s[0:1]
	s_add_i32 m0, s40, 0xc000
	ds_read_b128 v[182:185], v149
	ds_read_b128 v[186:189], v149 offset:1024
	ds_read_b128 v[190:193], v149 offset:2048
	ds_read_b128 v[194:197], v149 offset:3072
	ds_read_b128 v[198:201], v149 offset:4096
	ds_read_b128 v[202:205], v149 offset:5120
	ds_read_b128 v[206:209], v149 offset:6144
	ds_read_b128 v[210:213], v149 offset:7168
	global_load_lds_dwordx4 v[216:217], off
	v_lshl_add_u64 v[216:217], v[144:145], 0, s[0:1]
	s_add_i32 m0, s40, 0xe000
	s_nop 0
	global_load_lds_dwordx4 v[216:217], off
	s_waitcnt vmcnt(8)
	s_waitcnt lgkmcnt(0)
	s_barrier
	s_waitcnt lgkmcnt(0)
	v_mfma_f32_16x16x32_bf16 v[128:131], v[150:153], v[182:185], v[128:131]
	v_mfma_f32_16x16x32_bf16 v[124:127], v[158:161], v[182:185], v[124:127]
	v_mfma_f32_16x16x32_bf16 v[112:115], v[150:153], v[190:193], v[112:115]
	v_mfma_f32_16x16x32_bf16 v[108:111], v[158:161], v[190:193], v[108:111]
	v_mfma_f32_16x16x32_bf16 v[96:99], v[150:153], v[198:201], v[96:99]
	v_mfma_f32_16x16x32_bf16 v[92:95], v[158:161], v[198:201], v[92:95]
	v_mfma_f32_16x16x32_bf16 v[80:83], v[150:153], v[206:209], v[80:83]
	v_mfma_f32_16x16x32_bf16 v[76:79], v[158:161], v[206:209], v[76:79]
	v_mfma_f32_16x16x32_bf16 v[128:131], v[154:157], v[186:189], v[128:131]
	v_mfma_f32_16x16x32_bf16 v[124:127], v[162:165], v[186:189], v[124:127]
	v_mfma_f32_16x16x32_bf16 v[112:115], v[154:157], v[194:197], v[112:115]
	v_mfma_f32_16x16x32_bf16 v[108:111], v[162:165], v[194:197], v[108:111]
	v_mfma_f32_16x16x32_bf16 v[96:99], v[154:157], v[202:205], v[96:99]
	v_mfma_f32_16x16x32_bf16 v[92:95], v[162:165], v[202:205], v[92:95]
	v_mfma_f32_16x16x32_bf16 v[80:83], v[154:157], v[210:213], v[80:83]
	v_mfma_f32_16x16x32_bf16 v[76:79], v[162:165], v[210:213], v[76:79]
	v_mfma_f32_16x16x32_bf16 v[120:123], v[166:169], v[182:185], v[120:123]
	v_mfma_f32_16x16x32_bf16 v[116:119], v[174:177], v[182:185], v[116:119]
	v_mfma_f32_16x16x32_bf16 v[104:107], v[166:169], v[190:193], v[104:107]
	v_mfma_f32_16x16x32_bf16 v[100:103], v[174:177], v[190:193], v[100:103]
	v_mfma_f32_16x16x32_bf16 v[88:91], v[166:169], v[198:201], v[88:91]
	v_mfma_f32_16x16x32_bf16 v[84:87], v[174:177], v[198:201], v[84:87]
	v_mfma_f32_16x16x32_bf16 v[72:75], v[166:169], v[206:209], v[72:75]
	v_mfma_f32_16x16x32_bf16 v[68:71], v[174:177], v[206:209], v[68:71]
	v_mfma_f32_16x16x32_bf16 v[120:123], v[170:173], v[186:189], v[120:123]
	v_mfma_f32_16x16x32_bf16 v[116:119], v[178:181], v[186:189], v[116:119]
	v_mfma_f32_16x16x32_bf16 v[104:107], v[170:173], v[194:197], v[104:107]
	v_mfma_f32_16x16x32_bf16 v[100:103], v[178:181], v[194:197], v[100:103]
	v_mfma_f32_16x16x32_bf16 v[88:91], v[170:173], v[202:205], v[88:91]
	v_mfma_f32_16x16x32_bf16 v[84:87], v[178:181], v[202:205], v[84:87]
	v_mfma_f32_16x16x32_bf16 v[72:75], v[170:173], v[210:213], v[72:75]
	v_mfma_f32_16x16x32_bf16 v[68:71], v[178:181], v[210:213], v[68:71]
	s_barrier
	s_add_i32 s68, s69, s39
	v_lshl_add_u64 v[216:217], s[28:29], 0, v[2:3]
	s_mov_b32 m0, s68
	ds_read_b128 v[182:185], v149 offset:16384
	ds_read_b128 v[186:189], v149 offset:17408
	ds_read_b128 v[190:193], v149 offset:18432
	ds_read_b128 v[194:197], v149 offset:19456
	ds_read_b128 v[198:201], v149 offset:20480
	ds_read_b128 v[202:205], v149 offset:21504
	ds_read_b128 v[206:209], v149 offset:22528
	ds_read_b128 v[210:213], v149 offset:23552
	global_load_lds_dwordx4 v[216:217], off
	s_add_i32 m0, s68, 0x2000
	s_add_u32 s68, s28, 0x40000
	v_lshl_add_u64 v[218:219], s[28:29], 0, v[136:137]
	s_addc_u32 s69, s29, 0
	s_add_i32 s67, s67, s39
	global_load_lds_dwordx4 v[218:219], off
	v_lshl_add_u64 v[220:221], s[68:69], 0, v[2:3]
	s_mov_b32 m0, s67
	v_lshl_add_u64 v[228:229], s[30:31], 0, v[134:135]
	global_load_lds_dwordx4 v[220:221], off
	v_lshl_add_u64 v[220:221], s[68:69], 0, v[136:137]
	s_add_i32 m0, s67, 0x2000
	s_nop 0
	global_load_lds_dwordx4 v[220:221], off
	v_lshl_add_u64 v[220:221], s[30:31], 0, v[132:133]
	s_mov_b32 m0, s40
	s_nop 0
	global_load_lds_dwordx4 v[220:221], off
	s_mov_b32 m0, s41
	s_nop 0
	global_load_lds_dwordx4 v[228:229], off
	s_waitcnt vmcnt(8)
	s_waitcnt lgkmcnt(0)
	s_barrier
; #define PG8_STAGE(bufoff, gbase, voff) do { _Pragma("unroll") for (int _i = 0; _i < 2; ++_i) \
;         __builtin_amdgcn_global_load_lds((const unsigned*)((const char*)(gbase) + (voff)[_i]), (PG8_LAS unsigned*)(lds + (bufoff) + ldsw + _i * 8192), 16, 0, 0); } while (0)
; #define PG8_LDA(dst, b, h) do { _Pragma("unroll") for (int m = 0; m < 4; ++m) _Pragma("unroll") for (int k = 0; k < 2; ++k) dst[m][k] = *(const PG8_LAS bf16x8*)(lds + PG8_SA(b, h) + aoff + m * 2048 + k * 1024); } while (0)
; #define PG8_LDB(dst, b, h) do { _Pragma("unroll") for (int n = 0; n < 2; ++n) _Pragma("unroll") for (int k = 0; k < 2; ++k) dst[n][k] = *(const PG8_LAS bf16x8*)(lds + PG8_SB(b, h) + boff + n * 2048 + k * 1024); } while (0)
; #define PG8_MMA(ai, bj, At, Bt) do { __builtin_amdgcn_s_setprio(1); _Pragma("unroll") for (int m = 0; m < 4; ++m) _Pragma("unroll") for (int n = 0; n < 2; ++n) _Pragma("unroll") for (int k = 0; k < 2; ++k) \
;         acc[ai][bj][m][n] = __builtin_amdgcn_mfma_f32_16x16x32_bf16(Bt[n][k], At[m][k], acc[ai][bj][m][n], 0, 0, 0); __builtin_amdgcn_s_setprio(0); } while (0)
; #define PG8_WAIT_V(n) asm volatile("s_waitcnt vmcnt(" #n ")" ::: "memory")
; #define PG8_WAIT_L(n) asm volatile("s_waitcnt lgkmcnt(" #n ")" ::: "memory")
; #define PG8_BAR __builtin_amdgcn_s_barrier()
; #define PG8_SCHED __builtin_amdgcn_sched_barrier(0)
; template <class Epi, class Sched, bool ALIGN_EPI = false, bool SP2 = false>
; __device__ __forceinline__ void gemm_phase(PG8_LAS unsigned char* lds, const Gemm g, const Sched& S, const Epi& E) {
;     ...
;             PG8_WAIT_V(8); PG8_WAIT_L(0); PG8_BAR; if (cur.half == 0) { PG8_MMA(1, 0, At, B0); PG8_MMA(1, 1, At, B1); } PG8_BAR; PG8_SCHED;
;             PG8_LDB(B0, 1, 0); PG8_LDB(B1, 1, 1); PG8_SCHED; PG8_LDA(At, 1, 0); PG8_STAGE(PG8_SA(0, 1), a2 + hstep, voffA);
;             PG8_WAIT_V(8); PG8_WAIT_L(0); PG8_BAR; PG8_MMA(0, 0, At, B0); PG8_MMA(0, 1, At, B1); PG8_BAR; PG8_SCHED;
	s_waitcnt lgkmcnt(0)
	v_mfma_f32_16x16x32_bf16 v[64:67], v[150:153], v[182:185], v[64:67]
	v_mfma_f32_16x16x32_bf16 v[60:63], v[158:161], v[182:185], v[60:63]
	v_mfma_f32_16x16x32_bf16 v[48:51], v[150:153], v[190:193], v[48:51]
	v_mfma_f32_16x16x32_bf16 v[44:47], v[158:161], v[190:193], v[44:47]
	v_mfma_f32_16x16x32_bf16 v[32:35], v[150:153], v[198:201], v[32:35]
	v_mfma_f32_16x16x32_bf16 v[28:31], v[158:161], v[198:201], v[28:31]
	v_mfma_f32_16x16x32_bf16 v[16:19], v[150:153], v[206:209], v[16:19]
	v_mfma_f32_16x16x32_bf16 v[12:15], v[158:161], v[206:209], v[12:15]
	v_mfma_f32_16x16x32_bf16 v[64:67], v[154:157], v[186:189], v[64:67]
	v_mfma_f32_16x16x32_bf16 v[60:63], v[162:165], v[186:189], v[60:63]
	v_mfma_f32_16x16x32_bf16 v[48:51], v[154:157], v[194:197], v[48:51]
	v_mfma_f32_16x16x32_bf16 v[44:47], v[162:165], v[194:197], v[44:47]
	v_mfma_f32_16x16x32_bf16 v[32:35], v[154:157], v[202:205], v[32:35]
	v_mfma_f32_16x16x32_bf16 v[28:31], v[162:165], v[202:205], v[28:31]
	v_mfma_f32_16x16x32_bf16 v[16:19], v[154:157], v[210:213], v[16:19]
	v_mfma_f32_16x16x32_bf16 v[12:15], v[162:165], v[210:213], v[12:15]
	v_mfma_f32_16x16x32_bf16 v[56:59], v[166:169], v[182:185], v[56:59]
	v_mfma_f32_16x16x32_bf16 v[52:55], v[174:177], v[182:185], v[52:55]
	v_mfma_f32_16x16x32_bf16 v[40:43], v[166:169], v[190:193], v[40:43]
	v_mfma_f32_16x16x32_bf16 v[36:39], v[174:177], v[190:193], v[36:39]
	v_mfma_f32_16x16x32_bf16 v[24:27], v[166:169], v[198:201], v[24:27]
	v_mfma_f32_16x16x32_bf16 v[20:23], v[174:177], v[198:201], v[20:23]
	v_mfma_f32_16x16x32_bf16 v[8:11], v[166:169], v[206:209], v[8:11]
	v_mfma_f32_16x16x32_bf16 v[4:7], v[174:177], v[206:209], v[4:7]
	v_mfma_f32_16x16x32_bf16 v[56:59], v[170:173], v[186:189], v[56:59]
	v_mfma_f32_16x16x32_bf16 v[52:55], v[178:181], v[186:189], v[52:55]
	v_mfma_f32_16x16x32_bf16 v[40:43], v[170:173], v[194:197], v[40:43]
	v_mfma_f32_16x16x32_bf16 v[36:39], v[178:181], v[194:197], v[36:39]
	v_mfma_f32_16x16x32_bf16 v[24:27], v[170:173], v[202:205], v[24:27]
	v_mfma_f32_16x16x32_bf16 v[20:23], v[178:181], v[202:205], v[20:23]
	v_mfma_f32_16x16x32_bf16 v[8:11], v[170:173], v[210:213], v[8:11]
	v_mfma_f32_16x16x32_bf16 v[4:7], v[178:181], v[210:213], v[4:7]
	s_barrier
	s_add_i32 s67, 0, 0x18000
	s_add_i32 s68, 0, 0x1c000
	v_add_u32_e32 v162, s67, v148
	v_add_u32_e32 v178, s68, v148
	ds_read_b128 v[150:153], v162
	ds_read_b128 v[154:157], v162 offset:1024
	ds_read_b128 v[158:161], v162 offset:2048
	ds_read_b128 v[162:165], v162 offset:3072
	ds_read_b128 v[166:169], v178
	ds_read_b128 v[170:173], v178 offset:1024
	ds_read_b128 v[174:177], v178 offset:2048
	ds_read_b128 v[178:181], v178 offset:3072
	s_add_u32 s30, s30, 0x40000
	s_addc_u32 s31, s31, 0
	s_mov_b32 m0, s56
	v_lshl_add_u64 v[230:231], s[30:31], 0, v[132:133]
	ds_read_b128 v[182:185], v149 offset:32768
	ds_read_b128 v[186:189], v149 offset:33792
	ds_read_b128 v[190:193], v149 offset:34816
	ds_read_b128 v[194:197], v149 offset:35840
	ds_read_b128 v[198:201], v149 offset:36864
	ds_read_b128 v[202:205], v149 offset:37888
	ds_read_b128 v[206:209], v149 offset:38912
	ds_read_b128 v[210:213], v149 offset:39936
	global_load_lds_dwordx4 v[230:231], off
	v_lshl_add_u64 v[230:231], s[30:31], 0, v[134:135]
	s_mov_b32 m0, s57
	s_nop 0
	global_load_lds_dwordx4 v[230:231], off
	s_waitcnt vmcnt(8)
	s_waitcnt lgkmcnt(0)
	s_barrier
	s_waitcnt lgkmcnt(0)
	v_mfma_f32_16x16x32_bf16 v[128:131], v[150:153], v[182:185], v[128:131]
	v_mfma_f32_16x16x32_bf16 v[124:127], v[158:161], v[182:185], v[124:127]
	v_mfma_f32_16x16x32_bf16 v[112:115], v[150:153], v[190:193], v[112:115]
	v_mfma_f32_16x16x32_bf16 v[108:111], v[158:161], v[190:193], v[108:111]
	v_mfma_f32_16x16x32_bf16 v[96:99], v[150:153], v[198:201], v[96:99]
	v_mfma_f32_16x16x32_bf16 v[92:95], v[158:161], v[198:201], v[92:95]
	v_mfma_f32_16x16x32_bf16 v[80:83], v[150:153], v[206:209], v[80:83]
	v_mfma_f32_16x16x32_bf16 v[76:79], v[158:161], v[206:209], v[76:79]
	v_mfma_f32_16x16x32_bf16 v[128:131], v[154:157], v[186:189], v[128:131]
	v_mfma_f32_16x16x32_bf16 v[124:127], v[162:165], v[186:189], v[124:127]
	v_mfma_f32_16x16x32_bf16 v[112:115], v[154:157], v[194:197], v[112:115]
	v_mfma_f32_16x16x32_bf16 v[108:111], v[162:165], v[194:197], v[108:111]
	v_mfma_f32_16x16x32_bf16 v[96:99], v[154:157], v[202:205], v[96:99]
	v_mfma_f32_16x16x32_bf16 v[92:95], v[162:165], v[202:205], v[92:95]
	v_mfma_f32_16x16x32_bf16 v[80:83], v[154:157], v[210:213], v[80:83]
	v_mfma_f32_16x16x32_bf16 v[76:79], v[162:165], v[210:213], v[76:79]
	v_mfma_f32_16x16x32_bf16 v[120:123], v[166:169], v[182:185], v[120:123]
	v_mfma_f32_16x16x32_bf16 v[116:119], v[174:177], v[182:185], v[116:119]
	v_mfma_f32_16x16x32_bf16 v[104:107], v[166:169], v[190:193], v[104:107]
	v_mfma_f32_16x16x32_bf16 v[100:103], v[174:177], v[190:193], v[100:103]
	v_mfma_f32_16x16x32_bf16 v[88:91], v[166:169], v[198:201], v[88:91]
	v_mfma_f32_16x16x32_bf16 v[84:87], v[174:177], v[198:201], v[84:87]
	v_mfma_f32_16x16x32_bf16 v[72:75], v[166:169], v[206:209], v[72:75]
	v_mfma_f32_16x16x32_bf16 v[68:71], v[174:177], v[206:209], v[68:71]
	v_mfma_f32_16x16x32_bf16 v[120:123], v[170:173], v[186:189], v[120:123]
	v_mfma_f32_16x16x32_bf16 v[116:119], v[178:181], v[186:189], v[116:119]
	v_mfma_f32_16x16x32_bf16 v[104:107], v[170:173], v[194:197], v[104:107]
	v_mfma_f32_16x16x32_bf16 v[100:103], v[178:181], v[194:197], v[100:103]
	v_mfma_f32_16x16x32_bf16 v[88:91], v[170:173], v[202:205], v[88:91]
	v_mfma_f32_16x16x32_bf16 v[84:87], v[178:181], v[202:205], v[84:87]
	v_mfma_f32_16x16x32_bf16 v[72:75], v[170:173], v[210:213], v[72:75]
	v_mfma_f32_16x16x32_bf16 v[68:71], v[178:181], v[210:213], v[68:71]
	s_barrier
; template <class Epi, class Sched, bool ALIGN_EPI = false, bool SP2 = false>
; __device__ __forceinline__ void gemm_phase(PG8_LAS unsigned char* lds, const Gemm g, const Sched& S, const Epi& E) {
;     ...
;             PG8_LDA(At, 1, 1); PG8_STAGE(PG8_SB(1, 0), b3, voffB); PG8_STAGE(PG8_SB(1, 1), b3 + hstep, voffB); PG8_STAGE(PG8_SA(1, 0), a3, voffA);
;             PG8_WAIT_V(8); PG8_WAIT_L(0); PG8_BAR; if (cur.half == 0) { PG8_MMA(1, 0, At, B0); PG8_MMA(1, 1, At, B1); } PG8_BAR; PG8_SCHED;
;             } else {
;             PG8_LDB(B0, 0, 0); PG8_SCHED; PG8_LDA(At, 0, 0); PG8_STAGE(PG8_SA(1, 1), a1 + hstep, voffA);
;             PG8_WAIT_L(8); PG8_BAR; PG8_WAIT_L(0); PG8_MMA(0, 0, At, B0); PG8_BAR; PG8_SCHED;
;             PG8_LDB(B1, 0, 1); PG8_STAGE(PG8_SB(0, 0), b2, voffB);
;             PG8_BAR; PG8_WAIT_L(0); PG8_MMA(0, 1, At, B1); PG8_BAR;
;             PG8_LDA(At, 0, 1); PG8_STAGE(PG8_SA(0, 0), a2, voffA);
;             PG8_BAR; PG8_WAIT_L(0); PG8_MMA(1, 0, At, B0); PG8_BAR; PG8_SCHED;
;             PG8_STAGE(PG8_SB(0, 1), b2 + hstep, voffB);
;             PG8_WAIT_V(6); PG8_BAR; PG8_MMA(1, 1, At, B1); PG8_BAR;
;             PG8_LDB(B0, 1, 0); PG8_SCHED; PG8_LDA(At, 1, 0); PG8_STAGE(PG8_SA(0, 1), a2 + hstep, voffA);
;             PG8_WAIT_L(8); PG8_BAR; PG8_WAIT_L(0); PG8_MMA(0, 0, At, B0); PG8_BAR; PG8_SCHED;
;             PG8_LDB(B1, 1, 1); PG8_STAGE(PG8_SB(1, 0), b3, voffB);
;             PG8_BAR; PG8_WAIT_L(0); PG8_MMA(0, 1, At, B1); PG8_BAR;
;             PG8_LDA(At, 1, 1); PG8_STAGE(PG8_SA(1, 0), a3, voffA);
;             PG8_BAR; PG8_WAIT_L(0); PG8_MMA(1, 0, At, B0); PG8_BAR; PG8_SCHED;
;             PG8_STAGE(PG8_SB(1, 1), b3 + hstep, voffB);
;             PG8_WAIT_V(6); PG8_BAR; PG8_MMA(1, 1, At, B1); PG8_BAR;
;             }
;         }
;         if constexpr (ALIGN_EPI) { if (wr == 0) PG8_BAR; }
;     ...
;         const unsigned long long te_ = __builtin_amdgcn_s_memrealtime();
;     ...
;         if constexpr (!Epi::AFTER_DRAIN) { E(acc, cur, wr, wc, fr, fq); S.done(cur); }
;     ...
;         if ((PROBE_KIND == 19 || PROBE_KIND == 24 || PROBE_KIND == 28) && g.probe) pg8_probe_acc += (unsigned)(__builtin_amdgcn_s_memrealtime() - te_);
;     ...
;         if (!has_next) break;
;         if constexpr (!Epi::CHAIN) {
; #pragma unroll
;         for (int a = 0; a < 2; ++a)
; #pragma unroll
;             for (int b = 0; b < 2; ++b)
; #pragma unroll
	s_add_i32 s30, s67, s39
	v_lshl_add_u64 v[216:217], v[216:217], 0, s[42:43]
	s_mov_b32 m0, s30
	ds_read_b128 v[182:185], v149 offset:49152
	ds_read_b128 v[186:189], v149 offset:50176
	ds_read_b128 v[190:193], v149 offset:51200
	ds_read_b128 v[194:197], v149 offset:52224
	ds_read_b128 v[198:201], v149 offset:53248
	ds_read_b128 v[202:205], v149 offset:54272
	ds_read_b128 v[206:209], v149 offset:55296
	ds_read_b128 v[210:213], v149 offset:56320
	global_load_lds_dwordx4 v[216:217], off
	s_add_i32 m0, s30, 0x2000
	s_add_u32 s28, s28, 0x40080
	v_lshl_add_u64 v[216:217], v[218:219], 0, s[42:43]
	s_addc_u32 s29, s29, 0
	s_add_i32 s30, s68, s39
	global_load_lds_dwordx4 v[216:217], off
	v_lshl_add_u64 v[216:217], s[28:29], 0, v[2:3]
	s_mov_b32 m0, s30
	s_nop 0
	global_load_lds_dwordx4 v[216:217], off
	v_lshl_add_u64 v[216:217], s[28:29], 0, v[136:137]
	s_add_i32 m0, s30, 0x2000
	s_nop 0
	global_load_lds_dwordx4 v[216:217], off
	v_lshl_add_u64 v[216:217], v[220:221], 0, s[42:43]
	s_mov_b32 m0, s58
	s_nop 0
	global_load_lds_dwordx4 v[216:217], off
	v_lshl_add_u64 v[216:217], v[228:229], 0, s[42:43]
	s_mov_b32 m0, s59
	s_nop 0
	global_load_lds_dwordx4 v[216:217], off
	s_waitcnt vmcnt(8)
	s_waitcnt lgkmcnt(0)
	s_barrier
	s_waitcnt lgkmcnt(0)
	v_mfma_f32_16x16x32_bf16 v[64:67], v[150:153], v[182:185], v[64:67]
	v_mfma_f32_16x16x32_bf16 v[60:63], v[158:161], v[182:185], v[60:63]
	v_mfma_f32_16x16x32_bf16 v[48:51], v[150:153], v[190:193], v[48:51]
	v_mfma_f32_16x16x32_bf16 v[44:47], v[158:161], v[190:193], v[44:47]
	v_mfma_f32_16x16x32_bf16 v[32:35], v[150:153], v[198:201], v[32:35]
	v_mfma_f32_16x16x32_bf16 v[28:31], v[158:161], v[198:201], v[28:31]
	v_mfma_f32_16x16x32_bf16 v[16:19], v[150:153], v[206:209], v[16:19]
	v_mfma_f32_16x16x32_bf16 v[12:15], v[158:161], v[206:209], v[12:15]
	v_mfma_f32_16x16x32_bf16 v[64:67], v[154:157], v[186:189], v[64:67]
	v_mfma_f32_16x16x32_bf16 v[60:63], v[162:165], v[186:189], v[60:63]
	v_mfma_f32_16x16x32_bf16 v[48:51], v[154:157], v[194:197], v[48:51]
	v_mfma_f32_16x16x32_bf16 v[44:47], v[162:165], v[194:197], v[44:47]
	v_mfma_f32_16x16x32_bf16 v[32:35], v[154:157], v[202:205], v[32:35]
	v_mfma_f32_16x16x32_bf16 v[28:31], v[162:165], v[202:205], v[28:31]
	v_mfma_f32_16x16x32_bf16 v[16:19], v[154:157], v[210:213], v[16:19]
	v_mfma_f32_16x16x32_bf16 v[12:15], v[162:165], v[210:213], v[12:15]
	v_mfma_f32_16x16x32_bf16 v[56:59], v[166:169], v[182:185], v[56:59]
	v_mfma_f32_16x16x32_bf16 v[52:55], v[174:177], v[182:185], v[52:55]
	v_mfma_f32_16x16x32_bf16 v[40:43], v[166:169], v[190:193], v[40:43]
	v_mfma_f32_16x16x32_bf16 v[36:39], v[174:177], v[190:193], v[36:39]
	v_mfma_f32_16x16x32_bf16 v[24:27], v[166:169], v[198:201], v[24:27]
	v_mfma_f32_16x16x32_bf16 v[20:23], v[174:177], v[198:201], v[20:23]
	v_mfma_f32_16x16x32_bf16 v[8:11], v[166:169], v[206:209], v[8:11]
	v_mfma_f32_16x16x32_bf16 v[4:7], v[174:177], v[206:209], v[4:7]
	v_mfma_f32_16x16x32_bf16 v[56:59], v[170:173], v[186:189], v[56:59]
	v_mfma_f32_16x16x32_bf16 v[52:55], v[178:181], v[186:189], v[52:55]
	v_mfma_f32_16x16x32_bf16 v[40:43], v[170:173], v[194:197], v[40:43]
	v_mfma_f32_16x16x32_bf16 v[36:39], v[178:181], v[194:197], v[36:39]
	v_mfma_f32_16x16x32_bf16 v[24:27], v[170:173], v[202:205], v[24:27]
	v_mfma_f32_16x16x32_bf16 v[20:23], v[178:181], v[202:205], v[20:23]
	v_mfma_f32_16x16x32_bf16 v[8:11], v[170:173], v[210:213], v[8:11]
	v_mfma_f32_16x16x32_bf16 v[4:7], v[178:181], v[210:213], v[4:7]
	s_barrier
	s_add_i32 s66, s66, 2
	s_add_u32 s0, s0, 0x100
	s_addc_u32 s1, s1, 0
	s_cmp_gt_u32 s66, 13
	s_cbranch_scc0 .LBB0_1300
	s_add_u32 s0, s62, 0xffffff00
	s_addc_u32 s1, s63, -1
	s_andn2_b64 vcc, exec, s[20:21]
	s_cbranch_vccnz .LBB0_1303
	v_mov_b32_e32 v4, 0
	s_mov_b32 s16, s10
	s_mov_b32 s8, s6
	s_mov_b64 s[4:5], s[26:27]
	s_mov_b32 s60, s61
	v_mov_b32_e32 v5, v4
	v_mov_b32_e32 v6, v4
	v_mov_b32_e32 v7, v4
	v_mov_b32_e32 v8, v4
	v_mov_b32_e32 v9, v4
	v_mov_b32_e32 v10, v4
	v_mov_b32_e32 v11, v4
	v_mov_b32_e32 v20, v4
	v_mov_b32_e32 v21, v4
	v_mov_b32_e32 v22, v4
	v_mov_b32_e32 v23, v4
	v_mov_b32_e32 v24, v4
	v_mov_b32_e32 v25, v4
	v_mov_b32_e32 v26, v4
	v_mov_b32_e32 v27, v4
	v_mov_b32_e32 v36, v4
	v_mov_b32_e32 v37, v4
	v_mov_b32_e32 v38, v4
	v_mov_b32_e32 v39, v4
	v_mov_b32_e32 v40, v4
	v_mov_b32_e32 v41, v4
	v_mov_b32_e32 v42, v4
	v_mov_b32_e32 v43, v4
	v_mov_b32_e32 v52, v4
	v_mov_b32_e32 v53, v4
	v_mov_b32_e32 v54, v4
	v_mov_b32_e32 v55, v4
	v_mov_b32_e32 v56, v4
	v_mov_b32_e32 v57, v4
	v_mov_b32_e32 v58, v4
	v_mov_b32_e32 v59, v4
	v_mov_b32_e32 v12, v4
	v_mov_b32_e32 v13, v4
	v_mov_b32_e32 v14, v4
	v_mov_b32_e32 v15, v4
	v_mov_b32_e32 v16, v4
	v_mov_b32_e32 v17, v4
	v_mov_b32_e32 v18, v4
	v_mov_b32_e32 v19, v4
	v_mov_b32_e32 v28, v4
	v_mov_b32_e32 v29, v4
	v_mov_b32_e32 v30, v4
	v_mov_b32_e32 v31, v4
	v_mov_b32_e32 v32, v4
	v_mov_b32_e32 v33, v4
	v_mov_b32_e32 v34, v4
	v_mov_b32_e32 v35, v4
	v_mov_b32_e32 v44, v4
	v_mov_b32_e32 v45, v4
	v_mov_b32_e32 v46, v4
	v_mov_b32_e32 v47, v4
	v_mov_b32_e32 v48, v4
	v_mov_b32_e32 v49, v4
	v_mov_b32_e32 v50, v4
	v_mov_b32_e32 v51, v4
	v_mov_b32_e32 v60, v4
	v_mov_b32_e32 v61, v4
	v_mov_b32_e32 v62, v4
	v_mov_b32_e32 v63, v4
	v_mov_b32_e32 v64, v4
	v_mov_b32_e32 v65, v4
	v_mov_b32_e32 v66, v4
	v_mov_b32_e32 v67, v4
	v_mov_b32_e32 v68, v4
	v_mov_b32_e32 v69, v4
	v_mov_b32_e32 v70, v4
	v_mov_b32_e32 v71, v4
	v_mov_b32_e32 v72, v4
	v_mov_b32_e32 v73, v4
	v_mov_b32_e32 v74, v4
	v_mov_b32_e32 v75, v4
	v_mov_b32_e32 v84, v4
	v_mov_b32_e32 v85, v4
	v_mov_b32_e32 v86, v4
	v_mov_b32_e32 v87, v4
	v_mov_b32_e32 v88, v4
	v_mov_b32_e32 v89, v4
	v_mov_b32_e32 v90, v4
	v_mov_b32_e32 v91, v4
	v_mov_b32_e32 v100, v4
	v_mov_b32_e32 v101, v4
	v_mov_b32_e32 v102, v4
	v_mov_b32_e32 v103, v4
	v_mov_b32_e32 v104, v4
	v_mov_b32_e32 v105, v4
	v_mov_b32_e32 v106, v4
	v_mov_b32_e32 v107, v4
	v_mov_b32_e32 v116, v4
	v_mov_b32_e32 v117, v4
	v_mov_b32_e32 v118, v4
	v_mov_b32_e32 v119, v4
	v_mov_b32_e32 v120, v4
	v_mov_b32_e32 v121, v4
	v_mov_b32_e32 v122, v4
	v_mov_b32_e32 v123, v4
	v_mov_b32_e32 v76, v4
	v_mov_b32_e32 v77, v4
	v_mov_b32_e32 v78, v4
	v_mov_b32_e32 v79, v4
	v_mov_b32_e32 v80, v4
	v_mov_b32_e32 v81, v4
	v_mov_b32_e32 v82, v4
	v_mov_b32_e32 v83, v4
	v_mov_b32_e32 v92, v4
	v_mov_b32_e32 v93, v4
	v_mov_b32_e32 v94, v4
	v_mov_b32_e32 v95, v4
	v_mov_b32_e32 v96, v4
	v_mov_b32_e32 v97, v4
	v_mov_b32_e32 v98, v4
	v_mov_b32_e32 v99, v4
	v_mov_b32_e32 v108, v4
	v_mov_b32_e32 v109, v4
	v_mov_b32_e32 v110, v4
	v_mov_b32_e32 v111, v4
	v_mov_b32_e32 v112, v4
	v_mov_b32_e32 v113, v4
	v_mov_b32_e32 v114, v4
	v_mov_b32_e32 v115, v4
	v_mov_b32_e32 v124, v4
	v_mov_b32_e32 v125, v4
	v_mov_b32_e32 v126, v4
	v_mov_b32_e32 v127, v4
	v_mov_b32_e32 v128, v4
	v_mov_b32_e32 v129, v4
	v_mov_b32_e32 v130, v4
	v_mov_b32_e32 v131, v4
	s_andn2_b64 vcc, exec, s[14:15]
	s_cbranch_vccnz .LBB0_1304
	s_branch .LBB0_1305

; #define GAS __attribute__((address_space(1)))
; __device__ __forceinline__ unsigned xb_add(unsigned* p, unsigned v) { return __hip_atomic_fetch_add(p, v, __ATOMIC_RELAXED, __HIP_MEMORY_SCOPE_AGENT); }
; #define SEAM_LOCAL(k) do { if (IN(k) && IN((k) + 1)) { TBAR0(); xcd_barrier(bar, true, true); TBAR1(); } } while (0)
; __device__ __forceinline__ void xcd_barrier(const XcdBarrier& b, const bool group_local = false, const bool xcc_only = false) {
;     asm volatile("s_waitcnt vmcnt(0)" ::: "memory");
;     __syncthreads();
;     if (threadIdx.x == 0) {
;         GAS unsigned* barg = (GAS unsigned*)b.bar; asm volatile("" : "+s"(barg)); unsigned* bar = (unsigned*)barg;
;         __builtin_amdgcn_s_waitcnt(0);
;         unsigned nloc = b.st[0], nx = b.st[1];
;         if (nloc == 0u) { xcd_barrier_complete(bar, b.x, nloc, nx); b.st[0] = nloc; b.st[1] = nx; }
;         const unsigned old = xb_add(&bar[XB_XSUB(b.x)], 1u);
; __global__ void __launch_bounds__(NWAVES * 64, 2) mk_fwd(Args args) {
;     ...
;             SEAM_LOCAL(pb + 3);
.LBB0_1358:
	v_readlane_b32 s0, v255, 23
	s_add_i32 s22, s0, 5
	v_readlane_b32 s0, v255, 6
	v_readlane_b32 s1, v255, 7
	s_cmp_ge_i32 s22, s1
	s_cbranch_scc1 .LBB0_1434
	s_waitcnt vmcnt(0)
	s_waitcnt vmcnt(0) lgkmcnt(0)
	s_barrier
	s_setprio 0
	s_mov_b64 s[14:15], exec
	v_readlane_b32 s0, v255, 43
	v_readlane_b32 s1, v255, 44
	s_and_b64 s[0:1], s[14:15], s[0:1]
	s_mov_b64 exec, s[0:1]
	s_cbranch_execz .LBB0_1433
	v_readlane_b32 s0, v255, 10
	v_readlane_b32 s4, v255, 12
	v_readlane_b32 s1, v255, 11
	s_waitcnt vmcnt(0) expcnt(0) lgkmcnt(0)
	v_mov_b32_e32 v4, s4
	ds_read_b32 v2, v4
	ds_read_b32 v6, v4 offset:4
	s_waitcnt lgkmcnt(1)
	v_cmp_ne_u32_e32 vcc, 0, v2
	s_cbranch_vccnz .LBB0_1375
	v_readlane_b32 s4, v255, 0
	v_readlane_b32 s5, v255, 1
	s_load_dwordx2 s[8:9], s[4:5], 0x4
	v_readlane_b32 s4, v255, 47
	s_lshl_b32 s4, s4, 2
	s_add_u32 s4, s0, s4
	s_addc_u32 s5, s1, 0
	s_add_u32 s6, s0, 0x1000
	s_addc_u32 s7, s1, 0
	s_waitcnt lgkmcnt(0)
	s_mul_i32 s23, s8, s33
	s_add_u32 s8, s0, 0x1100
	s_mul_i32 s23, s23, s9
	s_addc_u32 s9, s1, 0
	s_add_u32 s10, s0, 0x1200
	s_addc_u32 s11, s1, 0
	s_add_u32 s12, s0, 0x1300
	s_addc_u32 s13, s1, 0
	s_mov_b32 s24, 1
	s_branch .LBB0_1363

;     __device__ __forceinline__ void a_ready(const Unit&) const { if (++ncall == 3 && sig != nullptr && threadIdx.x == 0) __hip_atomic_fetch_add(sig, 1u, __ATOMIC_RELAXED, __HIP_MEMORY_SCOPE_AGENT); }
; __device__ __forceinline__ f32x4 load_row_partials(const float* rsp, int pm, int tid) { f32x4 p = {0.f, 0.f, 0.f, 0.f}; if (tid < BM) p = *(const f32x4*)(rsp + (size_t)(pm * BM + tid) * 4); return p; }
; #define PG8_BAR __builtin_amdgcn_s_barrier()
; template <class Epi, class Sched, bool ALIGN_EPI = false, bool SP2 = false>
; __device__ __forceinline__ void gemm_phase(PG8_LAS unsigned char* lds, const Gemm g, const Sched& S, const Epi& E) {
;     ...
;     for (int i = 0; i < 2; ++i) { int R, C; stage_rc(tid * 16 + i * 8192, R, C); const int Rb = Epi::PERM ? ((R & ~31) + perm32(R & 31)) : R;
;         voffA[i] = (unsigned)(R * K + C) * 2u; voffB[i] = (unsigned)(Rb * K + C) * 2u; }
;     const size_t kstep = (size_t)(BK * 2);
;     const size_t hstep = (size_t)HALF * K * 2;
;     const size_t tstep = 2 * hstep;
;     const unsigned ldsw = (unsigned)wid * 1024u;
;     const int aoff = lds_byte(wr * 64 + fr, fq * 8), boff = lds_byte(wc * 32 + fr, fq * 8);
;     ...
;     Unit cur, nxt; int ui = 0;
;     ...
;     unsigned pg8_probe_acc = 0u;
;     ...
;     if (!S.next(0, cur)) return;
;     ...
;     const unsigned long long tramp_ = __builtin_amdgcn_s_memrealtime();
;     ...
;     static_assert(!Epi::ROWSCALE || SP2, "row factors are staged in the SP2 prologue");
;     f32x4 rowp_ = {0.f, 0.f, 0.f, 0.f}; if constexpr (Epi::ROWSCALE) rowp_ = load_row_partials(E.rsp, cur.pm, tid);
;     f32x4 acc[2][2][4][2];
; #pragma unroll
;     for (int a = 0; a < 2; ++a)
; #pragma unroll
;         for (int b = 0; b < 2; ++b)
; #pragma unroll
;             for (int m = 0; m < 4; ++m)
; #pragma unroll
;                 for (int n = 0; n < 2; ++n) acc[a][b][m][n] = (f32x4){0.f, 0.f, 0.f, 0.f};
;     bf16x8 At[4][2], B0[2][2], B1[2][2];
;     const char* cA = (const char*)g.A + (size_t)cur.pm * tstep + (cur.half == 2 ? hstep : (size_t)0); const char* cB = (const char*)g.Bt + (size_t)cur.pn * tstep;
;     S.a_ready(cur);
;     if constexpr (SP2) {
;         PG8_STAGE(PG8_SB(0, 0), cB, voffB); PG8_STAGE(PG8_SB(0, 1), cB + hstep, voffB); PG8_STAGE(PG8_SA(0, 0), cA, voffA); PG8_STAGE(PG8_SA(0, 1), cA + hstep, voffA);
;         if (wr == 1) PG8_BAR;
.LBB0_1467:
	s_or_b64 exec, exec, s[0:1]
	v_ashrrev_i32_e32 v2, 31, v16
	v_lshrrev_b32_e32 v2, 26, v2
	v_add_u32_e32 v2, v16, v2
	v_ashrrev_i32_e32 v17, 6, v2
	v_bfe_i32 v2, v16, 27, 1
	v_lshlrev_b32_e32 v8, 4, v16
	v_lshrrev_b32_e32 v2, 22, v2
	v_add_u32_e32 v2, v8, v2
	v_and_b32_e32 v2, 0xfffffc00, v2
	v_sub_u32_e32 v2, v8, v2
	v_lshrrev_b32_e32 v9, 4, v2
	v_bitop3_b32 v2, v9, v2, 32 bitop3:0x6c
	v_ashrrev_i32_e32 v10, 31, v2
	v_lshrrev_b32_e32 v10, 26, v10
	v_add_u32_e32 v10, v2, v10
	v_lshlrev_b32_e32 v9, 3, v17
	v_ashrrev_i32_e32 v18, 6, v10
	v_and_b32_e32 v10, 0xc0, v10
	v_and_b32_e32 v9, -16, v9
	v_sub_u32_e32 v2, v2, v10
	v_add_u32_e32 v9, v18, v9
	v_ashrrev_i16_sdwa v2, v224, sext(v2) dst_sel:DWORD dst_unused:UNUSED_PAD src0_sel:DWORD src1_sel:BYTE_0
	v_lshlrev_b32_e32 v11, 5, v17
	v_bfe_i32 v19, v2, 0, 16
	v_lshlrev_b32_e32 v2, 1, v9
	v_lshrrev_b32_e32 v10, 2, v9
	v_and_b32_e32 v12, 3, v18
	s_mov_b32 s0, 0x1fffe0
	v_and_b32_e32 v11, 32, v11
	v_and_b32_e32 v2, 24, v2
	v_and_b32_e32 v10, 4, v10
	v_and_or_b32 v12, v9, s0, v12
	v_or3_b32 v2, v12, v10, v2
	v_add_lshl_u32 v10, v11, v19, 1
	v_add_u32_e32 v8, 0x2000, v8
	v_lshl_add_u32 v132, v9, 11, v10
	v_ashrrev_i32_e32 v9, 31, v8
	v_lshrrev_b32_e32 v9, 22, v9
	v_add_u32_e32 v9, v8, v9
	v_ashrrev_i32_e32 v20, 10, v9
	v_mul_i32_i24_e32 v9, 0x400, v20
	v_sub_u32_e32 v8, v8, v9
	v_lshrrev_b32_e32 v9, 4, v8
	v_bitop3_b32 v8, v9, v8, 32 bitop3:0x6c
	v_lshl_add_u32 v2, v2, 11, v10
	v_ashrrev_i32_e32 v10, 31, v8
	v_lshrrev_b32_e32 v10, 26, v10
	v_lshlrev_b32_e32 v9, 3, v20
	v_add_u32_e32 v10, v8, v10
	v_and_b32_e32 v9, -16, v9
	v_ashrrev_i32_e32 v21, 6, v10
	v_add_u32_e32 v9, v21, v9
	v_and_b32_e32 v12, 3, v21
	s_ashr_i32 s29, s18, 6
	s_mul_i32 s36, s77, 0xee0000
	s_ashr_i32 s28, s18, 8
	v_and_or_b32 v12, v9, s0, v12
	s_lshl_b32 s25, s29, 10
	s_lshl_b64 s[0:1], s[36:37], 1
	s_add_u32 s0, s10, s0
	s_addc_u32 s1, s11, s1
	s_add_u32 s30, s10, 0x14000000
	s_addc_u32 s31, s11, 0
	s_waitcnt lgkmcnt(0)
	s_sext_i32_i16 s20, s8
	s_add_u32 s34, s0, 0x1500000
	v_and_b32_e32 v10, 0xc0, v10
	s_addc_u32 s35, s1, 0
	s_ashr_i32 s15, s14, 31
	s_ashr_i32 s21, s20, 31
	v_sub_u32_e32 v8, v8, v10
	s_lshl_b64 s[8:9], s[14:15], 19
	s_lshl_b64 s[0:1], s[20:21], 19
	v_ashrrev_i16_sdwa v8, v224, sext(v8) dst_sel:DWORD dst_unused:UNUSED_PAD src0_sel:DWORD src1_sel:BYTE_0
	s_add_u32 s0, s34, s0
	v_lshlrev_b32_e32 v11, 5, v20
	v_bfe_i32 v22, v8, 0, 16
	v_lshlrev_b32_e32 v8, 1, v9
	v_lshrrev_b32_e32 v10, 2, v9
	s_addc_u32 s1, s35, s1
	s_add_i32 s15, s25, 0
	v_and_b32_e32 v11, 32, v11
	v_and_b32_e32 v8, 24, v8
	v_and_b32_e32 v10, 4, v10
	s_add_i32 m0, s15, 0x10000
	v_or3_b32 v8, v12, v10, v8
	v_add_lshl_u32 v10, v11, v22, 1
	global_load_lds_dwordx4 v2, s[0:1]
	s_add_i32 m0, s15, 0x12000
	v_lshl_add_u32 v136, v8, 11, v10
	s_add_u32 s16, s0, 0x40000
	global_load_lds_dwordx4 v136, s[0:1]
	s_addc_u32 s17, s1, 0
	s_add_i32 m0, s15, 0x14000
	v_lshl_add_u32 v134, v9, 11, v10
	global_load_lds_dwordx4 v2, s[16:17]
	s_add_i32 m0, s15, 0x16000
	s_add_u32 s26, s30, s8
	s_addc_u32 s27, s31, s9
	s_add_i32 s21, s15, 0x2000
	global_load_lds_dwordx4 v136, s[16:17]
	s_mov_b32 m0, s15
	s_add_u32 s8, s26, 0x40000
	global_load_lds_dwordx4 v132, s[26:27]
	s_mov_b32 m0, s21
	s_addc_u32 s9, s27, 0
	s_add_i32 s36, s15, 0x4000
	global_load_lds_dwordx4 v134, s[26:27]
	s_mov_b32 m0, s36
	s_add_i32 s40, s15, 0x6000
	global_load_lds_dwordx4 v132, s[8:9]
	s_mov_b32 m0, s40
	s_cmp_eq_u32 s28, 1
	global_load_lds_dwordx4 v134, s[8:9]
	s_cselect_b64 s[8:9], -1, 0
	s_cmp_lg_u32 s28, 1
	s_cbranch_scc1 .LBB0_1469
	s_setprio 1
	s_barrier

; #define PG8_STAGE(bufoff, gbase, voff) do { _Pragma("unroll") for (int _i = 0; _i < 2; ++_i) \
;         __builtin_amdgcn_global_load_lds((const unsigned*)((const char*)(gbase) + (voff)[_i]), (PG8_LAS unsigned*)(lds + (bufoff) + ldsw + _i * 8192), 16, 0, 0); } while (0)
; #define PG8_LDA(dst, b, h) do { _Pragma("unroll") for (int m = 0; m < 4; ++m) _Pragma("unroll") for (int k = 0; k < 2; ++k) dst[m][k] = *(const PG8_LAS bf16x8*)(lds + PG8_SA(b, h) + aoff + m * 2048 + k * 1024); } while (0)
; #define PG8_LDB(dst, b, h) do { _Pragma("unroll") for (int n = 0; n < 2; ++n) _Pragma("unroll") for (int k = 0; k < 2; ++k) dst[n][k] = *(const PG8_LAS bf16x8*)(lds + PG8_SB(b, h) + boff + n * 2048 + k * 1024); } while (0)
; #define PG8_MMA(ai, bj, At, Bt) do { __builtin_amdgcn_s_setprio(1); _Pragma("unroll") for (int m = 0; m < 4; ++m) _Pragma("unroll") for (int n = 0; n < 2; ++n) _Pragma("unroll") for (int k = 0; k < 2; ++k) \
;         acc[ai][bj][m][n] = __builtin_amdgcn_mfma_f32_16x16x32_bf16(Bt[n][k], At[m][k], acc[ai][bj][m][n], 0, 0, 0); __builtin_amdgcn_s_setprio(0); } while (0)
; #define PG8_WAIT_V(n) asm volatile("s_waitcnt vmcnt(" #n ")" ::: "memory")
; #define PG8_WAIT_L(n) asm volatile("s_waitcnt lgkmcnt(" #n ")" ::: "memory")
; #define PG8_BAR __builtin_amdgcn_s_barrier()
; #define PG8_SCHED __builtin_amdgcn_sched_barrier(0)
; template <class Epi, class Sched, bool ALIGN_EPI = false, bool SP2 = false>
; __device__ __forceinline__ void gemm_phase(PG8_LAS unsigned char* lds, const Gemm g, const Sched& S, const Epi& E) {
;     ...
;             PG8_LDB(B0, 0, 0); PG8_LDB(B1, 0, 1); PG8_SCHED; PG8_LDA(At, 0, 0); PG8_STAGE(PG8_SA(1, 1), a1 + hstep, voffA);
;     ...
;             if (PROBE_KIND == 18 && t == 0 && ui > 0 && g.probe) { const unsigned long long tq_ = __builtin_amdgcn_s_memrealtime(); PG8_WAIT_V(8); pg8_probe_acc += (unsigned)(__builtin_amdgcn_s_memrealtime() - tq_); }
;     ...
;             PG8_WAIT_V(8); PG8_WAIT_L(0); PG8_BAR; PG8_MMA(0, 0, At, B0); PG8_MMA(0, 1, At, B1); PG8_BAR; PG8_SCHED;
;             PG8_LDA(At, 0, 1); PG8_STAGE(PG8_SB(0, 0), b2, voffB); PG8_STAGE(PG8_SB(0, 1), b2 + hstep, voffB); PG8_STAGE(PG8_SA(0, 0), a2, voffA);
;             PG8_WAIT_V(8); PG8_WAIT_L(0); PG8_BAR; if (cur.half == 0) { PG8_MMA(1, 0, At, B0); PG8_MMA(1, 1, At, B1); } PG8_BAR; PG8_SCHED;
.Lpj_gu_1:
	s_waitcnt lgkmcnt(0)
	s_barrier
	s_waitcnt lgkmcnt(0)
	v_mfma_f32_16x16x32_bf16 v[128:131], v[142:145], v[180:183], 0
	v_mfma_f32_16x16x32_bf16 v[124:127], v[156:159], v[180:183], 0
	v_mfma_f32_16x16x32_bf16 v[112:115], v[142:145], v[188:191], 0
	v_mfma_f32_16x16x32_bf16 v[108:111], v[156:159], v[188:191], 0
	v_mfma_f32_16x16x32_bf16 v[96:99], v[142:145], v[196:199], 0
	v_mfma_f32_16x16x32_bf16 v[92:95], v[156:159], v[196:199], 0
	v_mfma_f32_16x16x32_bf16 v[80:83], v[142:145], v[204:207], 0
	v_mfma_f32_16x16x32_bf16 v[76:79], v[156:159], v[204:207], 0
	v_mfma_f32_16x16x32_bf16 v[128:131], v[152:155], v[184:187], v[128:131]
	v_mfma_f32_16x16x32_bf16 v[124:127], v[160:163], v[184:187], v[124:127]
	v_mfma_f32_16x16x32_bf16 v[112:115], v[152:155], v[192:195], v[112:115]
	v_mfma_f32_16x16x32_bf16 v[108:111], v[160:163], v[192:195], v[108:111]
	v_mfma_f32_16x16x32_bf16 v[96:99], v[152:155], v[200:203], v[96:99]
	v_mfma_f32_16x16x32_bf16 v[92:95], v[160:163], v[200:203], v[92:95]
	v_mfma_f32_16x16x32_bf16 v[80:83], v[152:155], v[208:211], v[80:83]
	v_mfma_f32_16x16x32_bf16 v[76:79], v[160:163], v[208:211], v[76:79]
	v_mfma_f32_16x16x32_bf16 v[120:123], v[164:167], v[180:183], 0
	v_mfma_f32_16x16x32_bf16 v[116:119], v[172:175], v[180:183], 0
	v_mfma_f32_16x16x32_bf16 v[104:107], v[164:167], v[188:191], 0
	v_mfma_f32_16x16x32_bf16 v[100:103], v[172:175], v[188:191], 0
	v_mfma_f32_16x16x32_bf16 v[88:91], v[164:167], v[196:199], 0
	v_mfma_f32_16x16x32_bf16 v[84:87], v[172:175], v[196:199], 0
	v_mfma_f32_16x16x32_bf16 v[72:75], v[164:167], v[204:207], 0
	v_mfma_f32_16x16x32_bf16 v[68:71], v[172:175], v[204:207], 0
	v_mfma_f32_16x16x32_bf16 v[120:123], v[168:171], v[184:187], v[120:123]
	v_mfma_f32_16x16x32_bf16 v[116:119], v[176:179], v[184:187], v[116:119]
	v_mfma_f32_16x16x32_bf16 v[104:107], v[168:171], v[192:195], v[104:107]
	v_mfma_f32_16x16x32_bf16 v[100:103], v[176:179], v[192:195], v[100:103]
	v_mfma_f32_16x16x32_bf16 v[88:91], v[168:171], v[200:203], v[88:91]
	v_mfma_f32_16x16x32_bf16 v[84:87], v[176:179], v[200:203], v[84:87]
	v_mfma_f32_16x16x32_bf16 v[72:75], v[168:171], v[208:211], v[72:75]
	v_mfma_f32_16x16x32_bf16 v[68:71], v[176:179], v[208:211], v[68:71]
	s_barrier
	s_add_i32 s67, s67, s25
	v_lshl_add_u64 v[212:213], s[0:1], 0, v[2:3]
	s_mov_b32 m0, s67
	ds_read_b128 v[180:183], v150 offset:16384
	ds_read_b128 v[184:187], v150 offset:17408
	ds_read_b128 v[188:191], v150 offset:18432
	ds_read_b128 v[192:195], v150 offset:19456
	ds_read_b128 v[196:199], v150 offset:20480
	ds_read_b128 v[200:203], v150 offset:21504
	ds_read_b128 v[204:207], v150 offset:22528
	ds_read_b128 v[208:211], v150 offset:23552
	global_load_lds_dwordx4 v[212:213], off
	s_add_i32 m0, s67, 0x2000
	s_add_u32 s68, s0, 0x40000
	v_lshl_add_u64 v[214:215], s[0:1], 0, v[136:137]
	s_addc_u32 s69, s1, 0
	s_add_i32 s67, s70, s25
	global_load_lds_dwordx4 v[214:215], off
	v_lshl_add_u64 v[216:217], s[68:69], 0, v[2:3]
	s_mov_b32 m0, s67
	v_lshl_add_u64 v[218:219], s[28:29], 0, v[134:135]
	global_load_lds_dwordx4 v[216:217], off
	v_lshl_add_u64 v[216:217], s[68:69], 0, v[136:137]
	s_add_i32 m0, s67, 0x2000
	s_nop 0
	global_load_lds_dwordx4 v[216:217], off
	v_lshl_add_u64 v[216:217], s[28:29], 0, v[132:133]
	s_mov_b32 m0, s15
	s_nop 0
	global_load_lds_dwordx4 v[216:217], off
	s_mov_b32 m0, s21
	s_nop 0
	global_load_lds_dwordx4 v[218:219], off
	s_cmp_eq_u32 s32, 0
	s_cbranch_scc1 .Lpw_gu_2
	s_waitcnt vmcnt(16)
	s_branch .Lpj_gu_2
	.p2align 6
	s_nop 0
	s_nop 0
	s_nop 0
	s_nop 0
	s_nop 0

; #define PG8_STAGE(bufoff, gbase, voff) do { _Pragma("unroll") for (int _i = 0; _i < 2; ++_i) \
;         __builtin_amdgcn_global_load_lds((const unsigned*)((const char*)(gbase) + (voff)[_i]), (PG8_LAS unsigned*)(lds + (bufoff) + ldsw + _i * 8192), 16, 0, 0); } while (0)
; #define PG8_LDA(dst, b, h) do { _Pragma("unroll") for (int m = 0; m < 4; ++m) _Pragma("unroll") for (int k = 0; k < 2; ++k) dst[m][k] = *(const PG8_LAS bf16x8*)(lds + PG8_SA(b, h) + aoff + m * 2048 + k * 1024); } while (0)
; #define PG8_LDB(dst, b, h) do { _Pragma("unroll") for (int n = 0; n < 2; ++n) _Pragma("unroll") for (int k = 0; k < 2; ++k) dst[n][k] = *(const PG8_LAS bf16x8*)(lds + PG8_SB(b, h) + boff + n * 2048 + k * 1024); } while (0)
; #define PG8_WAIT_V(n) asm volatile("s_waitcnt vmcnt(" #n ")" ::: "memory")
; #define PG8_WAIT_L(n) asm volatile("s_waitcnt lgkmcnt(" #n ")" ::: "memory")
; template <class Epi, class Sched, bool ALIGN_EPI = false, bool SP2 = false>
; __device__ __forceinline__ void gemm_phase(PG8_LAS unsigned char* lds, const Gemm g, const Sched& S, const Epi& E) {
;     ...
;             PG8_LDB(B0, 0, 0); PG8_LDB(B1, 0, 1); PG8_SCHED; PG8_LDA(At, 0, 0); PG8_STAGE(PG8_SA(1, 1), a1 + hstep, voffA);
;     ...
;             if (PROBE_KIND == 18 && t == 0 && ui > 0 && g.probe) { const unsigned long long tq_ = __builtin_amdgcn_s_memrealtime(); PG8_WAIT_V(8); pg8_probe_acc += (unsigned)(__builtin_amdgcn_s_memrealtime() - tq_); }
;     ...
;             PG8_WAIT_V(8); PG8_WAIT_L(0); PG8_BAR; PG8_MMA(0, 0, At, B0); PG8_MMA(0, 1, At, B1); PG8_BAR; PG8_SCHED;
;             PG8_LDA(At, 0, 1); PG8_STAGE(PG8_SB(0, 0), b2, voffB); PG8_STAGE(PG8_SB(0, 1), b2 + hstep, voffB); PG8_STAGE(PG8_SA(0, 0), a2, voffA);
;             PG8_WAIT_V(8); PG8_WAIT_L(0); PG8_BAR; if (cur.half == 0) { PG8_MMA(1, 0, At, B0); PG8_MMA(1, 1, At, B1); } PG8_BAR; PG8_SCHED;
;             PG8_LDB(B0, 1, 0); PG8_LDB(B1, 1, 1); PG8_SCHED; PG8_LDA(At, 1, 0); PG8_STAGE(PG8_SA(0, 1), a2 + hstep, voffA);
;             PG8_WAIT_V(8); PG8_WAIT_L(0); PG8_BAR; PG8_MMA(0, 0, At, B0); PG8_MMA(0, 1, At, B1); PG8_BAR; PG8_SCHED;
;             PG8_LDA(At, 1, 1); PG8_STAGE(PG8_SB(1, 0), b3, voffB); PG8_STAGE(PG8_SB(1, 1), b3 + hstep, voffB); PG8_STAGE(PG8_SA(1, 0), a3, voffA);
;             PG8_WAIT_V(8); PG8_WAIT_L(0); PG8_BAR; if (cur.half == 0) { PG8_MMA(1, 0, At, B0); PG8_MMA(1, 1, At, B1); } PG8_BAR; PG8_SCHED;
.Lpj_gu_2:
	s_waitcnt lgkmcnt(0)
	s_barrier
	s_waitcnt lgkmcnt(0)
	v_mfma_f32_16x16x32_bf16 v[64:67], v[142:145], v[180:183], 0
	v_mfma_f32_16x16x32_bf16 v[60:63], v[156:159], v[180:183], 0
	v_mfma_f32_16x16x32_bf16 v[48:51], v[142:145], v[188:191], 0
	v_mfma_f32_16x16x32_bf16 v[44:47], v[156:159], v[188:191], 0
	v_mfma_f32_16x16x32_bf16 v[32:35], v[142:145], v[196:199], 0
	v_mfma_f32_16x16x32_bf16 v[28:31], v[156:159], v[196:199], 0
	v_mfma_f32_16x16x32_bf16 v[16:19], v[142:145], v[204:207], 0
	v_mfma_f32_16x16x32_bf16 v[12:15], v[156:159], v[204:207], 0
	v_mfma_f32_16x16x32_bf16 v[64:67], v[152:155], v[184:187], v[64:67]
	v_mfma_f32_16x16x32_bf16 v[60:63], v[160:163], v[184:187], v[60:63]
	v_mfma_f32_16x16x32_bf16 v[48:51], v[152:155], v[192:195], v[48:51]
	v_mfma_f32_16x16x32_bf16 v[44:47], v[160:163], v[192:195], v[44:47]
	v_mfma_f32_16x16x32_bf16 v[32:35], v[152:155], v[200:203], v[32:35]
	v_mfma_f32_16x16x32_bf16 v[28:31], v[160:163], v[200:203], v[28:31]
	v_mfma_f32_16x16x32_bf16 v[16:19], v[152:155], v[208:211], v[16:19]
	v_mfma_f32_16x16x32_bf16 v[12:15], v[160:163], v[208:211], v[12:15]
	v_mfma_f32_16x16x32_bf16 v[56:59], v[164:167], v[180:183], 0
	v_mfma_f32_16x16x32_bf16 v[52:55], v[172:175], v[180:183], 0
	v_mfma_f32_16x16x32_bf16 v[40:43], v[164:167], v[188:191], 0
	v_mfma_f32_16x16x32_bf16 v[36:39], v[172:175], v[188:191], 0
	v_mfma_f32_16x16x32_bf16 v[24:27], v[164:167], v[196:199], 0
	v_mfma_f32_16x16x32_bf16 v[20:23], v[172:175], v[196:199], 0
	v_mfma_f32_16x16x32_bf16 v[8:11], v[164:167], v[204:207], 0
	v_mfma_f32_16x16x32_bf16 v[4:7], v[172:175], v[204:207], 0
	v_mfma_f32_16x16x32_bf16 v[56:59], v[168:171], v[184:187], v[56:59]
	v_mfma_f32_16x16x32_bf16 v[52:55], v[176:179], v[184:187], v[52:55]
	v_mfma_f32_16x16x32_bf16 v[40:43], v[168:171], v[192:195], v[40:43]
	v_mfma_f32_16x16x32_bf16 v[36:39], v[176:179], v[192:195], v[36:39]
	v_mfma_f32_16x16x32_bf16 v[24:27], v[168:171], v[200:203], v[24:27]
	v_mfma_f32_16x16x32_bf16 v[20:23], v[176:179], v[200:203], v[20:23]
	v_mfma_f32_16x16x32_bf16 v[8:11], v[168:171], v[208:211], v[8:11]
	v_mfma_f32_16x16x32_bf16 v[4:7], v[176:179], v[208:211], v[4:7]
	s_barrier
	s_add_i32 s67, 0, 0x18000
	v_add_u32_e32 v151, s67, v147
	s_add_i32 s68, 0, 0x1c000
	ds_read_b128 v[142:145], v151
	ds_read_b128 v[152:155], v151 offset:1024
	ds_read_b128 v[156:159], v151 offset:2048
	ds_read_b128 v[160:163], v151 offset:3072
	v_add_u32_e32 v151, s68, v147
	ds_read_b128 v[164:167], v151
	ds_read_b128 v[168:171], v151 offset:1024
	ds_read_b128 v[172:175], v151 offset:2048
	ds_read_b128 v[176:179], v151 offset:3072
	s_add_u32 s28, s28, 0x40000
	s_addc_u32 s29, s29, 0
	s_mov_b32 m0, s36
	v_lshl_add_u64 v[220:221], s[28:29], 0, v[132:133]
	ds_read_b128 v[180:183], v150 offset:32768
	ds_read_b128 v[184:187], v150 offset:33792
	ds_read_b128 v[188:191], v150 offset:34816
	ds_read_b128 v[192:195], v150 offset:35840
	ds_read_b128 v[196:199], v150 offset:36864
	ds_read_b128 v[200:203], v150 offset:37888
	ds_read_b128 v[204:207], v150 offset:38912
	ds_read_b128 v[208:211], v150 offset:39936
	global_load_lds_dwordx4 v[220:221], off
	v_lshl_add_u64 v[220:221], s[28:29], 0, v[134:135]
	s_mov_b32 m0, s40
	s_nop 0
	global_load_lds_dwordx4 v[220:221], off
	s_waitcnt vmcnt(8)
	s_waitcnt lgkmcnt(0)
	s_barrier
	s_waitcnt lgkmcnt(0)
	v_mfma_f32_16x16x32_bf16 v[128:131], v[142:145], v[180:183], v[128:131]
	v_mfma_f32_16x16x32_bf16 v[124:127], v[156:159], v[180:183], v[124:127]
	v_mfma_f32_16x16x32_bf16 v[112:115], v[142:145], v[188:191], v[112:115]
	v_mfma_f32_16x16x32_bf16 v[108:111], v[156:159], v[188:191], v[108:111]
	v_mfma_f32_16x16x32_bf16 v[96:99], v[142:145], v[196:199], v[96:99]
	v_mfma_f32_16x16x32_bf16 v[92:95], v[156:159], v[196:199], v[92:95]
	v_mfma_f32_16x16x32_bf16 v[80:83], v[142:145], v[204:207], v[80:83]
	v_mfma_f32_16x16x32_bf16 v[76:79], v[156:159], v[204:207], v[76:79]
	v_mfma_f32_16x16x32_bf16 v[128:131], v[152:155], v[184:187], v[128:131]
	v_mfma_f32_16x16x32_bf16 v[124:127], v[160:163], v[184:187], v[124:127]
	v_mfma_f32_16x16x32_bf16 v[112:115], v[152:155], v[192:195], v[112:115]
	v_mfma_f32_16x16x32_bf16 v[108:111], v[160:163], v[192:195], v[108:111]
	v_mfma_f32_16x16x32_bf16 v[96:99], v[152:155], v[200:203], v[96:99]
	v_mfma_f32_16x16x32_bf16 v[92:95], v[160:163], v[200:203], v[92:95]
	v_mfma_f32_16x16x32_bf16 v[80:83], v[152:155], v[208:211], v[80:83]
	v_mfma_f32_16x16x32_bf16 v[76:79], v[160:163], v[208:211], v[76:79]
	v_mfma_f32_16x16x32_bf16 v[120:123], v[164:167], v[180:183], v[120:123]
	v_mfma_f32_16x16x32_bf16 v[116:119], v[172:175], v[180:183], v[116:119]
	v_mfma_f32_16x16x32_bf16 v[104:107], v[164:167], v[188:191], v[104:107]
	v_mfma_f32_16x16x32_bf16 v[100:103], v[172:175], v[188:191], v[100:103]
	v_mfma_f32_16x16x32_bf16 v[88:91], v[164:167], v[196:199], v[88:91]
	v_mfma_f32_16x16x32_bf16 v[84:87], v[172:175], v[196:199], v[84:87]
	v_mfma_f32_16x16x32_bf16 v[72:75], v[164:167], v[204:207], v[72:75]
	v_mfma_f32_16x16x32_bf16 v[68:71], v[172:175], v[204:207], v[68:71]
	v_mfma_f32_16x16x32_bf16 v[120:123], v[168:171], v[184:187], v[120:123]
	v_mfma_f32_16x16x32_bf16 v[116:119], v[176:179], v[184:187], v[116:119]
	v_mfma_f32_16x16x32_bf16 v[104:107], v[168:171], v[192:195], v[104:107]
	v_mfma_f32_16x16x32_bf16 v[100:103], v[176:179], v[192:195], v[100:103]
	v_mfma_f32_16x16x32_bf16 v[88:91], v[168:171], v[200:203], v[88:91]
	v_mfma_f32_16x16x32_bf16 v[84:87], v[176:179], v[200:203], v[84:87]
	v_mfma_f32_16x16x32_bf16 v[72:75], v[168:171], v[208:211], v[72:75]
	v_mfma_f32_16x16x32_bf16 v[68:71], v[176:179], v[208:211], v[68:71]
	s_barrier
;     __device__ __forceinline__ void a_ready(const Unit&) const { if (++ncall == 3 && sig != nullptr && threadIdx.x == 0) __hip_atomic_fetch_add(sig, 1u, __ATOMIC_RELAXED, __HIP_MEMORY_SCOPE_AGENT); }
; #define PG8_LDA(dst, b, h) do { _Pragma("unroll") for (int m = 0; m < 4; ++m) _Pragma("unroll") for (int k = 0; k < 2; ++k) dst[m][k] = *(const PG8_LAS bf16x8*)(lds + PG8_SA(b, h) + aoff + m * 2048 + k * 1024); } while (0)
; template <class Epi, class Sched, bool ALIGN_EPI = false, bool SP2 = false>
; __device__ __forceinline__ void gemm_phase(PG8_LAS unsigned char* lds, const Gemm g, const Sched& S, const Epi& E) {
;     ...
;         for (int t = 0; t < nt; t += 2) {
;             const bool last = (t == nt - 2);
;             const char* a1 = cA + (size_t)(t + 1) * kstep;
;             const char* a2 = last ? nA : cA + (size_t)(t + 2) * kstep; const char* b2 = last ? nB : cB + (size_t)(t + 2) * kstep;
;             const char* a3 = a2 + kstep; const char* b3 = b2 + kstep;
;             if (last && has_next) S.a_ready(nxt);
;             if constexpr (SP2) {
;             PG8_LDB(B0, 0, 0); PG8_LDB(B1, 0, 1); PG8_SCHED; PG8_LDA(At, 0, 0); PG8_STAGE(PG8_SA(1, 1), a1 + hstep, voffA);
;     ...
;             if (PROBE_KIND == 18 && t == 0 && ui > 0 && g.probe) { const unsigned long long tq_ = __builtin_amdgcn_s_memrealtime(); PG8_WAIT_V(8); pg8_probe_acc += (unsigned)(__builtin_amdgcn_s_memrealtime() - tq_); }
;     ...
;             PG8_WAIT_V(8); PG8_WAIT_L(0); PG8_BAR; PG8_MMA(0, 0, At, B0); PG8_MMA(0, 1, At, B1); PG8_BAR; PG8_SCHED;
;             PG8_LDA(At, 0, 1); PG8_STAGE(PG8_SB(0, 0), b2, voffB); PG8_STAGE(PG8_SB(0, 1), b2 + hstep, voffB); PG8_STAGE(PG8_SA(0, 0), a2, voffA);
;             PG8_WAIT_V(8); PG8_WAIT_L(0); PG8_BAR; if (cur.half == 0) { PG8_MMA(1, 0, At, B0); PG8_MMA(1, 1, At, B1); } PG8_BAR; PG8_SCHED;
;             PG8_LDB(B0, 1, 0); PG8_LDB(B1, 1, 1); PG8_SCHED; PG8_LDA(At, 1, 0); PG8_STAGE(PG8_SA(0, 1), a2 + hstep, voffA);
;             PG8_WAIT_V(8); PG8_WAIT_L(0); PG8_BAR; PG8_MMA(0, 0, At, B0); PG8_MMA(0, 1, At, B1); PG8_BAR; PG8_SCHED;
;             PG8_LDA(At, 1, 1); PG8_STAGE(PG8_SB(1, 0), b3, voffB); PG8_STAGE(PG8_SB(1, 1), b3 + hstep, voffB); PG8_STAGE(PG8_SA(1, 0), a3, voffA);
;             PG8_WAIT_V(8); PG8_WAIT_L(0); PG8_BAR; if (cur.half == 0) { PG8_MMA(1, 0, At, B0); PG8_MMA(1, 1, At, B1); } PG8_BAR; PG8_SCHED;
	s_add_i32 s28, s67, s25
	v_lshl_add_u64 v[212:213], v[212:213], 0, s[42:43]
	s_mov_b32 m0, s28
	ds_read_b128 v[180:183], v150 offset:49152
	ds_read_b128 v[184:187], v150 offset:50176
	ds_read_b128 v[188:191], v150 offset:51200
	ds_read_b128 v[192:195], v150 offset:52224
	ds_read_b128 v[196:199], v150 offset:53248
	ds_read_b128 v[200:203], v150 offset:54272
	ds_read_b128 v[204:207], v150 offset:55296
	ds_read_b128 v[208:211], v150 offset:56320
	global_load_lds_dwordx4 v[212:213], off
	s_add_i32 m0, s28, 0x2000
	s_add_u32 s0, s0, 0x40080
	v_lshl_add_u64 v[212:213], v[214:215], 0, s[42:43]
	s_addc_u32 s1, s1, 0
	s_add_i32 s28, s68, s25
	global_load_lds_dwordx4 v[212:213], off
	v_lshl_add_u64 v[212:213], s[0:1], 0, v[2:3]
	s_mov_b32 m0, s28
	s_nop 0
	global_load_lds_dwordx4 v[212:213], off
	v_lshl_add_u64 v[212:213], s[0:1], 0, v[136:137]
	s_add_i32 m0, s28, 0x2000
	s_nop 0
	global_load_lds_dwordx4 v[212:213], off
	v_lshl_add_u64 v[212:213], v[216:217], 0, s[42:43]
	s_mov_b32 m0, s41
	s_nop 0
	global_load_lds_dwordx4 v[212:213], off
	v_lshl_add_u64 v[212:213], v[218:219], 0, s[42:43]
	s_mov_b32 m0, s60
	s_nop 0
	global_load_lds_dwordx4 v[212:213], off
	s_waitcnt vmcnt(8)
	s_waitcnt lgkmcnt(0)
	s_barrier
	s_waitcnt lgkmcnt(0)
	v_mfma_f32_16x16x32_bf16 v[64:67], v[142:145], v[180:183], v[64:67]
	v_mfma_f32_16x16x32_bf16 v[60:63], v[156:159], v[180:183], v[60:63]
	v_mfma_f32_16x16x32_bf16 v[48:51], v[142:145], v[188:191], v[48:51]
	v_mfma_f32_16x16x32_bf16 v[44:47], v[156:159], v[188:191], v[44:47]
	v_mfma_f32_16x16x32_bf16 v[32:35], v[142:145], v[196:199], v[32:35]
	v_mfma_f32_16x16x32_bf16 v[28:31], v[156:159], v[196:199], v[28:31]
	v_mfma_f32_16x16x32_bf16 v[16:19], v[142:145], v[204:207], v[16:19]
	v_mfma_f32_16x16x32_bf16 v[12:15], v[156:159], v[204:207], v[12:15]
	v_mfma_f32_16x16x32_bf16 v[64:67], v[152:155], v[184:187], v[64:67]
	v_mfma_f32_16x16x32_bf16 v[60:63], v[160:163], v[184:187], v[60:63]
	v_mfma_f32_16x16x32_bf16 v[48:51], v[152:155], v[192:195], v[48:51]
	v_mfma_f32_16x16x32_bf16 v[44:47], v[160:163], v[192:195], v[44:47]
	v_mfma_f32_16x16x32_bf16 v[32:35], v[152:155], v[200:203], v[32:35]
	v_mfma_f32_16x16x32_bf16 v[28:31], v[160:163], v[200:203], v[28:31]
	v_mfma_f32_16x16x32_bf16 v[16:19], v[152:155], v[208:211], v[16:19]
	v_mfma_f32_16x16x32_bf16 v[12:15], v[160:163], v[208:211], v[12:15]
	v_mfma_f32_16x16x32_bf16 v[56:59], v[164:167], v[180:183], v[56:59]
	v_mfma_f32_16x16x32_bf16 v[52:55], v[172:175], v[180:183], v[52:55]
	v_mfma_f32_16x16x32_bf16 v[40:43], v[164:167], v[188:191], v[40:43]
	v_mfma_f32_16x16x32_bf16 v[36:39], v[172:175], v[188:191], v[36:39]
	v_mfma_f32_16x16x32_bf16 v[24:27], v[164:167], v[196:199], v[24:27]
	v_mfma_f32_16x16x32_bf16 v[20:23], v[172:175], v[196:199], v[20:23]
	v_mfma_f32_16x16x32_bf16 v[8:11], v[164:167], v[204:207], v[8:11]
	v_mfma_f32_16x16x32_bf16 v[4:7], v[172:175], v[204:207], v[4:7]
	v_mfma_f32_16x16x32_bf16 v[56:59], v[168:171], v[184:187], v[56:59]
	v_mfma_f32_16x16x32_bf16 v[52:55], v[176:179], v[184:187], v[52:55]
	v_mfma_f32_16x16x32_bf16 v[40:43], v[168:171], v[192:195], v[40:43]
	v_mfma_f32_16x16x32_bf16 v[36:39], v[176:179], v[192:195], v[36:39]
	v_mfma_f32_16x16x32_bf16 v[24:27], v[168:171], v[200:203], v[24:27]
	v_mfma_f32_16x16x32_bf16 v[20:23], v[176:179], v[200:203], v[20:23]
	v_mfma_f32_16x16x32_bf16 v[8:11], v[168:171], v[208:211], v[8:11]
	v_mfma_f32_16x16x32_bf16 v[4:7], v[176:179], v[208:211], v[4:7]
	s_barrier
	s_add_i32 s66, s66, 2
	s_add_u32 s26, s26, 0x100
	s_addc_u32 s27, s27, 0
	s_add_u32 s64, s64, 0x100
	s_addc_u32 s65, s65, 0
	s_mov_b32 s32, 1
.LBB0_1477:
	s_add_u32 s0, s26, 0xfffc0080
	s_addc_u32 s1, s27, -1
	s_add_i32 s67, 0, 0x10000
	s_cmp_eq_u32 s66, 12
	s_cselect_b32 s29, s17, s1
	s_cselect_b32 s28, s62, s0
	v_add_u32_e32 v151, s67, v147
	s_cselect_b32 s1, s19, s65
	s_cselect_b32 s0, s63, s64
	s_add_i32 s70, 0, 0x14000
	ds_read_b128 v[142:145], v151
	ds_read_b128 v[152:155], v151 offset:1024
	ds_read_b128 v[156:159], v151 offset:2048
	ds_read_b128 v[160:163], v151 offset:3072
	v_add_u32_e32 v151, s70, v147
	ds_read_b128 v[164:167], v151
	ds_read_b128 v[168:171], v151 offset:1024
	ds_read_b128 v[172:175], v151 offset:2048
	ds_read_b128 v[176:179], v151 offset:3072
	v_lshl_add_u64 v[212:213], s[26:27], 0, v[138:139]
	s_add_i32 m0, s15, 0xc000
	ds_read_b128 v[180:183], v150
	ds_read_b128 v[184:187], v150 offset:1024
	ds_read_b128 v[188:191], v150 offset:2048
	ds_read_b128 v[192:195], v150 offset:3072
	ds_read_b128 v[196:199], v150 offset:4096
	ds_read_b128 v[200:203], v150 offset:5120
	ds_read_b128 v[204:207], v150 offset:6144
	ds_read_b128 v[208:211], v150 offset:7168
	global_load_lds_dwordx4 v[212:213], off
	v_lshl_add_u64 v[212:213], s[26:27], 0, v[140:141]
	s_add_i32 m0, s15, 0xe000
	s_nop 0
	global_load_lds_dwordx4 v[212:213], off
	s_waitcnt vmcnt(8)
	s_waitcnt lgkmcnt(0)
	s_barrier
; #define PG8_STAGE(bufoff, gbase, voff) do { _Pragma("unroll") for (int _i = 0; _i < 2; ++_i) \
;         __builtin_amdgcn_global_load_lds((const unsigned*)((const char*)(gbase) + (voff)[_i]), (PG8_LAS unsigned*)(lds + (bufoff) + ldsw + _i * 8192), 16, 0, 0); } while (0)
; #define PG8_LDA(dst, b, h) do { _Pragma("unroll") for (int m = 0; m < 4; ++m) _Pragma("unroll") for (int k = 0; k < 2; ++k) dst[m][k] = *(const PG8_LAS bf16x8*)(lds + PG8_SA(b, h) + aoff + m * 2048 + k * 1024); } while (0)
; #define PG8_LDB(dst, b, h) do { _Pragma("unroll") for (int n = 0; n < 2; ++n) _Pragma("unroll") for (int k = 0; k < 2; ++k) dst[n][k] = *(const PG8_LAS bf16x8*)(lds + PG8_SB(b, h) + boff + n * 2048 + k * 1024); } while (0)
; #define PG8_WAIT_V(n) asm volatile("s_waitcnt vmcnt(" #n ")" ::: "memory")
; #define PG8_WAIT_L(n) asm volatile("s_waitcnt lgkmcnt(" #n ")" ::: "memory")
; template <class Epi, class Sched, bool ALIGN_EPI = false, bool SP2 = false>
; __device__ __forceinline__ void gemm_phase(PG8_LAS unsigned char* lds, const Gemm g, const Sched& S, const Epi& E) {
;     ...
;             PG8_LDB(B0, 0, 0); PG8_LDB(B1, 0, 1); PG8_SCHED; PG8_LDA(At, 0, 0); PG8_STAGE(PG8_SA(1, 1), a1 + hstep, voffA);
;     ...
;             if (PROBE_KIND == 18 && t == 0 && ui > 0 && g.probe) { const unsigned long long tq_ = __builtin_amdgcn_s_memrealtime(); PG8_WAIT_V(8); pg8_probe_acc += (unsigned)(__builtin_amdgcn_s_memrealtime() - tq_); }
;     ...
;             PG8_WAIT_V(8); PG8_WAIT_L(0); PG8_BAR; PG8_MMA(0, 0, At, B0); PG8_MMA(0, 1, At, B1); PG8_BAR; PG8_SCHED;
;             PG8_LDA(At, 0, 1); PG8_STAGE(PG8_SB(0, 0), b2, voffB); PG8_STAGE(PG8_SB(0, 1), b2 + hstep, voffB); PG8_STAGE(PG8_SA(0, 0), a2, voffA);
;             PG8_WAIT_V(8); PG8_WAIT_L(0); PG8_BAR; if (cur.half == 0) { PG8_MMA(1, 0, At, B0); PG8_MMA(1, 1, At, B1); } PG8_BAR; PG8_SCHED;
;             PG8_LDB(B0, 1, 0); PG8_LDB(B1, 1, 1); PG8_SCHED; PG8_LDA(At, 1, 0); PG8_STAGE(PG8_SA(0, 1), a2 + hstep, voffA);
;             PG8_WAIT_V(8); PG8_WAIT_L(0); PG8_BAR; PG8_MMA(0, 0, At, B0); PG8_MMA(0, 1, At, B1); PG8_BAR; PG8_SCHED;
;             PG8_LDA(At, 1, 1); PG8_STAGE(PG8_SB(1, 0), b3, voffB); PG8_STAGE(PG8_SB(1, 1), b3 + hstep, voffB); PG8_STAGE(PG8_SA(1, 0), a3, voffA);
;             PG8_WAIT_V(8); PG8_WAIT_L(0); PG8_BAR; if (cur.half == 0) { PG8_MMA(1, 0, At, B0); PG8_MMA(1, 1, At, B1); } PG8_BAR; PG8_SCHED;
	s_waitcnt lgkmcnt(0)
	v_mfma_f32_16x16x32_bf16 v[128:131], v[142:145], v[180:183], v[128:131]
	v_mfma_f32_16x16x32_bf16 v[124:127], v[156:159], v[180:183], v[124:127]
	v_mfma_f32_16x16x32_bf16 v[112:115], v[142:145], v[188:191], v[112:115]
	v_mfma_f32_16x16x32_bf16 v[108:111], v[156:159], v[188:191], v[108:111]
	v_mfma_f32_16x16x32_bf16 v[96:99], v[142:145], v[196:199], v[96:99]
	v_mfma_f32_16x16x32_bf16 v[92:95], v[156:159], v[196:199], v[92:95]
	v_mfma_f32_16x16x32_bf16 v[80:83], v[142:145], v[204:207], v[80:83]
	v_mfma_f32_16x16x32_bf16 v[76:79], v[156:159], v[204:207], v[76:79]
	v_mfma_f32_16x16x32_bf16 v[128:131], v[152:155], v[184:187], v[128:131]
	v_mfma_f32_16x16x32_bf16 v[124:127], v[160:163], v[184:187], v[124:127]
	v_mfma_f32_16x16x32_bf16 v[112:115], v[152:155], v[192:195], v[112:115]
	v_mfma_f32_16x16x32_bf16 v[108:111], v[160:163], v[192:195], v[108:111]
	v_mfma_f32_16x16x32_bf16 v[96:99], v[152:155], v[200:203], v[96:99]
	v_mfma_f32_16x16x32_bf16 v[92:95], v[160:163], v[200:203], v[92:95]
	v_mfma_f32_16x16x32_bf16 v[80:83], v[152:155], v[208:211], v[80:83]
	v_mfma_f32_16x16x32_bf16 v[76:79], v[160:163], v[208:211], v[76:79]
	v_mfma_f32_16x16x32_bf16 v[120:123], v[164:167], v[180:183], v[120:123]
	v_mfma_f32_16x16x32_bf16 v[116:119], v[172:175], v[180:183], v[116:119]
	v_mfma_f32_16x16x32_bf16 v[104:107], v[164:167], v[188:191], v[104:107]
	v_mfma_f32_16x16x32_bf16 v[100:103], v[172:175], v[188:191], v[100:103]
	v_mfma_f32_16x16x32_bf16 v[88:91], v[164:167], v[196:199], v[88:91]
	v_mfma_f32_16x16x32_bf16 v[84:87], v[172:175], v[196:199], v[84:87]
	v_mfma_f32_16x16x32_bf16 v[72:75], v[164:167], v[204:207], v[72:75]
	v_mfma_f32_16x16x32_bf16 v[68:71], v[172:175], v[204:207], v[68:71]
	v_mfma_f32_16x16x32_bf16 v[120:123], v[168:171], v[184:187], v[120:123]
	v_mfma_f32_16x16x32_bf16 v[116:119], v[176:179], v[184:187], v[116:119]
	v_mfma_f32_16x16x32_bf16 v[104:107], v[168:171], v[192:195], v[104:107]
	v_mfma_f32_16x16x32_bf16 v[100:103], v[176:179], v[192:195], v[100:103]
	v_mfma_f32_16x16x32_bf16 v[88:91], v[168:171], v[200:203], v[88:91]
	v_mfma_f32_16x16x32_bf16 v[84:87], v[176:179], v[200:203], v[84:87]
	v_mfma_f32_16x16x32_bf16 v[72:75], v[168:171], v[208:211], v[72:75]
	v_mfma_f32_16x16x32_bf16 v[68:71], v[176:179], v[208:211], v[68:71]
	s_barrier
	s_add_i32 s67, s67, s25
	v_lshl_add_u64 v[212:213], s[0:1], 0, v[2:3]
	s_mov_b32 m0, s67
	ds_read_b128 v[180:183], v150 offset:16384
	ds_read_b128 v[184:187], v150 offset:17408
	ds_read_b128 v[188:191], v150 offset:18432
	ds_read_b128 v[192:195], v150 offset:19456
	ds_read_b128 v[196:199], v150 offset:20480
	ds_read_b128 v[200:203], v150 offset:21504
	ds_read_b128 v[204:207], v150 offset:22528
	ds_read_b128 v[208:211], v150 offset:23552
	global_load_lds_dwordx4 v[212:213], off
	s_add_i32 m0, s67, 0x2000
	s_add_u32 s68, s0, 0x40000
	v_lshl_add_u64 v[214:215], s[0:1], 0, v[136:137]
	s_addc_u32 s69, s1, 0
	s_add_i32 s67, s70, s25
	global_load_lds_dwordx4 v[214:215], off
	v_lshl_add_u64 v[216:217], s[68:69], 0, v[2:3]
	s_mov_b32 m0, s67
	v_lshl_add_u64 v[218:219], s[28:29], 0, v[134:135]
	global_load_lds_dwordx4 v[216:217], off
	v_lshl_add_u64 v[216:217], s[68:69], 0, v[136:137]
	s_add_i32 m0, s67, 0x2000
	s_nop 0
	global_load_lds_dwordx4 v[216:217], off
	v_lshl_add_u64 v[216:217], s[28:29], 0, v[132:133]
	s_mov_b32 m0, s15
	s_nop 0
	global_load_lds_dwordx4 v[216:217], off
	s_mov_b32 m0, s21
	s_nop 0
	global_load_lds_dwordx4 v[218:219], off
	s_waitcnt vmcnt(8)
	s_waitcnt lgkmcnt(0)
	s_barrier
	s_waitcnt lgkmcnt(0)
	v_mfma_f32_16x16x32_bf16 v[64:67], v[142:145], v[180:183], v[64:67]
	v_mfma_f32_16x16x32_bf16 v[60:63], v[156:159], v[180:183], v[60:63]
	v_mfma_f32_16x16x32_bf16 v[48:51], v[142:145], v[188:191], v[48:51]
	v_mfma_f32_16x16x32_bf16 v[44:47], v[156:159], v[188:191], v[44:47]
	v_mfma_f32_16x16x32_bf16 v[32:35], v[142:145], v[196:199], v[32:35]
	v_mfma_f32_16x16x32_bf16 v[28:31], v[156:159], v[196:199], v[28:31]
	v_mfma_f32_16x16x32_bf16 v[16:19], v[142:145], v[204:207], v[16:19]
	v_mfma_f32_16x16x32_bf16 v[12:15], v[156:159], v[204:207], v[12:15]
	v_mfma_f32_16x16x32_bf16 v[64:67], v[152:155], v[184:187], v[64:67]
	v_mfma_f32_16x16x32_bf16 v[60:63], v[160:163], v[184:187], v[60:63]
	v_mfma_f32_16x16x32_bf16 v[48:51], v[152:155], v[192:195], v[48:51]
	v_mfma_f32_16x16x32_bf16 v[44:47], v[160:163], v[192:195], v[44:47]
	v_mfma_f32_16x16x32_bf16 v[32:35], v[152:155], v[200:203], v[32:35]
	v_mfma_f32_16x16x32_bf16 v[28:31], v[160:163], v[200:203], v[28:31]
	v_mfma_f32_16x16x32_bf16 v[16:19], v[152:155], v[208:211], v[16:19]
	v_mfma_f32_16x16x32_bf16 v[12:15], v[160:163], v[208:211], v[12:15]
	v_mfma_f32_16x16x32_bf16 v[56:59], v[164:167], v[180:183], v[56:59]
	v_mfma_f32_16x16x32_bf16 v[52:55], v[172:175], v[180:183], v[52:55]
	v_mfma_f32_16x16x32_bf16 v[40:43], v[164:167], v[188:191], v[40:43]
	v_mfma_f32_16x16x32_bf16 v[36:39], v[172:175], v[188:191], v[36:39]
	v_mfma_f32_16x16x32_bf16 v[24:27], v[164:167], v[196:199], v[24:27]
	v_mfma_f32_16x16x32_bf16 v[20:23], v[172:175], v[196:199], v[20:23]
	v_mfma_f32_16x16x32_bf16 v[8:11], v[164:167], v[204:207], v[8:11]
	v_mfma_f32_16x16x32_bf16 v[4:7], v[172:175], v[204:207], v[4:7]
	v_mfma_f32_16x16x32_bf16 v[56:59], v[168:171], v[184:187], v[56:59]
	v_mfma_f32_16x16x32_bf16 v[52:55], v[176:179], v[184:187], v[52:55]
	v_mfma_f32_16x16x32_bf16 v[40:43], v[168:171], v[192:195], v[40:43]
	v_mfma_f32_16x16x32_bf16 v[36:39], v[176:179], v[192:195], v[36:39]
	v_mfma_f32_16x16x32_bf16 v[24:27], v[168:171], v[200:203], v[24:27]
	v_mfma_f32_16x16x32_bf16 v[20:23], v[176:179], v[200:203], v[20:23]
	v_mfma_f32_16x16x32_bf16 v[8:11], v[168:171], v[208:211], v[8:11]
	v_mfma_f32_16x16x32_bf16 v[4:7], v[176:179], v[208:211], v[4:7]
	s_barrier
; #define PG8_STAGE(bufoff, gbase, voff) do { _Pragma("unroll") for (int _i = 0; _i < 2; ++_i) \
;         __builtin_amdgcn_global_load_lds((const unsigned*)((const char*)(gbase) + (voff)[_i]), (PG8_LAS unsigned*)(lds + (bufoff) + ldsw + _i * 8192), 16, 0, 0); } while (0)
; #define PG8_LDA(dst, b, h) do { _Pragma("unroll") for (int m = 0; m < 4; ++m) _Pragma("unroll") for (int k = 0; k < 2; ++k) dst[m][k] = *(const PG8_LAS bf16x8*)(lds + PG8_SA(b, h) + aoff + m * 2048 + k * 1024); } while (0)
; #define PG8_LDB(dst, b, h) do { _Pragma("unroll") for (int n = 0; n < 2; ++n) _Pragma("unroll") for (int k = 0; k < 2; ++k) dst[n][k] = *(const PG8_LAS bf16x8*)(lds + PG8_SB(b, h) + boff + n * 2048 + k * 1024); } while (0)
; #define PG8_MMA(ai, bj, At, Bt) do { __builtin_amdgcn_s_setprio(1); _Pragma("unroll") for (int m = 0; m < 4; ++m) _Pragma("unroll") for (int n = 0; n < 2; ++n) _Pragma("unroll") for (int k = 0; k < 2; ++k) \
;         acc[ai][bj][m][n] = __builtin_amdgcn_mfma_f32_16x16x32_bf16(Bt[n][k], At[m][k], acc[ai][bj][m][n], 0, 0, 0); __builtin_amdgcn_s_setprio(0); } while (0)
; #define PG8_WAIT_V(n) asm volatile("s_waitcnt vmcnt(" #n ")" ::: "memory")
; #define PG8_WAIT_L(n) asm volatile("s_waitcnt lgkmcnt(" #n ")" ::: "memory")
; #define PG8_BAR __builtin_amdgcn_s_barrier()
; #define PG8_SCHED __builtin_amdgcn_sched_barrier(0)
; template <class Epi, class Sched, bool ALIGN_EPI = false, bool SP2 = false>
; __device__ __forceinline__ void gemm_phase(PG8_LAS unsigned char* lds, const Gemm g, const Sched& S, const Epi& E) {
;     ...
;             PG8_LDB(B0, 1, 0); PG8_LDB(B1, 1, 1); PG8_SCHED; PG8_LDA(At, 1, 0); PG8_STAGE(PG8_SA(0, 1), a2 + hstep, voffA);
;             PG8_WAIT_V(8); PG8_WAIT_L(0); PG8_BAR; PG8_MMA(0, 0, At, B0); PG8_MMA(0, 1, At, B1); PG8_BAR; PG8_SCHED;
	s_add_i32 s67, 0, 0x18000
	v_add_u32_e32 v151, s67, v147
	s_add_i32 s68, 0, 0x1c000
	ds_read_b128 v[142:145], v151
	ds_read_b128 v[152:155], v151 offset:1024
	ds_read_b128 v[156:159], v151 offset:2048
	ds_read_b128 v[160:163], v151 offset:3072
	v_add_u32_e32 v151, s68, v147
	ds_read_b128 v[164:167], v151
	ds_read_b128 v[168:171], v151 offset:1024
	ds_read_b128 v[172:175], v151 offset:2048
	ds_read_b128 v[176:179], v151 offset:3072
	s_add_u32 s28, s28, 0x40000
	s_addc_u32 s29, s29, 0
	s_mov_b32 m0, s36
	v_lshl_add_u64 v[220:221], s[28:29], 0, v[132:133]
	ds_read_b128 v[180:183], v150 offset:32768
	ds_read_b128 v[184:187], v150 offset:33792
	ds_read_b128 v[188:191], v150 offset:34816
	ds_read_b128 v[192:195], v150 offset:35840
	ds_read_b128 v[196:199], v150 offset:36864
	ds_read_b128 v[200:203], v150 offset:37888
	ds_read_b128 v[204:207], v150 offset:38912
	ds_read_b128 v[208:211], v150 offset:39936
	global_load_lds_dwordx4 v[220:221], off
	v_lshl_add_u64 v[220:221], s[28:29], 0, v[134:135]
	s_mov_b32 m0, s40
	s_nop 0
	global_load_lds_dwordx4 v[220:221], off
	s_waitcnt vmcnt(8)
	s_waitcnt lgkmcnt(0)
	s_barrier
	s_waitcnt lgkmcnt(0)
	v_mfma_f32_16x16x32_bf16 v[128:131], v[142:145], v[180:183], v[128:131]
	v_mfma_f32_16x16x32_bf16 v[124:127], v[156:159], v[180:183], v[124:127]
	v_mfma_f32_16x16x32_bf16 v[112:115], v[142:145], v[188:191], v[112:115]
	v_mfma_f32_16x16x32_bf16 v[108:111], v[156:159], v[188:191], v[108:111]
	v_mfma_f32_16x16x32_bf16 v[96:99], v[142:145], v[196:199], v[96:99]
	v_mfma_f32_16x16x32_bf16 v[92:95], v[156:159], v[196:199], v[92:95]
	v_mfma_f32_16x16x32_bf16 v[80:83], v[142:145], v[204:207], v[80:83]
	v_mfma_f32_16x16x32_bf16 v[76:79], v[156:159], v[204:207], v[76:79]
	v_mfma_f32_16x16x32_bf16 v[128:131], v[152:155], v[184:187], v[128:131]
	v_mfma_f32_16x16x32_bf16 v[124:127], v[160:163], v[184:187], v[124:127]
	v_mfma_f32_16x16x32_bf16 v[112:115], v[152:155], v[192:195], v[112:115]
	v_mfma_f32_16x16x32_bf16 v[108:111], v[160:163], v[192:195], v[108:111]
	v_mfma_f32_16x16x32_bf16 v[96:99], v[152:155], v[200:203], v[96:99]
	v_mfma_f32_16x16x32_bf16 v[92:95], v[160:163], v[200:203], v[92:95]
	v_mfma_f32_16x16x32_bf16 v[80:83], v[152:155], v[208:211], v[80:83]
	v_mfma_f32_16x16x32_bf16 v[76:79], v[160:163], v[208:211], v[76:79]
	v_mfma_f32_16x16x32_bf16 v[120:123], v[164:167], v[180:183], v[120:123]
	v_mfma_f32_16x16x32_bf16 v[116:119], v[172:175], v[180:183], v[116:119]
	v_mfma_f32_16x16x32_bf16 v[104:107], v[164:167], v[188:191], v[104:107]
	v_mfma_f32_16x16x32_bf16 v[100:103], v[172:175], v[188:191], v[100:103]
	v_mfma_f32_16x16x32_bf16 v[88:91], v[164:167], v[196:199], v[88:91]
	v_mfma_f32_16x16x32_bf16 v[84:87], v[172:175], v[196:199], v[84:87]
	v_mfma_f32_16x16x32_bf16 v[72:75], v[164:167], v[204:207], v[72:75]
	v_mfma_f32_16x16x32_bf16 v[68:71], v[172:175], v[204:207], v[68:71]
	v_mfma_f32_16x16x32_bf16 v[120:123], v[168:171], v[184:187], v[120:123]
	v_mfma_f32_16x16x32_bf16 v[116:119], v[176:179], v[184:187], v[116:119]
	v_mfma_f32_16x16x32_bf16 v[104:107], v[168:171], v[192:195], v[104:107]
	v_mfma_f32_16x16x32_bf16 v[100:103], v[176:179], v[192:195], v[100:103]
	v_mfma_f32_16x16x32_bf16 v[88:91], v[168:171], v[200:203], v[88:91]
	v_mfma_f32_16x16x32_bf16 v[84:87], v[176:179], v[200:203], v[84:87]
	v_mfma_f32_16x16x32_bf16 v[72:75], v[168:171], v[208:211], v[72:75]
	v_mfma_f32_16x16x32_bf16 v[68:71], v[176:179], v[208:211], v[68:71]
	s_barrier
;     __device__ __forceinline__ void a_ready(const Unit&) const { if (++ncall == 3 && sig != nullptr && threadIdx.x == 0) __hip_atomic_fetch_add(sig, 1u, __ATOMIC_RELAXED, __HIP_MEMORY_SCOPE_AGENT); }
; #define PG8_WAIT_V(n) asm volatile("s_waitcnt vmcnt(" #n ")" ::: "memory")
; #define PG8_WAIT_L(n) asm volatile("s_waitcnt lgkmcnt(" #n ")" ::: "memory")
; #define PG8_BAR __builtin_amdgcn_s_barrier()
; template <class Epi, class Sched, bool ALIGN_EPI = false, bool SP2 = false>
; __device__ __forceinline__ void gemm_phase(PG8_LAS unsigned char* lds, const Gemm g, const Sched& S, const Epi& E) {
;     ...
;         for (int t = 0; t < nt; t += 2) {
;             const bool last = (t == nt - 2);
;             const char* a1 = cA + (size_t)(t + 1) * kstep;
;             const char* a2 = last ? nA : cA + (size_t)(t + 2) * kstep; const char* b2 = last ? nB : cB + (size_t)(t + 2) * kstep;
;             const char* a3 = a2 + kstep; const char* b3 = b2 + kstep;
;             if (last && has_next) S.a_ready(nxt);
;             if constexpr (SP2) {
;             PG8_LDB(B0, 0, 0); PG8_LDB(B1, 0, 1); PG8_SCHED; PG8_LDA(At, 0, 0); PG8_STAGE(PG8_SA(1, 1), a1 + hstep, voffA);
;     ...
;             if (PROBE_KIND == 18 && t == 0 && ui > 0 && g.probe) { const unsigned long long tq_ = __builtin_amdgcn_s_memrealtime(); PG8_WAIT_V(8); pg8_probe_acc += (unsigned)(__builtin_amdgcn_s_memrealtime() - tq_); }
;     ...
;             PG8_WAIT_V(8); PG8_WAIT_L(0); PG8_BAR; PG8_MMA(0, 0, At, B0); PG8_MMA(0, 1, At, B1); PG8_BAR; PG8_SCHED;
;             PG8_LDA(At, 0, 1); PG8_STAGE(PG8_SB(0, 0), b2, voffB); PG8_STAGE(PG8_SB(0, 1), b2 + hstep, voffB); PG8_STAGE(PG8_SA(0, 0), a2, voffA);
;             PG8_WAIT_V(8); PG8_WAIT_L(0); PG8_BAR; if (cur.half == 0) { PG8_MMA(1, 0, At, B0); PG8_MMA(1, 1, At, B1); } PG8_BAR; PG8_SCHED;
;             PG8_LDB(B0, 1, 0); PG8_LDB(B1, 1, 1); PG8_SCHED; PG8_LDA(At, 1, 0); PG8_STAGE(PG8_SA(0, 1), a2 + hstep, voffA);
;             PG8_WAIT_V(8); PG8_WAIT_L(0); PG8_BAR; PG8_MMA(0, 0, At, B0); PG8_MMA(0, 1, At, B1); PG8_BAR; PG8_SCHED;
;             PG8_LDA(At, 1, 1); PG8_STAGE(PG8_SB(1, 0), b3, voffB); PG8_STAGE(PG8_SB(1, 1), b3 + hstep, voffB); PG8_STAGE(PG8_SA(1, 0), a3, voffA);
;             PG8_WAIT_V(8); PG8_WAIT_L(0); PG8_BAR; if (cur.half == 0) { PG8_MMA(1, 0, At, B0); PG8_MMA(1, 1, At, B1); } PG8_BAR; PG8_SCHED;
;     ...
;         if constexpr (ALIGN_EPI) { if (wr == 0) PG8_BAR; }
	s_add_i32 s28, s67, s25
	v_lshl_add_u64 v[212:213], v[212:213], 0, s[42:43]
	s_mov_b32 m0, s28
	ds_read_b128 v[180:183], v150 offset:49152
	ds_read_b128 v[184:187], v150 offset:50176
	ds_read_b128 v[188:191], v150 offset:51200
	ds_read_b128 v[192:195], v150 offset:52224
	ds_read_b128 v[196:199], v150 offset:53248
	ds_read_b128 v[200:203], v150 offset:54272
	ds_read_b128 v[204:207], v150 offset:55296
	ds_read_b128 v[208:211], v150 offset:56320
	global_load_lds_dwordx4 v[212:213], off
	s_add_i32 m0, s28, 0x2000
	s_add_u32 s0, s0, 0x40080
	v_lshl_add_u64 v[212:213], v[214:215], 0, s[42:43]
	s_addc_u32 s1, s1, 0
	s_add_i32 s28, s68, s25
	global_load_lds_dwordx4 v[212:213], off
	v_lshl_add_u64 v[212:213], s[0:1], 0, v[2:3]
	s_mov_b32 m0, s28
	s_nop 0
	global_load_lds_dwordx4 v[212:213], off
	v_lshl_add_u64 v[212:213], s[0:1], 0, v[136:137]
	s_add_i32 m0, s28, 0x2000
	s_nop 0
	global_load_lds_dwordx4 v[212:213], off
	v_lshl_add_u64 v[212:213], v[216:217], 0, s[42:43]
	s_mov_b32 m0, s41
	s_nop 0
	global_load_lds_dwordx4 v[212:213], off
	v_lshl_add_u64 v[212:213], v[218:219], 0, s[42:43]
	s_mov_b32 m0, s60
	s_nop 0
	global_load_lds_dwordx4 v[212:213], off
	s_waitcnt vmcnt(8)
	s_waitcnt lgkmcnt(0)
	s_barrier
	s_waitcnt lgkmcnt(0)
	v_mfma_f32_16x16x32_bf16 v[64:67], v[142:145], v[180:183], v[64:67]
	v_mfma_f32_16x16x32_bf16 v[60:63], v[156:159], v[180:183], v[60:63]
	v_mfma_f32_16x16x32_bf16 v[48:51], v[142:145], v[188:191], v[48:51]
	v_mfma_f32_16x16x32_bf16 v[44:47], v[156:159], v[188:191], v[44:47]
	v_mfma_f32_16x16x32_bf16 v[32:35], v[142:145], v[196:199], v[32:35]
	v_mfma_f32_16x16x32_bf16 v[28:31], v[156:159], v[196:199], v[28:31]
	v_mfma_f32_16x16x32_bf16 v[16:19], v[142:145], v[204:207], v[16:19]
	v_mfma_f32_16x16x32_bf16 v[12:15], v[156:159], v[204:207], v[12:15]
	v_mfma_f32_16x16x32_bf16 v[64:67], v[152:155], v[184:187], v[64:67]
	v_mfma_f32_16x16x32_bf16 v[60:63], v[160:163], v[184:187], v[60:63]
	v_mfma_f32_16x16x32_bf16 v[48:51], v[152:155], v[192:195], v[48:51]
	v_mfma_f32_16x16x32_bf16 v[44:47], v[160:163], v[192:195], v[44:47]
	v_mfma_f32_16x16x32_bf16 v[32:35], v[152:155], v[200:203], v[32:35]
	v_mfma_f32_16x16x32_bf16 v[28:31], v[160:163], v[200:203], v[28:31]
	v_mfma_f32_16x16x32_bf16 v[16:19], v[152:155], v[208:211], v[16:19]
	v_mfma_f32_16x16x32_bf16 v[12:15], v[160:163], v[208:211], v[12:15]
	v_mfma_f32_16x16x32_bf16 v[56:59], v[164:167], v[180:183], v[56:59]
	v_mfma_f32_16x16x32_bf16 v[52:55], v[172:175], v[180:183], v[52:55]
	v_mfma_f32_16x16x32_bf16 v[40:43], v[164:167], v[188:191], v[40:43]
	v_mfma_f32_16x16x32_bf16 v[36:39], v[172:175], v[188:191], v[36:39]
	v_mfma_f32_16x16x32_bf16 v[24:27], v[164:167], v[196:199], v[24:27]
	v_mfma_f32_16x16x32_bf16 v[20:23], v[172:175], v[196:199], v[20:23]
	v_mfma_f32_16x16x32_bf16 v[8:11], v[164:167], v[204:207], v[8:11]
	v_mfma_f32_16x16x32_bf16 v[4:7], v[172:175], v[204:207], v[4:7]
	v_mfma_f32_16x16x32_bf16 v[56:59], v[168:171], v[184:187], v[56:59]
	v_mfma_f32_16x16x32_bf16 v[52:55], v[176:179], v[184:187], v[52:55]
	v_mfma_f32_16x16x32_bf16 v[40:43], v[168:171], v[192:195], v[40:43]
	v_mfma_f32_16x16x32_bf16 v[36:39], v[176:179], v[192:195], v[36:39]
	v_mfma_f32_16x16x32_bf16 v[24:27], v[168:171], v[200:203], v[24:27]
	v_mfma_f32_16x16x32_bf16 v[20:23], v[176:179], v[200:203], v[20:23]
	v_mfma_f32_16x16x32_bf16 v[8:11], v[168:171], v[208:211], v[8:11]
	v_mfma_f32_16x16x32_bf16 v[4:7], v[176:179], v[208:211], v[4:7]
	s_barrier
	s_add_i32 s66, s66, 2
	s_add_u32 s26, s26, 0x100
	s_addc_u32 s27, s27, 0
	s_add_u32 s64, s64, 0x100
	s_addc_u32 s65, s65, 0
	s_cmp_gt_u32 s66, 13
	s_cbranch_scc0 .LBB0_1477
	s_and_b64 vcc, exec, s[12:13]
	s_cbranch_vccz .LBB0_1480
	s_barrier

; #define GAS __attribute__((address_space(1)))
; __device__ __forceinline__ unsigned xb_add(unsigned* p, unsigned v) { return __hip_atomic_fetch_add(p, v, __ATOMIC_RELAXED, __HIP_MEMORY_SCOPE_AGENT); }
; #define SEAM_LOCAL(k) do { if (IN(k) && IN((k) + 1)) { TBAR0(); xcd_barrier(bar, true, true); TBAR1(); } } while (0)
; __device__ __forceinline__ void xcd_barrier(const XcdBarrier& b, const bool group_local = false, const bool xcc_only = false) {
;     asm volatile("s_waitcnt vmcnt(0)" ::: "memory");
;     __syncthreads();
;     if (threadIdx.x == 0) {
;         GAS unsigned* barg = (GAS unsigned*)b.bar; asm volatile("" : "+s"(barg)); unsigned* bar = (unsigned*)barg;
;         __builtin_amdgcn_s_waitcnt(0);
;         unsigned nloc = b.st[0], nx = b.st[1];
;         if (nloc == 0u) { xcd_barrier_complete(bar, b.x, nloc, nx); b.st[0] = nloc; b.st[1] = nx; }
;         const unsigned old = xb_add(&bar[XB_XSUB(b.x)], 1u);
;         const unsigned gen = old / nloc;
; __global__ void __launch_bounds__(NWAVES * 64, 2) mk_fwd(Args args) {
;     ...
;             SEAM_LOCAL(pb + 4);
.LBB0_1672:
	v_readlane_b32 s0, v255, 23
	s_add_i32 s22, s0, 6
	v_readlane_b32 s0, v255, 6
	v_readlane_b32 s1, v255, 7
	s_cmp_ge_i32 s22, s1
	s_cbranch_scc1 .LBB0_1748
	s_waitcnt vmcnt(0)
	s_waitcnt vmcnt(0) lgkmcnt(0)
	s_barrier
	s_setprio 0
	s_mov_b64 s[14:15], exec
	v_readlane_b32 s0, v255, 43
	v_readlane_b32 s1, v255, 44
	s_and_b64 s[0:1], s[14:15], s[0:1]
	s_mov_b64 exec, s[0:1]
	s_cbranch_execz .LBB0_1747
	v_readlane_b32 s0, v255, 10
	v_readlane_b32 s4, v255, 12
	v_readlane_b32 s1, v255, 11
	s_waitcnt vmcnt(0) expcnt(0) lgkmcnt(0)
	v_mov_b32_e32 v4, s4
	ds_read_b32 v2, v4
	ds_read_b32 v6, v4 offset:4
	s_waitcnt lgkmcnt(1)
	v_cmp_ne_u32_e32 vcc, 0, v2
	s_cbranch_vccnz .LBB0_1689
	v_readlane_b32 s4, v255, 0
	v_readlane_b32 s5, v255, 1
	s_load_dwordx2 s[8:9], s[4:5], 0x4
	v_readlane_b32 s4, v255, 47
	s_lshl_b32 s4, s4, 2
	s_add_u32 s4, s0, s4
	s_addc_u32 s5, s1, 0
	s_add_u32 s6, s0, 0x1000
	s_addc_u32 s7, s1, 0
	s_waitcnt lgkmcnt(0)
	s_mul_i32 s23, s8, s33
	s_add_u32 s8, s0, 0x1100
	s_mul_i32 s23, s23, s9
	s_addc_u32 s9, s1, 0
	s_add_u32 s10, s0, 0x1200
	s_addc_u32 s11, s1, 0
	s_add_u32 s12, s0, 0x1300
	s_addc_u32 s13, s1, 0
	s_mov_b32 s24, 1
	s_branch .LBB0_1677

; __device__ __forceinline__ unsigned xb_ld(unsigned* p)              { return __hip_atomic_load(p, __ATOMIC_RELAXED, __HIP_MEMORY_SCOPE_AGENT); }
; #define XB_SPIN(cond, bar) do { unsigned _sp = 0; while (cond) { __builtin_amdgcn_s_sleep(1); \
;     if ((++_sp & 255u) == 0u) { if (xb_ld(&(bar)[XB_TMO])) break; if (_sp > XB_SPIN_CAP) { atomicAdd(&(bar)[XB_TMO], 1u); break; } } } } while (0)
; __device__ __forceinline__ void xcd_barrier(const XcdBarrier& b, const bool group_local = false, const bool xcc_only = false) {
;     ...
;             XB_SPIN(xb_ld(&bar[XB_XGEN(b.x)]) <= gen, bar);
.LBB0_1729:
	s_add_u32 s4, s6, 0x2400
	s_addc_u32 s5, s7, 0
	v_mov_b64_e32 v[4:5], s[4:5]
	s_or_b64 s[12:13], s[12:13], exec
	s_or_b64 exec, exec, s[0:1]
	s_and_saveexec_b64 s[0:1], s[12:13]
	s_cbranch_execnz .LBB0_1427
	s_branch .LBB0_1428
	.p2align 6
	s_nop 0
	s_nop 0
	s_nop 0
	s_nop 0
	s_nop 0
	s_nop 0
	s_nop 0
	s_nop 0
.LBB0_1730:
	s_or_b64 exec, exec, s[26:27]
	s_and_b64 s[26:27], s[28:29], exec

;     __device__ __forceinline__ void a_ready(const Unit&) const { if (++ncall == 3 && sig != nullptr && threadIdx.x == 0) __hip_atomic_fetch_add(sig, 1u, __ATOMIC_RELAXED, __HIP_MEMORY_SCOPE_AGENT); }
; #define PG8_STAGE(bufoff, gbase, voff) do { _Pragma("unroll") for (int _i = 0; _i < 2; ++_i) \
;         __builtin_amdgcn_global_load_lds((const unsigned*)((const char*)(gbase) + (voff)[_i]), (PG8_LAS unsigned*)(lds + (bufoff) + ldsw + _i * 8192), 16, 0, 0); } while (0)
; #define PG8_BAR __builtin_amdgcn_s_barrier()
; template <class Epi, class Sched, bool ALIGN_EPI = false, bool SP2 = false>
; __device__ __forceinline__ void gemm_phase(PG8_LAS unsigned char* lds, const Gemm g, const Sched& S, const Epi& E) {
;     ...
;     for (int i = 0; i < 2; ++i) { int R, C; stage_rc(tid * 16 + i * 8192, R, C); const int Rb = Epi::PERM ? ((R & ~31) + perm32(R & 31)) : R;
;         voffA[i] = (unsigned)(R * K + C) * 2u; voffB[i] = (unsigned)(Rb * K + C) * 2u; }
;     const size_t kstep = (size_t)(BK * 2);
;     const size_t hstep = (size_t)HALF * K * 2;
;     const size_t tstep = 2 * hstep;
;     const unsigned ldsw = (unsigned)wid * 1024u;
;     const int aoff = lds_byte(wr * 64 + fr, fq * 8), boff = lds_byte(wc * 32 + fr, fq * 8);
;     ...
;     const char* cA = (const char*)g.A + (size_t)cur.pm * tstep + (cur.half == 2 ? hstep : (size_t)0); const char* cB = (const char*)g.Bt + (size_t)cur.pn * tstep;
;     S.a_ready(cur);
;     if constexpr (SP2) {
;         PG8_STAGE(PG8_SB(0, 0), cB, voffB); PG8_STAGE(PG8_SB(0, 1), cB + hstep, voffB); PG8_STAGE(PG8_SA(0, 0), cA, voffA); PG8_STAGE(PG8_SA(0, 1), cA + hstep, voffA);
;         if (wr == 1) PG8_BAR;
.LBB0_1766:
	v_ashrrev_i32_e32 v2, 31, v146
	v_lshrrev_b32_e32 v2, 26, v2
	v_add_u32_e32 v2, v146, v2
	v_ashrrev_i32_e32 v4, 6, v2
	v_bfe_i32 v2, v146, 27, 1
	v_lshlrev_b32_e32 v8, 4, v146
	v_lshrrev_b32_e32 v2, 22, v2
	v_add_u32_e32 v2, v8, v2
	v_and_b32_e32 v2, 0xfffffc00, v2
	v_sub_u32_e32 v2, v8, v2
	s_mul_i32 s36, s77, 0xee0000
	v_lshrrev_b32_e32 v5, 4, v2
	s_lshl_b64 s[8:9], s[36:37], 1
	v_bitop3_b32 v2, v5, v2, 32 bitop3:0x6c
	s_add_u32 s5, s12, s8
	v_ashrrev_i32_e32 v6, 31, v2
	s_addc_u32 s8, s13, s9
	s_or_b32 s6, s1, s6
	s_mov_b32 s1, s37
	v_lshrrev_b32_e32 v6, 26, v6
	s_lshl_b64 s[0:1], s[0:1], 20
	v_lshlrev_b32_e32 v5, 3, v4
	v_add_u32_e32 v7, v2, v6
	s_add_u32 s0, s12, s0
	v_and_b32_e32 v5, -16, v5
	v_ashrrev_i32_e32 v6, 6, v7
	v_and_b32_e32 v7, 0xc0, v7
	s_addc_u32 s1, s13, s1
	s_mul_i32 s6, s6, 0x160000
	v_add_u32_e32 v9, v6, v5
	v_sub_u32_e32 v2, v2, v7
	s_sub_u32 s28, s0, s6
	v_lshlrev_b32_e32 v5, 5, v4
	v_ashrrev_i16_sdwa v2, v224, sext(v2) dst_sel:DWORD dst_unused:UNUSED_PAD src0_sel:DWORD src1_sel:BYTE_0
	v_lshlrev_b32_e32 v10, 1, v9
	v_lshrrev_b32_e32 v11, 2, v9
	v_and_b32_e32 v12, 3, v6
	s_mov_b32 s0, 0xffffe0
	s_subb_u32 s29, s1, 0
	v_and_b32_e32 v5, 32, v5
	v_bfe_i32 v7, v2, 0, 16
	v_and_b32_e32 v10, 24, v10
	v_and_b32_e32 v11, 4, v11
	v_and_or_b32 v12, v9, s0, v12
	s_movk_i32 s1, 0xb00
	v_add_u32_e32 v2, v5, v7
	v_or3_b32 v10, v12, v11, v10
	v_mul_lo_u32 v9, v9, s1
	v_add_lshl_u32 v132, v2, v9, 1
	v_mul_u32_u24_e32 v9, 0xb00, v10
	v_add_lshl_u32 v2, v9, v2, 1
	v_add_u32_e32 v9, 0x2000, v8
	v_ashrrev_i32_e32 v8, 31, v9
	v_lshrrev_b32_e32 v8, 22, v8
	v_add_u32_e32 v8, v9, v8
	v_ashrrev_i32_e32 v8, 10, v8
	v_mul_i32_i24_e32 v10, 0x400, v8
	v_sub_u32_e32 v9, v9, v10
	v_lshrrev_b32_e32 v10, 4, v9
	v_bitop3_b32 v11, v10, v9, 32 bitop3:0x6c
	v_ashrrev_i32_e32 v10, 31, v11
	v_lshrrev_b32_e32 v10, 26, v10
	v_lshlrev_b32_e32 v9, 3, v8
	v_add_u32_e32 v12, v11, v10
	v_and_b32_e32 v9, -16, v9
	v_ashrrev_i32_e32 v10, 6, v12
	s_add_u32 s30, s5, 0x2000000
	v_add_u32_e32 v13, v10, v9
	v_and_b32_e32 v16, 3, v10
	s_addc_u32 s31, s8, 0
	v_and_or_b32 v16, v13, s0, v16
	s_add_i32 s0, s7, s4
	v_lshlrev_b32_e32 v14, 1, v13
	v_lshrrev_b32_e32 v15, 2, v13
	v_mul_lo_u32 v13, v13, s1
	s_ashr_i32 s1, s0, 31
	s_lshr_b32 s1, s1, 27
	s_add_i32 s1, s0, s1
	s_ashr_i32 s4, s1, 5
	s_and_b32 s1, s1, 0xffe0
	s_sub_i32 s0, s0, s1
	s_bfe_i32 s1, s0, 0x80000
	s_bfe_u32 s1, s1, 0x3000c
	s_add_i32 s1, s0, s1
	s_lshl_b32 s5, s4, 3
	s_bfe_i32 s4, s1, 0x80000
	s_and_b32 s1, s1, 0xf8
	s_sub_i32 s0, s0, s1
	s_sext_i32_i16 s4, s4
	s_sext_i32_i8 s0, s0
	s_ashr_i32 s17, s27, 6
	v_and_b32_e32 v12, 0xc0, v12
	s_add_i32 s23, s5, s0
	s_ashr_i32 s0, s4, 3
	s_ashr_i32 s22, s27, 8
	v_sub_u32_e32 v11, v11, v12
	s_lshl_b32 s34, s17, 10
	s_mul_hi_i32 s1, s0, 0x160000
	s_mul_i32 s0, s0, 0x160000
	v_lshlrev_b32_e32 v9, 5, v8
	v_ashrrev_i16_sdwa v11, v224, sext(v11) dst_sel:DWORD dst_unused:UNUSED_PAD src0_sel:DWORD src1_sel:BYTE_0
	s_add_u32 s0, s30, s0
	v_and_b32_e32 v9, 32, v9
	v_bfe_i32 v11, v11, 0, 16
	v_and_b32_e32 v14, 24, v14
	v_and_b32_e32 v15, 4, v15
	s_addc_u32 s1, s31, s1
	s_add_i32 s35, s34, 0
	v_add_u32_e32 v12, v9, v11
	v_or3_b32 v14, v16, v15, v14
	s_add_i32 m0, s35, 0x10000
	v_add_lshl_u32 v134, v12, v13, 1
	v_mul_u32_u24_e32 v13, 0xb00, v14
	global_load_lds_dwordx4 v2, s[0:1]
	s_add_i32 m0, s35, 0x12000
	v_add_lshl_u32 v136, v13, v12, 1
	s_add_u32 s6, s0, 0xb0000
	global_load_lds_dwordx4 v136, s[0:1]
	s_addc_u32 s7, s1, 0
	s_add_i32 m0, s35, 0x14000
	s_mul_i32 s8, s23, 0x160000
	global_load_lds_dwordx4 v2, s[6:7]
	s_add_i32 m0, s35, 0x16000
	s_mul_hi_i32 s5, s23, 0x160000
	global_load_lds_dwordx4 v136, s[6:7]
	s_add_u32 s6, s28, s8
	s_addc_u32 s7, s29, s5
	s_add_i32 s36, s35, 0x2000
	s_mov_b32 m0, s35
	s_add_u32 s8, s6, 0xb0000
	global_load_lds_dwordx4 v132, s[6:7]
	s_mov_b32 m0, s36
	s_addc_u32 s9, s7, 0
	s_add_i32 s38, s35, 0x4000
	global_load_lds_dwordx4 v134, s[6:7]
	s_mov_b32 m0, s38
	s_add_i32 s39, s35, 0x6000
	global_load_lds_dwordx4 v132, s[8:9]
	s_mov_b32 m0, s39
	s_cmp_lg_u32 s22, 1
	global_load_lds_dwordx4 v134, s[8:9]
	s_cbranch_scc1 .LBB0_1768
	s_setprio 1
	s_barrier

; #define PG8_STAGE(bufoff, gbase, voff) do { _Pragma("unroll") for (int _i = 0; _i < 2; ++_i) \
;         __builtin_amdgcn_global_load_lds((const unsigned*)((const char*)(gbase) + (voff)[_i]), (PG8_LAS unsigned*)(lds + (bufoff) + ldsw + _i * 8192), 16, 0, 0); } while (0)
; #define PG8_LDA(dst, b, h) do { _Pragma("unroll") for (int m = 0; m < 4; ++m) _Pragma("unroll") for (int k = 0; k < 2; ++k) dst[m][k] = *(const PG8_LAS bf16x8*)(lds + PG8_SA(b, h) + aoff + m * 2048 + k * 1024); } while (0)
; #define PG8_LDB(dst, b, h) do { _Pragma("unroll") for (int n = 0; n < 2; ++n) _Pragma("unroll") for (int k = 0; k < 2; ++k) dst[n][k] = *(const PG8_LAS bf16x8*)(lds + PG8_SB(b, h) + boff + n * 2048 + k * 1024); } while (0)
; #define PG8_WAIT_V(n) asm volatile("s_waitcnt vmcnt(" #n ")" ::: "memory")
; #define PG8_WAIT_L(n) asm volatile("s_waitcnt lgkmcnt(" #n ")" ::: "memory")
; template <class Epi, class Sched, bool ALIGN_EPI = false, bool SP2 = false>
; __device__ __forceinline__ void gemm_phase(PG8_LAS unsigned char* lds, const Gemm g, const Sched& S, const Epi& E) {
;     ...
;             PG8_LDB(B0, 0, 0); PG8_LDB(B1, 0, 1); PG8_SCHED; PG8_LDA(At, 0, 0); PG8_STAGE(PG8_SA(1, 1), a1 + hstep, voffA);
;     ...
;             if (PROBE_KIND == 18 && t == 0 && ui > 0 && g.probe) { const unsigned long long tq_ = __builtin_amdgcn_s_memrealtime(); PG8_WAIT_V(8); pg8_probe_acc += (unsigned)(__builtin_amdgcn_s_memrealtime() - tq_); }
;     ...
;             PG8_WAIT_V(8); PG8_WAIT_L(0); PG8_BAR; PG8_MMA(0, 0, At, B0); PG8_MMA(0, 1, At, B1); PG8_BAR; PG8_SCHED;
;             PG8_LDA(At, 0, 1); PG8_STAGE(PG8_SB(0, 0), b2, voffB); PG8_STAGE(PG8_SB(0, 1), b2 + hstep, voffB); PG8_STAGE(PG8_SA(0, 0), a2, voffA);
;             PG8_WAIT_V(8); PG8_WAIT_L(0); PG8_BAR; if (cur.half == 0) { PG8_MMA(1, 0, At, B0); PG8_MMA(1, 1, At, B1); } PG8_BAR; PG8_SCHED;
;             PG8_LDB(B0, 1, 0); PG8_LDB(B1, 1, 1); PG8_SCHED; PG8_LDA(At, 1, 0); PG8_STAGE(PG8_SA(0, 1), a2 + hstep, voffA);
;             PG8_WAIT_V(8); PG8_WAIT_L(0); PG8_BAR; PG8_MMA(0, 0, At, B0); PG8_MMA(0, 1, At, B1); PG8_BAR; PG8_SCHED;
;             PG8_LDA(At, 1, 1); PG8_STAGE(PG8_SB(1, 0), b3, voffB); PG8_STAGE(PG8_SB(1, 1), b3 + hstep, voffB); PG8_STAGE(PG8_SA(1, 0), a3, voffA);
;             PG8_WAIT_V(8); PG8_WAIT_L(0); PG8_BAR; if (cur.half == 0) { PG8_MMA(1, 0, At, B0); PG8_MMA(1, 1, At, B1); } PG8_BAR; PG8_SCHED;
.LBB0_1780:
	s_add_u32 s18, s6, s0
	s_addc_u32 s19, s7, s1
	s_add_u32 s18, s18, 0x100
	s_addc_u32 s19, s19, 0
	s_add_u32 s63, s60, s0
	s_addc_u32 s64, s61, s1
	s_add_i32 s65, 0, 0x10000
	s_cmpk_eq_i32 s0, 0x1500
	s_cselect_b32 s21, s15, s19
	s_cselect_b32 s20, s14, s18
	s_cselect_b32 s19, s11, s64
	s_cselect_b32 s18, s10, s63
	s_add_i32 s63, 0, 0x14000
	v_add_u32_e32 v162, s65, v148
	v_add_u32_e32 v178, s63, v148
	ds_read_b128 v[150:153], v162
	ds_read_b128 v[154:157], v162 offset:1024
	ds_read_b128 v[158:161], v162 offset:2048
	ds_read_b128 v[162:165], v162 offset:3072
	ds_read_b128 v[166:169], v178
	ds_read_b128 v[170:173], v178 offset:1024
	ds_read_b128 v[174:177], v178 offset:2048
	ds_read_b128 v[178:181], v178 offset:3072
	v_lshl_add_u64 v[214:215], v[142:143], 0, s[0:1]
	s_add_i32 m0, s35, 0xc000
	ds_read_b128 v[182:185], v149
	ds_read_b128 v[186:189], v149 offset:1024
	ds_read_b128 v[190:193], v149 offset:2048
	ds_read_b128 v[194:197], v149 offset:3072
	ds_read_b128 v[198:201], v149 offset:4096
	ds_read_b128 v[202:205], v149 offset:5120
	ds_read_b128 v[206:209], v149 offset:6144
	ds_read_b128 v[210:213], v149 offset:7168
	global_load_lds_dwordx4 v[214:215], off
	v_lshl_add_u64 v[214:215], v[144:145], 0, s[0:1]
	s_add_i32 m0, s35, 0xe000
	s_nop 0
	global_load_lds_dwordx4 v[214:215], off
	s_waitcnt vmcnt(8)
	s_waitcnt lgkmcnt(0)
	s_barrier
	s_waitcnt lgkmcnt(0)
	v_mfma_f32_16x16x32_bf16 v[128:131], v[150:153], v[182:185], v[128:131]
	v_mfma_f32_16x16x32_bf16 v[124:127], v[158:161], v[182:185], v[124:127]
	v_mfma_f32_16x16x32_bf16 v[112:115], v[150:153], v[190:193], v[112:115]
	v_mfma_f32_16x16x32_bf16 v[108:111], v[158:161], v[190:193], v[108:111]
	v_mfma_f32_16x16x32_bf16 v[96:99], v[150:153], v[198:201], v[96:99]
	v_mfma_f32_16x16x32_bf16 v[92:95], v[158:161], v[198:201], v[92:95]
	v_mfma_f32_16x16x32_bf16 v[80:83], v[150:153], v[206:209], v[80:83]
	v_mfma_f32_16x16x32_bf16 v[76:79], v[158:161], v[206:209], v[76:79]
	v_mfma_f32_16x16x32_bf16 v[128:131], v[154:157], v[186:189], v[128:131]
	v_mfma_f32_16x16x32_bf16 v[124:127], v[162:165], v[186:189], v[124:127]
	v_mfma_f32_16x16x32_bf16 v[112:115], v[154:157], v[194:197], v[112:115]
	v_mfma_f32_16x16x32_bf16 v[108:111], v[162:165], v[194:197], v[108:111]
	v_mfma_f32_16x16x32_bf16 v[96:99], v[154:157], v[202:205], v[96:99]
	v_mfma_f32_16x16x32_bf16 v[92:95], v[162:165], v[202:205], v[92:95]
	v_mfma_f32_16x16x32_bf16 v[80:83], v[154:157], v[210:213], v[80:83]
	v_mfma_f32_16x16x32_bf16 v[76:79], v[162:165], v[210:213], v[76:79]
	v_mfma_f32_16x16x32_bf16 v[120:123], v[166:169], v[182:185], v[120:123]
	v_mfma_f32_16x16x32_bf16 v[116:119], v[174:177], v[182:185], v[116:119]
	v_mfma_f32_16x16x32_bf16 v[104:107], v[166:169], v[190:193], v[104:107]
	v_mfma_f32_16x16x32_bf16 v[100:103], v[174:177], v[190:193], v[100:103]
	v_mfma_f32_16x16x32_bf16 v[88:91], v[166:169], v[198:201], v[88:91]
	v_mfma_f32_16x16x32_bf16 v[84:87], v[174:177], v[198:201], v[84:87]
	v_mfma_f32_16x16x32_bf16 v[72:75], v[166:169], v[206:209], v[72:75]
	v_mfma_f32_16x16x32_bf16 v[68:71], v[174:177], v[206:209], v[68:71]
	v_mfma_f32_16x16x32_bf16 v[120:123], v[170:173], v[186:189], v[120:123]
	v_mfma_f32_16x16x32_bf16 v[116:119], v[178:181], v[186:189], v[116:119]
	v_mfma_f32_16x16x32_bf16 v[104:107], v[170:173], v[194:197], v[104:107]
	v_mfma_f32_16x16x32_bf16 v[100:103], v[178:181], v[194:197], v[100:103]
	v_mfma_f32_16x16x32_bf16 v[88:91], v[170:173], v[202:205], v[88:91]
	v_mfma_f32_16x16x32_bf16 v[84:87], v[178:181], v[202:205], v[84:87]
	v_mfma_f32_16x16x32_bf16 v[72:75], v[170:173], v[210:213], v[72:75]
	v_mfma_f32_16x16x32_bf16 v[68:71], v[178:181], v[210:213], v[68:71]
	s_barrier
	s_add_i32 s64, s65, s34
	v_lshl_add_u64 v[214:215], s[18:19], 0, v[2:3]
	s_mov_b32 m0, s64
	ds_read_b128 v[182:185], v149 offset:16384
	ds_read_b128 v[186:189], v149 offset:17408
	ds_read_b128 v[190:193], v149 offset:18432
	ds_read_b128 v[194:197], v149 offset:19456
	ds_read_b128 v[198:201], v149 offset:20480
	ds_read_b128 v[202:205], v149 offset:21504
	ds_read_b128 v[206:209], v149 offset:22528
	ds_read_b128 v[210:213], v149 offset:23552
	global_load_lds_dwordx4 v[214:215], off
	s_add_i32 m0, s64, 0x2000
	s_add_u32 s64, s18, 0xb0000
	v_lshl_add_u64 v[216:217], s[18:19], 0, v[136:137]
	s_addc_u32 s65, s19, 0
	s_add_i32 s63, s63, s34
	global_load_lds_dwordx4 v[216:217], off
	v_lshl_add_u64 v[218:219], s[64:65], 0, v[2:3]
	s_mov_b32 m0, s63
	v_lshl_add_u64 v[220:221], s[20:21], 0, v[134:135]
	global_load_lds_dwordx4 v[218:219], off
	v_lshl_add_u64 v[218:219], s[64:65], 0, v[136:137]
	s_add_i32 m0, s63, 0x2000
	s_nop 0
	global_load_lds_dwordx4 v[218:219], off
	v_lshl_add_u64 v[218:219], s[20:21], 0, v[132:133]
	s_mov_b32 m0, s35
	s_nop 0
	global_load_lds_dwordx4 v[218:219], off
	s_mov_b32 m0, s36
	s_nop 0
	global_load_lds_dwordx4 v[220:221], off
	s_waitcnt vmcnt(8)
	s_waitcnt lgkmcnt(0)
	s_barrier
; #define PG8_STAGE(bufoff, gbase, voff) do { _Pragma("unroll") for (int _i = 0; _i < 2; ++_i) \
;         __builtin_amdgcn_global_load_lds((const unsigned*)((const char*)(gbase) + (voff)[_i]), (PG8_LAS unsigned*)(lds + (bufoff) + ldsw + _i * 8192), 16, 0, 0); } while (0)
; #define PG8_LDA(dst, b, h) do { _Pragma("unroll") for (int m = 0; m < 4; ++m) _Pragma("unroll") for (int k = 0; k < 2; ++k) dst[m][k] = *(const PG8_LAS bf16x8*)(lds + PG8_SA(b, h) + aoff + m * 2048 + k * 1024); } while (0)
; #define PG8_LDB(dst, b, h) do { _Pragma("unroll") for (int n = 0; n < 2; ++n) _Pragma("unroll") for (int k = 0; k < 2; ++k) dst[n][k] = *(const PG8_LAS bf16x8*)(lds + PG8_SB(b, h) + boff + n * 2048 + k * 1024); } while (0)
; #define PG8_MMA(ai, bj, At, Bt) do { __builtin_amdgcn_s_setprio(1); _Pragma("unroll") for (int m = 0; m < 4; ++m) _Pragma("unroll") for (int n = 0; n < 2; ++n) _Pragma("unroll") for (int k = 0; k < 2; ++k) \
;         acc[ai][bj][m][n] = __builtin_amdgcn_mfma_f32_16x16x32_bf16(Bt[n][k], At[m][k], acc[ai][bj][m][n], 0, 0, 0); __builtin_amdgcn_s_setprio(0); } while (0)
; #define PG8_WAIT_V(n) asm volatile("s_waitcnt vmcnt(" #n ")" ::: "memory")
; #define PG8_WAIT_L(n) asm volatile("s_waitcnt lgkmcnt(" #n ")" ::: "memory")
; #define PG8_BAR __builtin_amdgcn_s_barrier()
; #define PG8_SCHED __builtin_amdgcn_sched_barrier(0)
; template <class Epi, class Sched, bool ALIGN_EPI = false, bool SP2 = false>
; __device__ __forceinline__ void gemm_phase(PG8_LAS unsigned char* lds, const Gemm g, const Sched& S, const Epi& E) {
;     ...
;             PG8_WAIT_V(8); PG8_WAIT_L(0); PG8_BAR; if (cur.half == 0) { PG8_MMA(1, 0, At, B0); PG8_MMA(1, 1, At, B1); } PG8_BAR; PG8_SCHED;
;             PG8_LDB(B0, 1, 0); PG8_LDB(B1, 1, 1); PG8_SCHED; PG8_LDA(At, 1, 0); PG8_STAGE(PG8_SA(0, 1), a2 + hstep, voffA);
;             PG8_WAIT_V(8); PG8_WAIT_L(0); PG8_BAR; PG8_MMA(0, 0, At, B0); PG8_MMA(0, 1, At, B1); PG8_BAR; PG8_SCHED;
	s_waitcnt lgkmcnt(0)
	v_mfma_f32_16x16x32_bf16 v[64:67], v[150:153], v[182:185], v[64:67]
	v_mfma_f32_16x16x32_bf16 v[60:63], v[158:161], v[182:185], v[60:63]
	v_mfma_f32_16x16x32_bf16 v[48:51], v[150:153], v[190:193], v[48:51]
	v_mfma_f32_16x16x32_bf16 v[44:47], v[158:161], v[190:193], v[44:47]
	v_mfma_f32_16x16x32_bf16 v[32:35], v[150:153], v[198:201], v[32:35]
	v_mfma_f32_16x16x32_bf16 v[28:31], v[158:161], v[198:201], v[28:31]
	v_mfma_f32_16x16x32_bf16 v[16:19], v[150:153], v[206:209], v[16:19]
	v_mfma_f32_16x16x32_bf16 v[12:15], v[158:161], v[206:209], v[12:15]
	v_mfma_f32_16x16x32_bf16 v[64:67], v[154:157], v[186:189], v[64:67]
	v_mfma_f32_16x16x32_bf16 v[60:63], v[162:165], v[186:189], v[60:63]
	v_mfma_f32_16x16x32_bf16 v[48:51], v[154:157], v[194:197], v[48:51]
	v_mfma_f32_16x16x32_bf16 v[44:47], v[162:165], v[194:197], v[44:47]
	v_mfma_f32_16x16x32_bf16 v[32:35], v[154:157], v[202:205], v[32:35]
	v_mfma_f32_16x16x32_bf16 v[28:31], v[162:165], v[202:205], v[28:31]
	v_mfma_f32_16x16x32_bf16 v[16:19], v[154:157], v[210:213], v[16:19]
	v_mfma_f32_16x16x32_bf16 v[12:15], v[162:165], v[210:213], v[12:15]
	v_mfma_f32_16x16x32_bf16 v[56:59], v[166:169], v[182:185], v[56:59]
	v_mfma_f32_16x16x32_bf16 v[52:55], v[174:177], v[182:185], v[52:55]
	v_mfma_f32_16x16x32_bf16 v[40:43], v[166:169], v[190:193], v[40:43]
	v_mfma_f32_16x16x32_bf16 v[36:39], v[174:177], v[190:193], v[36:39]
	v_mfma_f32_16x16x32_bf16 v[24:27], v[166:169], v[198:201], v[24:27]
	v_mfma_f32_16x16x32_bf16 v[20:23], v[174:177], v[198:201], v[20:23]
	v_mfma_f32_16x16x32_bf16 v[8:11], v[166:169], v[206:209], v[8:11]
	v_mfma_f32_16x16x32_bf16 v[4:7], v[174:177], v[206:209], v[4:7]
	v_mfma_f32_16x16x32_bf16 v[56:59], v[170:173], v[186:189], v[56:59]
	v_mfma_f32_16x16x32_bf16 v[52:55], v[178:181], v[186:189], v[52:55]
	v_mfma_f32_16x16x32_bf16 v[40:43], v[170:173], v[194:197], v[40:43]
	v_mfma_f32_16x16x32_bf16 v[36:39], v[178:181], v[194:197], v[36:39]
	v_mfma_f32_16x16x32_bf16 v[24:27], v[170:173], v[202:205], v[24:27]
	v_mfma_f32_16x16x32_bf16 v[20:23], v[178:181], v[202:205], v[20:23]
	v_mfma_f32_16x16x32_bf16 v[8:11], v[170:173], v[210:213], v[8:11]
	v_mfma_f32_16x16x32_bf16 v[4:7], v[178:181], v[210:213], v[4:7]
	s_barrier
	s_add_i32 s63, 0, 0x18000
	s_add_i32 s64, 0, 0x1c000
	v_add_u32_e32 v162, s63, v148
	v_add_u32_e32 v178, s64, v148
	ds_read_b128 v[150:153], v162
	ds_read_b128 v[154:157], v162 offset:1024
	ds_read_b128 v[158:161], v162 offset:2048
	ds_read_b128 v[162:165], v162 offset:3072
	ds_read_b128 v[166:169], v178
	ds_read_b128 v[170:173], v178 offset:1024
	ds_read_b128 v[174:177], v178 offset:2048
	ds_read_b128 v[178:181], v178 offset:3072
	s_add_u32 s20, s20, 0xb0000
	s_addc_u32 s21, s21, 0
	s_mov_b32 m0, s38
	v_lshl_add_u64 v[230:231], s[20:21], 0, v[132:133]
	ds_read_b128 v[182:185], v149 offset:32768
	ds_read_b128 v[186:189], v149 offset:33792
	ds_read_b128 v[190:193], v149 offset:34816
	ds_read_b128 v[194:197], v149 offset:35840
	ds_read_b128 v[198:201], v149 offset:36864
	ds_read_b128 v[202:205], v149 offset:37888
	ds_read_b128 v[206:209], v149 offset:38912
	ds_read_b128 v[210:213], v149 offset:39936
	global_load_lds_dwordx4 v[230:231], off
	v_lshl_add_u64 v[230:231], s[20:21], 0, v[134:135]
	s_mov_b32 m0, s39
	s_nop 0
	global_load_lds_dwordx4 v[230:231], off
	s_waitcnt vmcnt(8)
	s_waitcnt lgkmcnt(0)
	s_barrier
	s_waitcnt lgkmcnt(0)
	v_mfma_f32_16x16x32_bf16 v[128:131], v[150:153], v[182:185], v[128:131]
	v_mfma_f32_16x16x32_bf16 v[124:127], v[158:161], v[182:185], v[124:127]
	v_mfma_f32_16x16x32_bf16 v[112:115], v[150:153], v[190:193], v[112:115]
	v_mfma_f32_16x16x32_bf16 v[108:111], v[158:161], v[190:193], v[108:111]
	v_mfma_f32_16x16x32_bf16 v[96:99], v[150:153], v[198:201], v[96:99]
	v_mfma_f32_16x16x32_bf16 v[92:95], v[158:161], v[198:201], v[92:95]
	v_mfma_f32_16x16x32_bf16 v[80:83], v[150:153], v[206:209], v[80:83]
	v_mfma_f32_16x16x32_bf16 v[76:79], v[158:161], v[206:209], v[76:79]
	v_mfma_f32_16x16x32_bf16 v[128:131], v[154:157], v[186:189], v[128:131]
	v_mfma_f32_16x16x32_bf16 v[124:127], v[162:165], v[186:189], v[124:127]
	v_mfma_f32_16x16x32_bf16 v[112:115], v[154:157], v[194:197], v[112:115]
	v_mfma_f32_16x16x32_bf16 v[108:111], v[162:165], v[194:197], v[108:111]
	v_mfma_f32_16x16x32_bf16 v[96:99], v[154:157], v[202:205], v[96:99]
	v_mfma_f32_16x16x32_bf16 v[92:95], v[162:165], v[202:205], v[92:95]
	v_mfma_f32_16x16x32_bf16 v[80:83], v[154:157], v[210:213], v[80:83]
	v_mfma_f32_16x16x32_bf16 v[76:79], v[162:165], v[210:213], v[76:79]
	v_mfma_f32_16x16x32_bf16 v[120:123], v[166:169], v[182:185], v[120:123]
	v_mfma_f32_16x16x32_bf16 v[116:119], v[174:177], v[182:185], v[116:119]
	v_mfma_f32_16x16x32_bf16 v[104:107], v[166:169], v[190:193], v[104:107]
	v_mfma_f32_16x16x32_bf16 v[100:103], v[174:177], v[190:193], v[100:103]
	v_mfma_f32_16x16x32_bf16 v[88:91], v[166:169], v[198:201], v[88:91]
	v_mfma_f32_16x16x32_bf16 v[84:87], v[174:177], v[198:201], v[84:87]
	v_mfma_f32_16x16x32_bf16 v[72:75], v[166:169], v[206:209], v[72:75]
	v_mfma_f32_16x16x32_bf16 v[68:71], v[174:177], v[206:209], v[68:71]
	v_mfma_f32_16x16x32_bf16 v[120:123], v[170:173], v[186:189], v[120:123]
	v_mfma_f32_16x16x32_bf16 v[116:119], v[178:181], v[186:189], v[116:119]
	v_mfma_f32_16x16x32_bf16 v[104:107], v[170:173], v[194:197], v[104:107]
	v_mfma_f32_16x16x32_bf16 v[100:103], v[178:181], v[194:197], v[100:103]
	v_mfma_f32_16x16x32_bf16 v[88:91], v[170:173], v[202:205], v[88:91]
	v_mfma_f32_16x16x32_bf16 v[84:87], v[178:181], v[202:205], v[84:87]
	v_mfma_f32_16x16x32_bf16 v[72:75], v[170:173], v[210:213], v[72:75]
	v_mfma_f32_16x16x32_bf16 v[68:71], v[178:181], v[210:213], v[68:71]
	s_barrier
; #define PG8_STAGE(bufoff, gbase, voff) do { _Pragma("unroll") for (int _i = 0; _i < 2; ++_i) \
;         __builtin_amdgcn_global_load_lds((const unsigned*)((const char*)(gbase) + (voff)[_i]), (PG8_LAS unsigned*)(lds + (bufoff) + ldsw + _i * 8192), 16, 0, 0); } while (0)
; #define PG8_LDA(dst, b, h) do { _Pragma("unroll") for (int m = 0; m < 4; ++m) _Pragma("unroll") for (int k = 0; k < 2; ++k) dst[m][k] = *(const PG8_LAS bf16x8*)(lds + PG8_SA(b, h) + aoff + m * 2048 + k * 1024); } while (0)
; #define PG8_MMA(ai, bj, At, Bt) do { __builtin_amdgcn_s_setprio(1); _Pragma("unroll") for (int m = 0; m < 4; ++m) _Pragma("unroll") for (int n = 0; n < 2; ++n) _Pragma("unroll") for (int k = 0; k < 2; ++k) \
;         acc[ai][bj][m][n] = __builtin_amdgcn_mfma_f32_16x16x32_bf16(Bt[n][k], At[m][k], acc[ai][bj][m][n], 0, 0, 0); __builtin_amdgcn_s_setprio(0); } while (0)
; #define PG8_WAIT_V(n) asm volatile("s_waitcnt vmcnt(" #n ")" ::: "memory")
; #define PG8_WAIT_L(n) asm volatile("s_waitcnt lgkmcnt(" #n ")" ::: "memory")
; #define PG8_BAR __builtin_amdgcn_s_barrier()
; #define PG8_SCHED __builtin_amdgcn_sched_barrier(0)
; template <class Epi, class Sched, bool ALIGN_EPI = false, bool SP2 = false>
; __device__ __forceinline__ void gemm_phase(PG8_LAS unsigned char* lds, const Gemm g, const Sched& S, const Epi& E) {
;     ...
;             PG8_LDA(At, 1, 1); PG8_STAGE(PG8_SB(1, 0), b3, voffB); PG8_STAGE(PG8_SB(1, 1), b3 + hstep, voffB); PG8_STAGE(PG8_SA(1, 0), a3, voffA);
;             PG8_WAIT_V(8); PG8_WAIT_L(0); PG8_BAR; if (cur.half == 0) { PG8_MMA(1, 0, At, B0); PG8_MMA(1, 1, At, B1); } PG8_BAR; PG8_SCHED;
;     ...
;         if (!has_next) break;
;         if constexpr (!Epi::CHAIN) {
; #pragma unroll
;         for (int a = 0; a < 2; ++a)
; #pragma unroll
;             for (int b = 0; b < 2; ++b)
; #pragma unroll
;                 for (int m = 0; m < 4; ++m)
; #pragma unroll
;                     for (int n = 0; n < 2; ++n) acc[a][b][m][n] = (f32x4){0.f, 0.f, 0.f, 0.f};
;         }
;         cur = nxt; cA = nA; cB = nB; ++ui;
	s_add_i32 s20, s63, s34
	v_lshl_add_u64 v[214:215], v[214:215], 0, s[42:43]
	s_mov_b32 m0, s20
	ds_read_b128 v[182:185], v149 offset:49152
	ds_read_b128 v[186:189], v149 offset:50176
	ds_read_b128 v[190:193], v149 offset:51200
	ds_read_b128 v[194:197], v149 offset:52224
	ds_read_b128 v[198:201], v149 offset:53248
	ds_read_b128 v[202:205], v149 offset:54272
	ds_read_b128 v[206:209], v149 offset:55296
	ds_read_b128 v[210:213], v149 offset:56320
	global_load_lds_dwordx4 v[214:215], off
	s_add_i32 m0, s20, 0x2000
	s_add_u32 s18, s18, 0xb0080
	v_lshl_add_u64 v[214:215], v[216:217], 0, s[42:43]
	s_addc_u32 s19, s19, 0
	s_add_i32 s20, s64, s34
	global_load_lds_dwordx4 v[214:215], off
	v_lshl_add_u64 v[214:215], s[18:19], 0, v[2:3]
	s_mov_b32 m0, s20
	s_nop 0
	global_load_lds_dwordx4 v[214:215], off
	v_lshl_add_u64 v[214:215], s[18:19], 0, v[136:137]
	s_add_i32 m0, s20, 0x2000
	s_nop 0
	global_load_lds_dwordx4 v[214:215], off
	v_lshl_add_u64 v[214:215], v[218:219], 0, s[42:43]
	s_mov_b32 m0, s40
	s_nop 0
	global_load_lds_dwordx4 v[214:215], off
	v_lshl_add_u64 v[214:215], v[220:221], 0, s[42:43]
	s_mov_b32 m0, s41
	s_nop 0
	global_load_lds_dwordx4 v[214:215], off
	s_waitcnt vmcnt(8)
	s_waitcnt lgkmcnt(0)
	s_barrier
	s_waitcnt lgkmcnt(0)
	v_mfma_f32_16x16x32_bf16 v[64:67], v[150:153], v[182:185], v[64:67]
	v_mfma_f32_16x16x32_bf16 v[60:63], v[158:161], v[182:185], v[60:63]
	v_mfma_f32_16x16x32_bf16 v[48:51], v[150:153], v[190:193], v[48:51]
	v_mfma_f32_16x16x32_bf16 v[44:47], v[158:161], v[190:193], v[44:47]
	v_mfma_f32_16x16x32_bf16 v[32:35], v[150:153], v[198:201], v[32:35]
	v_mfma_f32_16x16x32_bf16 v[28:31], v[158:161], v[198:201], v[28:31]
	v_mfma_f32_16x16x32_bf16 v[16:19], v[150:153], v[206:209], v[16:19]
	v_mfma_f32_16x16x32_bf16 v[12:15], v[158:161], v[206:209], v[12:15]
	v_mfma_f32_16x16x32_bf16 v[64:67], v[154:157], v[186:189], v[64:67]
	v_mfma_f32_16x16x32_bf16 v[60:63], v[162:165], v[186:189], v[60:63]
	v_mfma_f32_16x16x32_bf16 v[48:51], v[154:157], v[194:197], v[48:51]
	v_mfma_f32_16x16x32_bf16 v[44:47], v[162:165], v[194:197], v[44:47]
	v_mfma_f32_16x16x32_bf16 v[32:35], v[154:157], v[202:205], v[32:35]
	v_mfma_f32_16x16x32_bf16 v[28:31], v[162:165], v[202:205], v[28:31]
	v_mfma_f32_16x16x32_bf16 v[16:19], v[154:157], v[210:213], v[16:19]
	v_mfma_f32_16x16x32_bf16 v[12:15], v[162:165], v[210:213], v[12:15]
	v_mfma_f32_16x16x32_bf16 v[56:59], v[166:169], v[182:185], v[56:59]
	v_mfma_f32_16x16x32_bf16 v[52:55], v[174:177], v[182:185], v[52:55]
	v_mfma_f32_16x16x32_bf16 v[40:43], v[166:169], v[190:193], v[40:43]
	v_mfma_f32_16x16x32_bf16 v[36:39], v[174:177], v[190:193], v[36:39]
	v_mfma_f32_16x16x32_bf16 v[24:27], v[166:169], v[198:201], v[24:27]
	v_mfma_f32_16x16x32_bf16 v[20:23], v[174:177], v[198:201], v[20:23]
	v_mfma_f32_16x16x32_bf16 v[8:11], v[166:169], v[206:209], v[8:11]
	v_mfma_f32_16x16x32_bf16 v[4:7], v[174:177], v[206:209], v[4:7]
	v_mfma_f32_16x16x32_bf16 v[56:59], v[170:173], v[186:189], v[56:59]
	v_mfma_f32_16x16x32_bf16 v[52:55], v[178:181], v[186:189], v[52:55]
	v_mfma_f32_16x16x32_bf16 v[40:43], v[170:173], v[194:197], v[40:43]
	v_mfma_f32_16x16x32_bf16 v[36:39], v[178:181], v[194:197], v[36:39]
	v_mfma_f32_16x16x32_bf16 v[24:27], v[170:173], v[202:205], v[24:27]
	v_mfma_f32_16x16x32_bf16 v[20:23], v[178:181], v[202:205], v[20:23]
	v_mfma_f32_16x16x32_bf16 v[8:11], v[170:173], v[210:213], v[8:11]
	v_mfma_f32_16x16x32_bf16 v[4:7], v[178:181], v[210:213], v[4:7]
	s_barrier
	s_add_i32 s62, s62, 2
	s_add_u32 s0, s0, 0x100
	s_addc_u32 s1, s1, 0
	s_cmp_gt_u32 s62, 41
	s_cbranch_scc0 .LBB0_1780
	s_add_u32 s0, s60, 0xffffff00
	s_addc_u32 s1, s61, -1
	s_and_b64 vcc, exec, s[4:5]
	s_cbranch_vccnz .LBB0_1783
	v_mov_b32_e32 v4, 0
	s_mov_b32 s16, s58
	s_mov_b32 s23, s57
	s_mov_b64 s[6:7], s[14:15]
	s_mov_b32 s56, s59
	v_mov_b32_e32 v5, v4
	v_mov_b32_e32 v6, v4
	v_mov_b32_e32 v7, v4
	v_mov_b32_e32 v8, v4
	v_mov_b32_e32 v9, v4
	v_mov_b32_e32 v10, v4
	v_mov_b32_e32 v11, v4
	v_mov_b32_e32 v20, v4
	v_mov_b32_e32 v21, v4
	v_mov_b32_e32 v22, v4
	v_mov_b32_e32 v23, v4
	v_mov_b32_e32 v24, v4
	v_mov_b32_e32 v25, v4
	v_mov_b32_e32 v26, v4
	v_mov_b32_e32 v27, v4
	v_mov_b32_e32 v36, v4
	v_mov_b32_e32 v37, v4
	v_mov_b32_e32 v38, v4
	v_mov_b32_e32 v39, v4
	v_mov_b32_e32 v40, v4
	v_mov_b32_e32 v41, v4
	v_mov_b32_e32 v42, v4
	v_mov_b32_e32 v43, v4
	v_mov_b32_e32 v52, v4
	v_mov_b32_e32 v53, v4
	v_mov_b32_e32 v54, v4
	v_mov_b32_e32 v55, v4
	v_mov_b32_e32 v56, v4
	v_mov_b32_e32 v57, v4
	v_mov_b32_e32 v58, v4
	v_mov_b32_e32 v59, v4
	v_mov_b32_e32 v12, v4
	v_mov_b32_e32 v13, v4
	v_mov_b32_e32 v14, v4
	v_mov_b32_e32 v15, v4
	v_mov_b32_e32 v16, v4
	v_mov_b32_e32 v17, v4
	v_mov_b32_e32 v18, v4
	v_mov_b32_e32 v19, v4
	v_mov_b32_e32 v28, v4
	v_mov_b32_e32 v29, v4
	v_mov_b32_e32 v30, v4
	v_mov_b32_e32 v31, v4
	v_mov_b32_e32 v32, v4
	v_mov_b32_e32 v33, v4
	v_mov_b32_e32 v34, v4
	v_mov_b32_e32 v35, v4
	v_mov_b32_e32 v44, v4
	v_mov_b32_e32 v45, v4
	v_mov_b32_e32 v46, v4
	v_mov_b32_e32 v47, v4
	v_mov_b32_e32 v48, v4
	v_mov_b32_e32 v49, v4
	v_mov_b32_e32 v50, v4
	v_mov_b32_e32 v51, v4
	v_mov_b32_e32 v60, v4
	v_mov_b32_e32 v61, v4
	v_mov_b32_e32 v62, v4
	v_mov_b32_e32 v63, v4
	v_mov_b32_e32 v64, v4
	v_mov_b32_e32 v65, v4
	v_mov_b32_e32 v66, v4
	v_mov_b32_e32 v67, v4
	v_mov_b32_e32 v68, v4
	v_mov_b32_e32 v69, v4
	v_mov_b32_e32 v70, v4
	v_mov_b32_e32 v71, v4
	v_mov_b32_e32 v72, v4
	v_mov_b32_e32 v73, v4
	v_mov_b32_e32 v74, v4
	v_mov_b32_e32 v75, v4
	v_mov_b32_e32 v84, v4
	v_mov_b32_e32 v85, v4
	v_mov_b32_e32 v86, v4
	v_mov_b32_e32 v87, v4
	v_mov_b32_e32 v88, v4
	v_mov_b32_e32 v89, v4
	v_mov_b32_e32 v90, v4
	v_mov_b32_e32 v91, v4
	v_mov_b32_e32 v100, v4
	v_mov_b32_e32 v101, v4
	v_mov_b32_e32 v102, v4
	v_mov_b32_e32 v103, v4
	v_mov_b32_e32 v104, v4
	v_mov_b32_e32 v105, v4
	v_mov_b32_e32 v106, v4
	v_mov_b32_e32 v107, v4
	v_mov_b32_e32 v116, v4
	v_mov_b32_e32 v117, v4
	v_mov_b32_e32 v118, v4
	v_mov_b32_e32 v119, v4
	v_mov_b32_e32 v120, v4
	v_mov_b32_e32 v121, v4
	v_mov_b32_e32 v122, v4
	v_mov_b32_e32 v123, v4
	v_mov_b32_e32 v76, v4
	v_mov_b32_e32 v77, v4
	v_mov_b32_e32 v78, v4
	v_mov_b32_e32 v79, v4
	v_mov_b32_e32 v80, v4
	v_mov_b32_e32 v81, v4
	v_mov_b32_e32 v82, v4
	v_mov_b32_e32 v83, v4
	v_mov_b32_e32 v92, v4
	v_mov_b32_e32 v93, v4
	v_mov_b32_e32 v94, v4
	v_mov_b32_e32 v95, v4
	v_mov_b32_e32 v96, v4
	v_mov_b32_e32 v97, v4
	v_mov_b32_e32 v98, v4
	v_mov_b32_e32 v99, v4
	v_mov_b32_e32 v108, v4
	v_mov_b32_e32 v109, v4
	v_mov_b32_e32 v110, v4
	v_mov_b32_e32 v111, v4
	v_mov_b32_e32 v112, v4
	v_mov_b32_e32 v113, v4
	v_mov_b32_e32 v114, v4
	v_mov_b32_e32 v115, v4
	v_mov_b32_e32 v124, v4
	v_mov_b32_e32 v125, v4
	v_mov_b32_e32 v126, v4
	v_mov_b32_e32 v127, v4
	v_mov_b32_e32 v128, v4
	v_mov_b32_e32 v129, v4
	v_mov_b32_e32 v130, v4
	v_mov_b32_e32 v131, v4
	s_andn2_b64 vcc, exec, s[8:9]
	s_cbranch_vccnz .LBB0_1784
	s_branch .LBB0_1785

; #define GAS __attribute__((address_space(1)))
; __device__ __forceinline__ unsigned xb_add(unsigned* p, unsigned v) { return __hip_atomic_fetch_add(p, v, __ATOMIC_RELAXED, __HIP_MEMORY_SCOPE_AGENT); }
; #define SEAM_LOCAL(k) do { if (IN(k) && IN((k) + 1)) { TBAR0(); xcd_barrier(bar, true, true); TBAR1(); } } while (0)
; __device__ __forceinline__ void xcd_barrier(const XcdBarrier& b, const bool group_local = false, const bool xcc_only = false) {
;     asm volatile("s_waitcnt vmcnt(0)" ::: "memory");
;     __syncthreads();
;     if (threadIdx.x == 0) {
;         GAS unsigned* barg = (GAS unsigned*)b.bar; asm volatile("" : "+s"(barg)); unsigned* bar = (unsigned*)barg;
;         __builtin_amdgcn_s_waitcnt(0);
;         unsigned nloc = b.st[0], nx = b.st[1];
;         if (nloc == 0u) { xcd_barrier_complete(bar, b.x, nloc, nx); b.st[0] = nloc; b.st[1] = nx; }
;         const unsigned old = xb_add(&bar[XB_XSUB(b.x)], 1u);
; __global__ void __launch_bounds__(NWAVES * 64, 2) mk_fwd(Args args) {
;     ...
;             SEAM_LOCAL(pb + 5);
.LBB0_1920:
	s_waitcnt vmcnt(0)
	s_waitcnt vmcnt(0) lgkmcnt(0)
	s_barrier
	s_setprio 0
	s_mov_b64 s[14:15], exec
	v_readlane_b32 s0, v255, 43
	v_readlane_b32 s1, v255, 44
	s_and_b64 s[0:1], s[14:15], s[0:1]
	s_mov_b64 exec, s[0:1]
	s_cbranch_execnz .LBB0_1921
	s_getpc_b64 s[98:99]
